# baseline (speedup 1.0000x reference)
.LBB0_15:
.LBB0_16:
	s_setprio 2
	s_mov_b32 s27, s19
	v_mov_b32_e32 v1, 0x42c80000
	v_mov_b32_e32 v0, 0
	s_add_i32 s4, s34, -2
	s_max_i32 s4, s4, 0
	s_mul_i32 s5, s4, 0x804
	s_add_i32 s5, s5, s35
	s_add_i32 s6, s5, 0x0
	s_add_i32 s7, s5, 0x101004
	s_add_i32 s8, s5, 0x202008
	s_add_i32 s11, s5, 0x30300c
	s_add_i32 s15, s5, 0x404010
	s_mul_i32 s9, s4, 0x180c
	s_add_i32 s9, s9, s33
	buffer_load_dword v2, v28, s[16:19], s6 offen nt
	buffer_load_dword v3, v28, s[16:19], s7 offen nt
	buffer_load_dword v4, v28, s[16:19], s8 offen nt
	buffer_load_dword v5, v28, s[16:19], s11 offen nt
	buffer_load_dword v6, v28, s[16:19], s15 offen nt
	buffer_load_dwordx3 v[8:10], v27, s[24:27], s9 offen nt
	s_add_i32 s4, s34, -1
	s_max_i32 s4, s4, 0
	s_mul_i32 s5, s4, 0x804
	s_add_i32 s5, s5, s35
	s_add_i32 s6, s5, 0x0
	s_add_i32 s7, s5, 0x101004
	s_add_i32 s8, s5, 0x202008
	s_add_i32 s11, s5, 0x30300c
	s_add_i32 s15, s5, 0x404010
	s_mul_i32 s9, s4, 0x180c
	s_add_i32 s9, s9, s33
	buffer_load_dword v12, v28, s[16:19], s6 offen nt
	buffer_load_dword v13, v28, s[16:19], s7 offen nt
	buffer_load_dword v14, v28, s[16:19], s8 offen nt
	buffer_load_dword v15, v28, s[16:19], s11 offen nt
	buffer_load_dword v16, v28, s[16:19], s15 offen nt
	buffer_load_dwordx3 v[32:34], v27, s[24:27], s9 offen nt
	s_add_i32 s4, s34, 0
	s_min_i32 s4, s4, 0x200
	s_mul_i32 s5, s4, 0x804
	s_add_i32 s5, s5, s35
	s_add_i32 s6, s5, 0x0
	s_add_i32 s7, s5, 0x101004
	s_add_i32 s8, s5, 0x202008
	s_add_i32 s11, s5, 0x30300c
	s_add_i32 s15, s5, 0x404010
	s_mul_i32 s9, s4, 0x180c
	s_add_i32 s9, s9, s33
	buffer_load_dword v20, v28, s[16:19], s6 offen nt
	buffer_load_dword v21, v28, s[16:19], s7 offen nt
	buffer_load_dword v24, v28, s[16:19], s8 offen nt
	buffer_load_dword v25, v28, s[16:19], s11 offen nt
	buffer_load_dword v30, v28, s[16:19], s15 offen nt
	buffer_load_dwordx3 v[36:38], v27, s[24:27], s9 offen nt
	s_waitcnt vmcnt(12)
	v_mov_b32_dpp v40, v8 wave_shr:1 row_mask:0xf bank_mask:0xf bound_ctrl:1
	v_mov_b32_dpp v41, v9 wave_shr:1 row_mask:0xf bank_mask:0xf bound_ctrl:1
	v_mov_b32_dpp v42, v10 wave_shr:1 row_mask:0xf bank_mask:0xf bound_ctrl:1
	v_mov_b32_dpp v44, v8 wave_shl:1 row_mask:0xf bank_mask:0xf bound_ctrl:1
	v_mov_b32_dpp v45, v9 wave_shl:1 row_mask:0xf bank_mask:0xf bound_ctrl:1
	v_mov_b32_dpp v46, v10 wave_shl:1 row_mask:0xf bank_mask:0xf bound_ctrl:1
	v_mov_b32_dpp v48, v2 wave_shr:1 row_mask:0xf bank_mask:0xf bound_ctrl:1
	v_mov_b32_dpp v49, v3 wave_shr:1 row_mask:0xf bank_mask:0xf bound_ctrl:1
	v_mov_b32_dpp v50, v4 wave_shr:1 row_mask:0xf bank_mask:0xf bound_ctrl:1
	v_mov_b32_dpp v51, v5 wave_shr:1 row_mask:0xf bank_mask:0xf bound_ctrl:1
	v_mov_b32_dpp v52, v6 wave_shr:1 row_mask:0xf bank_mask:0xf bound_ctrl:1
	v_mov_b32_dpp v54, v2 wave_shl:1 row_mask:0xf bank_mask:0xf bound_ctrl:1
	v_mov_b32_dpp v55, v3 wave_shl:1 row_mask:0xf bank_mask:0xf bound_ctrl:1
	v_mov_b32_dpp v56, v4 wave_shl:1 row_mask:0xf bank_mask:0xf bound_ctrl:1
	v_mov_b32_dpp v57, v5 wave_shl:1 row_mask:0xf bank_mask:0xf bound_ctrl:1
	v_mov_b32_dpp v58, v6 wave_shl:1 row_mask:0xf bank_mask:0xf bound_ctrl:1
	v_pk_mul_f32 v[60:61], v[2:3], v[8:9] op_sel_hi:[1,0]
	v_pk_mul_f32 v[62:63], v[4:5], v[8:9] op_sel_hi:[1,0]
	v_mul_f32_e64 v64, v6, v8
	v_pk_mul_f32 v[66:67], v[2:3], v[8:9] op_sel:[0,1]
	v_pk_mul_f32 v[68:69], v[4:5], v[8:9] op_sel:[0,1]
	v_mul_f32_e64 v70, v6, v9
	v_pk_mul_f32 v[72:73], v[2:3], v[10:11] op_sel_hi:[1,0]
	v_pk_mul_f32 v[74:75], v[4:5], v[10:11] op_sel_hi:[1,0]
	v_mul_f32_e64 v76, v6, v10
	v_pk_add_f32 v[78:79], v[2:3], v[48:49]
	v_pk_add_f32 v[80:81], v[4:5], v[50:51]
	v_add_f32_e64 v82, v6, v52
	v_pk_fma_f32 v[60:61], v[48:49], v[40:41], v[60:61] op_sel_hi:[1,0,1]
	v_pk_fma_f32 v[62:63], v[50:51], v[40:41], v[62:63] op_sel_hi:[1,0,1]
	v_fma_f32 v64, v52, v40, v64
	v_pk_fma_f32 v[66:67], v[48:49], v[40:41], v[66:67] op_sel:[0,1,0]
	v_pk_fma_f32 v[68:69], v[50:51], v[40:41], v[68:69] op_sel:[0,1,0]
	v_fma_f32 v70, v52, v41, v70
	v_pk_fma_f32 v[72:73], v[48:49], v[42:43], v[72:73] op_sel_hi:[1,0,1]
	v_pk_fma_f32 v[74:75], v[50:51], v[42:43], v[74:75] op_sel_hi:[1,0,1]
	v_fma_f32 v76, v52, v42, v76
	v_pk_add_f32 v[78:79], v[78:79], v[54:55]
	v_pk_add_f32 v[80:81], v[80:81], v[56:57]
	v_add_f32_e64 v82, v82, v58
	v_pk_fma_f32 v[60:61], v[54:55], v[44:45], v[60:61] op_sel_hi:[1,0,1]
	v_pk_fma_f32 v[62:63], v[56:57], v[44:45], v[62:63] op_sel_hi:[1,0,1]
	v_fma_f32 v64, v58, v44, v64
	v_pk_fma_f32 v[66:67], v[54:55], v[44:45], v[66:67] op_sel:[0,1,0]
	v_pk_fma_f32 v[68:69], v[56:57], v[44:45], v[68:69] op_sel:[0,1,0]
	v_fma_f32 v70, v58, v45, v70
	v_pk_fma_f32 v[72:73], v[54:55], v[46:47], v[72:73] op_sel_hi:[1,0,1]
	v_pk_fma_f32 v[74:75], v[56:57], v[46:47], v[74:75] op_sel_hi:[1,0,1]
	v_fma_f32 v76, v58, v46, v76
	s_barrier
	s_add_i32 s4, s34, 1
	s_min_i32 s4, s4, 0x200
	s_mul_i32 s5, s4, 0x804
	s_add_i32 s5, s5, s35
	s_add_i32 s6, s5, 0x0
	s_add_i32 s7, s5, 0x101004
	s_add_i32 s8, s5, 0x202008
	s_add_i32 s11, s5, 0x30300c
	s_add_i32 s15, s5, 0x404010
	s_mul_i32 s9, s4, 0x180c
	s_add_i32 s9, s9, s33
	buffer_load_dword v48, v28, s[16:19], s6 offen nt
	buffer_load_dword v49, v28, s[16:19], s7 offen nt
	buffer_load_dword v50, v28, s[16:19], s8 offen nt
	buffer_load_dword v51, v28, s[16:19], s11 offen nt
	buffer_load_dword v52, v28, s[16:19], s15 offen nt
	buffer_load_dwordx3 v[56:58], v27, s[24:27], s9 offen nt
	s_waitcnt vmcnt(12)
	v_mov_b32_dpp v84, v32 wave_shr:1 row_mask:0xf bank_mask:0xf bound_ctrl:1
	v_mov_b32_dpp v85, v33 wave_shr:1 row_mask:0xf bank_mask:0xf bound_ctrl:1
	v_mov_b32_dpp v86, v34 wave_shr:1 row_mask:0xf bank_mask:0xf bound_ctrl:1
	v_mov_b32_dpp v88, v32 wave_shl:1 row_mask:0xf bank_mask:0xf bound_ctrl:1
	v_mov_b32_dpp v89, v33 wave_shl:1 row_mask:0xf bank_mask:0xf bound_ctrl:1
	v_mov_b32_dpp v90, v34 wave_shl:1 row_mask:0xf bank_mask:0xf bound_ctrl:1
	v_mov_b32_dpp v54, v12 wave_shr:1 row_mask:0xf bank_mask:0xf bound_ctrl:1
	v_mov_b32_dpp v55, v13 wave_shr:1 row_mask:0xf bank_mask:0xf bound_ctrl:1
	v_mov_b32_dpp v92, v14 wave_shr:1 row_mask:0xf bank_mask:0xf bound_ctrl:1
	v_mov_b32_dpp v93, v15 wave_shr:1 row_mask:0xf bank_mask:0xf bound_ctrl:1
	v_mov_b32_dpp v94, v16 wave_shr:1 row_mask:0xf bank_mask:0xf bound_ctrl:1
	v_mov_b32_dpp v96, v12 wave_shl:1 row_mask:0xf bank_mask:0xf bound_ctrl:1
	v_mov_b32_dpp v97, v13 wave_shl:1 row_mask:0xf bank_mask:0xf bound_ctrl:1
	v_mov_b32_dpp v98, v14 wave_shl:1 row_mask:0xf bank_mask:0xf bound_ctrl:1
	v_mov_b32_dpp v99, v15 wave_shl:1 row_mask:0xf bank_mask:0xf bound_ctrl:1
	v_mov_b32_dpp v100, v16 wave_shl:1 row_mask:0xf bank_mask:0xf bound_ctrl:1
	v_pk_mul_f32 v[102:103], v[12:13], v[32:33] op_sel_hi:[1,0]
	v_pk_mul_f32 v[104:105], v[14:15], v[32:33] op_sel_hi:[1,0]
	v_mul_f32_e64 v106, v16, v32
	v_pk_mul_f32 v[108:109], v[12:13], v[32:33] op_sel:[0,1]
	v_pk_mul_f32 v[110:111], v[14:15], v[32:33] op_sel:[0,1]
	v_mul_f32_e64 v112, v16, v33
	v_pk_mul_f32 v[114:115], v[12:13], v[34:35] op_sel_hi:[1,0]
	v_pk_mul_f32 v[116:117], v[14:15], v[34:35] op_sel_hi:[1,0]
	v_mul_f32_e64 v118, v16, v34
	v_pk_add_f32 v[120:121], v[12:13], v[54:55]
	v_pk_add_f32 v[122:123], v[14:15], v[92:93]
	v_add_f32_e64 v124, v16, v94
	v_pk_fma_f32 v[102:103], v[54:55], v[84:85], v[102:103] op_sel_hi:[1,0,1]
	v_pk_fma_f32 v[104:105], v[92:93], v[84:85], v[104:105] op_sel_hi:[1,0,1]
	v_fma_f32 v106, v94, v84, v106
	v_pk_fma_f32 v[108:109], v[54:55], v[84:85], v[108:109] op_sel:[0,1,0]
	v_pk_fma_f32 v[110:111], v[92:93], v[84:85], v[110:111] op_sel:[0,1,0]
	v_fma_f32 v112, v94, v85, v112
	v_pk_fma_f32 v[114:115], v[54:55], v[86:87], v[114:115] op_sel_hi:[1,0,1]
	v_pk_fma_f32 v[116:117], v[92:93], v[86:87], v[116:117] op_sel_hi:[1,0,1]
	v_fma_f32 v118, v94, v86, v118
	v_pk_add_f32 v[120:121], v[120:121], v[96:97]
	v_pk_add_f32 v[122:123], v[122:123], v[98:99]
	v_add_f32_e64 v124, v124, v100
	v_pk_fma_f32 v[102:103], v[96:97], v[88:89], v[102:103] op_sel_hi:[1,0,1]
	v_pk_fma_f32 v[104:105], v[98:99], v[88:89], v[104:105] op_sel_hi:[1,0,1]
	v_fma_f32 v106, v100, v88, v106
	v_pk_fma_f32 v[108:109], v[96:97], v[88:89], v[108:109] op_sel:[0,1,0]
	v_pk_fma_f32 v[110:111], v[98:99], v[88:89], v[110:111] op_sel:[0,1,0]
	v_fma_f32 v112, v100, v89, v112
	v_pk_fma_f32 v[114:115], v[96:97], v[90:91], v[114:115] op_sel_hi:[1,0,1]
	v_pk_fma_f32 v[116:117], v[98:99], v[90:91], v[116:117] op_sel_hi:[1,0,1]
	v_fma_f32 v118, v100, v90, v118
	s_barrier
	s_add_i32 s4, s34, 2
	s_min_i32 s4, s4, 0x200
	s_mul_i32 s5, s4, 0x804
	s_add_i32 s5, s5, s35
	s_add_i32 s6, s5, 0x0
	s_add_i32 s7, s5, 0x101004
	s_add_i32 s8, s5, 0x202008
	s_add_i32 s11, s5, 0x30300c
	s_add_i32 s15, s5, 0x404010
	s_mul_i32 s9, s4, 0x180c
	s_add_i32 s9, s9, s33
	buffer_load_dword v54, v28, s[16:19], s6 offen nt
	buffer_load_dword v55, v28, s[16:19], s7 offen nt
	buffer_load_dword v92, v28, s[16:19], s8 offen nt
	buffer_load_dword v93, v28, s[16:19], s11 offen nt
	buffer_load_dword v94, v28, s[16:19], s15 offen nt
	buffer_load_dwordx3 v[96:98], v27, s[24:27], s9 offen nt
	s_waitcnt vmcnt(12)
	v_mov_b32_dpp v128, v36 wave_shr:1 row_mask:0xf bank_mask:0xf bound_ctrl:1
	v_mov_b32_dpp v129, v37 wave_shr:1 row_mask:0xf bank_mask:0xf bound_ctrl:1
	v_mov_b32_dpp v130, v38 wave_shr:1 row_mask:0xf bank_mask:0xf bound_ctrl:1
	v_mov_b32_dpp v132, v36 wave_shl:1 row_mask:0xf bank_mask:0xf bound_ctrl:1
	v_mov_b32_dpp v133, v37 wave_shl:1 row_mask:0xf bank_mask:0xf bound_ctrl:1
	v_mov_b32_dpp v134, v38 wave_shl:1 row_mask:0xf bank_mask:0xf bound_ctrl:1
	v_mov_b32_dpp v100, v20 wave_shr:1 row_mask:0xf bank_mask:0xf bound_ctrl:1
	v_mov_b32_dpp v101, v21 wave_shr:1 row_mask:0xf bank_mask:0xf bound_ctrl:1
	v_mov_b32_dpp v126, v24 wave_shr:1 row_mask:0xf bank_mask:0xf bound_ctrl:1
	v_mov_b32_dpp v127, v25 wave_shr:1 row_mask:0xf bank_mask:0xf bound_ctrl:1
	v_mov_b32_dpp v136, v30 wave_shr:1 row_mask:0xf bank_mask:0xf bound_ctrl:1
	v_mov_b32_dpp v138, v20 wave_shl:1 row_mask:0xf bank_mask:0xf bound_ctrl:1
	v_mov_b32_dpp v139, v21 wave_shl:1 row_mask:0xf bank_mask:0xf bound_ctrl:1
	v_mov_b32_dpp v140, v24 wave_shl:1 row_mask:0xf bank_mask:0xf bound_ctrl:1
	v_mov_b32_dpp v141, v25 wave_shl:1 row_mask:0xf bank_mask:0xf bound_ctrl:1
	v_mov_b32_dpp v142, v30 wave_shl:1 row_mask:0xf bank_mask:0xf bound_ctrl:1
	v_pk_mul_f32 v[144:145], v[20:21], v[36:37] op_sel_hi:[1,0]
	v_pk_mul_f32 v[146:147], v[24:25], v[36:37] op_sel_hi:[1,0]
	v_mul_f32_e64 v148, v30, v36
	v_pk_mul_f32 v[150:151], v[20:21], v[36:37] op_sel:[0,1]
	v_pk_mul_f32 v[152:153], v[24:25], v[36:37] op_sel:[0,1]
	v_mul_f32_e64 v154, v30, v37
	v_pk_mul_f32 v[156:157], v[20:21], v[38:39] op_sel_hi:[1,0]
	v_pk_mul_f32 v[158:159], v[24:25], v[38:39] op_sel_hi:[1,0]
	v_mul_f32_e64 v160, v30, v38
	v_pk_add_f32 v[162:163], v[20:21], v[100:101]
	v_pk_add_f32 v[164:165], v[24:25], v[126:127]
	v_add_f32_e64 v166, v30, v136
	v_pk_fma_f32 v[144:145], v[100:101], v[128:129], v[144:145] op_sel_hi:[1,0,1]
	v_pk_fma_f32 v[146:147], v[126:127], v[128:129], v[146:147] op_sel_hi:[1,0,1]
	v_fma_f32 v148, v136, v128, v148
	v_pk_fma_f32 v[150:151], v[100:101], v[128:129], v[150:151] op_sel:[0,1,0]
	v_pk_fma_f32 v[152:153], v[126:127], v[128:129], v[152:153] op_sel:[0,1,0]
	v_fma_f32 v154, v136, v129, v154
	v_pk_fma_f32 v[156:157], v[100:101], v[130:131], v[156:157] op_sel_hi:[1,0,1]
	v_pk_fma_f32 v[158:159], v[126:127], v[130:131], v[158:159] op_sel_hi:[1,0,1]
	v_fma_f32 v160, v136, v130, v160
	v_pk_add_f32 v[162:163], v[162:163], v[138:139]
	v_pk_add_f32 v[164:165], v[164:165], v[140:141]
	v_add_f32_e64 v166, v166, v142
	v_pk_fma_f32 v[144:145], v[138:139], v[132:133], v[144:145] op_sel_hi:[1,0,1]
	v_pk_fma_f32 v[146:147], v[140:141], v[132:133], v[146:147] op_sel_hi:[1,0,1]
	v_fma_f32 v148, v142, v132, v148
	v_pk_fma_f32 v[150:151], v[138:139], v[132:133], v[150:151] op_sel:[0,1,0]
	v_pk_fma_f32 v[152:153], v[140:141], v[132:133], v[152:153] op_sel:[0,1,0]
	v_fma_f32 v154, v142, v133, v154
	v_pk_fma_f32 v[156:157], v[138:139], v[134:135], v[156:157] op_sel_hi:[1,0,1]
	v_pk_fma_f32 v[158:159], v[140:141], v[134:135], v[158:159] op_sel_hi:[1,0,1]
	v_fma_f32 v160, v142, v134, v160
	s_barrier
	ds_read_b128 v[136:139], v23 offset:0
	ds_read_b128 v[140:143], v23 offset:1024
	ds_read_b128 v[168:171], v23 offset:2048
	v_pk_add_f32 v[100:101], v[120:121], v[162:163]
	v_pk_add_f32 v[126:127], v[78:79], v[100:101]
	v_pk_add_f32 v[78:79], v[122:123], v[164:165]
	v_pk_add_f32 v[120:121], v[80:81], v[78:79]
	v_add_f32_e64 v80, v124, v166
	v_add_f32_e64 v122, v82, v80
	v_pk_add_f32 v[82:83], v[102:103], v[144:145]
	v_pk_add_f32 v[124:125], v[60:61], v[82:83]
	v_pk_add_f32 v[60:61], v[104:105], v[146:147]
	v_pk_add_f32 v[102:103], v[62:63], v[60:61]
	v_add_f32_e64 v62, v106, v148
	v_add_f32_e64 v104, v64, v62
	v_pk_add_f32 v[64:65], v[108:109], v[150:151]
	v_pk_add_f32 v[106:107], v[66:67], v[64:65]
	v_pk_add_f32 v[66:67], v[110:111], v[152:153]
	v_pk_add_f32 v[108:109], v[68:69], v[66:67]
	v_add_f32_e64 v68, v112, v154
	v_add_f32_e64 v110, v70, v68
	v_pk_add_f32 v[70:71], v[114:115], v[156:157]
	v_pk_add_f32 v[112:113], v[72:73], v[70:71]
	v_pk_add_f32 v[72:73], v[116:117], v[158:159]
	v_pk_add_f32 v[114:115], v[74:75], v[72:73]
	v_add_f32_e64 v74, v118, v160
	v_add_f32_e64 v116, v76, v74
	s_waitcnt lgkmcnt(2)
	v_pk_fma_f32 v[124:125], v[136:137], v[126:127], v[124:125] op_sel_hi:[0,1,1] neg_lo:[1,0,0] neg_hi:[1,0,0]
	v_pk_fma_f32 v[102:103], v[136:137], v[120:121], v[102:103] op_sel_hi:[0,1,1] neg_lo:[1,0,0] neg_hi:[1,0,0]
	v_fma_f32 v104, -v136, v122, v104
	v_pk_fma_f32 v[106:107], v[136:137], v[126:127], v[106:107] op_sel:[1,0,0] neg_lo:[1,0,0] neg_hi:[1,0,0]
	v_pk_fma_f32 v[108:109], v[136:137], v[120:121], v[108:109] op_sel:[1,0,0] neg_lo:[1,0,0] neg_hi:[1,0,0]
	v_fma_f32 v110, -v137, v122, v110
	v_pk_fma_f32 v[112:113], v[138:139], v[126:127], v[112:113] op_sel_hi:[0,1,1] neg_lo:[1,0,0] neg_hi:[1,0,0]
	v_pk_fma_f32 v[114:115], v[138:139], v[120:121], v[114:115] op_sel_hi:[0,1,1] neg_lo:[1,0,0] neg_hi:[1,0,0]
	v_fma_f32 v116, -v138, v122, v116
	v_pk_mul_f32 v[76:77], v[138:139], v[124:125] op_sel:[1,0]
	v_pk_mul_f32 v[174:175], v[138:139], v[102:103] op_sel:[1,0]
	v_mul_f32_e64 v180, v139, v104
	s_waitcnt lgkmcnt(1)
	v_pk_mul_f32 v[118:119], v[140:141], v[124:125] op_sel_hi:[0,1]
	v_pk_mul_f32 v[176:177], v[140:141], v[102:103] op_sel_hi:[0,1]
	v_mul_f32_e64 v182, v140, v104
	v_pk_mul_f32 v[172:173], v[140:141], v[124:125] op_sel:[1,0]
	v_pk_mul_f32 v[178:179], v[140:141], v[102:103] op_sel:[1,0]
	v_mul_f32_e64 v184, v141, v104
	v_pk_fma_f32 v[76:77], v[140:141], v[106:107], v[76:77] op_sel_hi:[0,1,1]
	v_pk_fma_f32 v[174:175], v[140:141], v[108:109], v[174:175] op_sel_hi:[0,1,1]
	v_fma_f32 v180, v140, v110, v180
	v_pk_fma_f32 v[118:119], v[142:143], v[106:107], v[118:119] op_sel_hi:[0,1,1]
	v_pk_fma_f32 v[176:177], v[142:143], v[108:109], v[176:177] op_sel_hi:[0,1,1]
	v_fma_f32 v182, v142, v110, v182
	v_pk_fma_f32 v[172:173], v[142:143], v[106:107], v[172:173] op_sel:[1,0,0]
	v_pk_fma_f32 v[178:179], v[142:143], v[108:109], v[178:179] op_sel:[1,0,0]
	v_fma_f32 v184, v143, v110, v184
	v_pk_fma_f32 v[76:77], v[140:141], v[112:113], v[76:77] op_sel:[1,0,0]
	v_pk_fma_f32 v[174:175], v[140:141], v[114:115], v[174:175] op_sel:[1,0,0]
	v_fma_f32 v180, v141, v116, v180
	v_pk_fma_f32 v[118:119], v[142:143], v[112:113], v[118:119] op_sel:[1,0,0]
	v_pk_fma_f32 v[176:177], v[142:143], v[114:115], v[176:177] op_sel:[1,0,0]
	v_fma_f32 v182, v143, v116, v182
	s_waitcnt lgkmcnt(0)
	v_pk_fma_f32 v[172:173], v[168:169], v[112:113], v[172:173] op_sel_hi:[0,1,1]
	v_pk_fma_f32 v[178:179], v[168:169], v[114:115], v[178:179] op_sel_hi:[0,1,1]
	v_fma_f32 v184, v168, v116, v184
	v_pk_mul_f32 v[186:187], v[136:137], v[76:77] op_sel_hi:[0,1]
	v_pk_mul_f32 v[188:189], v[136:137], v[174:175] op_sel_hi:[0,1]
	v_mul_f32_e64 v190, v136, v180
	v_pk_fma_f32 v[186:187], v[136:137], v[118:119], v[186:187] op_sel:[1,0,0]
	v_pk_fma_f32 v[188:189], v[136:137], v[176:177], v[188:189] op_sel:[1,0,0]
	v_fma_f32 v190, v137, v182, v190
	v_pk_fma_f32 v[186:187], v[138:139], v[172:173], v[186:187] op_sel_hi:[0,1,1]
	v_pk_fma_f32 v[188:189], v[138:139], v[178:179], v[188:189] op_sel_hi:[0,1,1]
	v_fma_f32 v190, v138, v184, v190
	v_pk_fma_f32 v[186:187], v[168:169], v[126:127], v[186:187] op_sel:[1,0,0] neg_lo:[0,0,1] neg_hi:[0,0,1]
	v_pk_fma_f32 v[188:189], v[168:169], v[120:121], v[188:189] op_sel:[1,0,0] neg_lo:[0,0,1] neg_hi:[0,0,1]
	v_fma_f32 v190, v169, v122, -v190
	s_add_i32 s4, s34, 3
	s_min_i32 s4, s4, 0x200
	s_mul_i32 s5, s4, 0x804
	s_add_i32 s5, s5, s35
	s_add_i32 s6, s5, 0x0
	s_add_i32 s7, s5, 0x101004
	s_add_i32 s8, s5, 0x202008
	s_add_i32 s11, s5, 0x30300c
	s_add_i32 s15, s5, 0x404010
	s_mul_i32 s9, s4, 0x180c
	s_add_i32 s9, s9, s33
	buffer_load_dword v2, v28, s[16:19], s6 offen nt
	buffer_load_dword v3, v28, s[16:19], s7 offen nt
	buffer_load_dword v4, v28, s[16:19], s8 offen nt
	buffer_load_dword v5, v28, s[16:19], s11 offen nt
	buffer_load_dword v6, v28, s[16:19], s15 offen nt
	buffer_load_dwordx3 v[8:10], v27, s[24:27], s9 offen nt
	s_waitcnt vmcnt(12)
	v_mov_b32_dpp v40, v56 wave_shr:1 row_mask:0xf bank_mask:0xf bound_ctrl:1
	v_mov_b32_dpp v41, v57 wave_shr:1 row_mask:0xf bank_mask:0xf bound_ctrl:1
	v_mov_b32_dpp v42, v58 wave_shr:1 row_mask:0xf bank_mask:0xf bound_ctrl:1
	v_mov_b32_dpp v44, v56 wave_shl:1 row_mask:0xf bank_mask:0xf bound_ctrl:1
	v_mov_b32_dpp v45, v57 wave_shl:1 row_mask:0xf bank_mask:0xf bound_ctrl:1
	v_mov_b32_dpp v46, v58 wave_shl:1 row_mask:0xf bank_mask:0xf bound_ctrl:1
	v_mov_b32_dpp v102, v48 wave_shr:1 row_mask:0xf bank_mask:0xf bound_ctrl:1
	v_mov_b32_dpp v103, v49 wave_shr:1 row_mask:0xf bank_mask:0xf bound_ctrl:1
	v_mov_b32_dpp v104, v50 wave_shr:1 row_mask:0xf bank_mask:0xf bound_ctrl:1
	v_mov_b32_dpp v105, v51 wave_shr:1 row_mask:0xf bank_mask:0xf bound_ctrl:1
	v_mov_b32_dpp v106, v52 wave_shr:1 row_mask:0xf bank_mask:0xf bound_ctrl:1
	v_mov_b32_dpp v108, v48 wave_shl:1 row_mask:0xf bank_mask:0xf bound_ctrl:1
	v_mov_b32_dpp v109, v49 wave_shl:1 row_mask:0xf bank_mask:0xf bound_ctrl:1
	v_mov_b32_dpp v110, v50 wave_shl:1 row_mask:0xf bank_mask:0xf bound_ctrl:1
	v_mov_b32_dpp v111, v51 wave_shl:1 row_mask:0xf bank_mask:0xf bound_ctrl:1
	v_mov_b32_dpp v112, v52 wave_shl:1 row_mask:0xf bank_mask:0xf bound_ctrl:1
	v_pk_mul_f32 v[114:115], v[48:49], v[56:57] op_sel_hi:[1,0]
	v_pk_mul_f32 v[116:117], v[50:51], v[56:57] op_sel_hi:[1,0]
	v_mul_f32_e64 v120, v52, v56
	v_pk_mul_f32 v[122:123], v[48:49], v[56:57] op_sel:[0,1]
	v_pk_mul_f32 v[124:125], v[50:51], v[56:57] op_sel:[0,1]
	v_mul_f32_e64 v126, v52, v57
	v_pk_mul_f32 v[136:137], v[48:49], v[58:59] op_sel_hi:[1,0]
	v_pk_mul_f32 v[138:139], v[50:51], v[58:59] op_sel_hi:[1,0]
	v_mul_f32_e64 v140, v52, v58
	v_pk_add_f32 v[142:143], v[48:49], v[102:103]
	v_pk_add_f32 v[168:169], v[50:51], v[104:105]
	v_add_f32_e64 v170, v52, v106
	v_pk_fma_f32 v[114:115], v[102:103], v[40:41], v[114:115] op_sel_hi:[1,0,1]
	v_pk_fma_f32 v[116:117], v[104:105], v[40:41], v[116:117] op_sel_hi:[1,0,1]
	v_fma_f32 v120, v106, v40, v120
	v_pk_fma_f32 v[122:123], v[102:103], v[40:41], v[122:123] op_sel:[0,1,0]
	v_pk_fma_f32 v[124:125], v[104:105], v[40:41], v[124:125] op_sel:[0,1,0]
	v_fma_f32 v126, v106, v41, v126
	v_pk_fma_f32 v[136:137], v[102:103], v[42:43], v[136:137] op_sel_hi:[1,0,1]
	v_pk_fma_f32 v[138:139], v[104:105], v[42:43], v[138:139] op_sel_hi:[1,0,1]
	v_fma_f32 v140, v106, v42, v140
	v_pk_add_f32 v[142:143], v[142:143], v[108:109]
	v_pk_add_f32 v[168:169], v[168:169], v[110:111]
	v_add_f32_e64 v170, v170, v112
	v_pk_fma_f32 v[114:115], v[108:109], v[44:45], v[114:115] op_sel_hi:[1,0,1]
	v_pk_fma_f32 v[116:117], v[110:111], v[44:45], v[116:117] op_sel_hi:[1,0,1]
	v_fma_f32 v120, v112, v44, v120
	v_pk_fma_f32 v[122:123], v[108:109], v[44:45], v[122:123] op_sel:[0,1,0]
	v_pk_fma_f32 v[124:125], v[110:111], v[44:45], v[124:125] op_sel:[0,1,0]
	v_fma_f32 v126, v112, v45, v126
	v_pk_fma_f32 v[136:137], v[108:109], v[46:47], v[136:137] op_sel_hi:[1,0,1]
	v_pk_fma_f32 v[138:139], v[110:111], v[46:47], v[138:139] op_sel_hi:[1,0,1]
	v_fma_f32 v140, v112, v46, v140
	s_barrier
	ds_read_b128 v[104:107], v23 offset:3072
	ds_read_b128 v[108:111], v23 offset:4096
	ds_read_b128 v[192:195], v23 offset:5120
	v_pk_add_f32 v[102:103], v[100:101], v[142:143]
	v_pk_add_f32 v[100:101], v[78:79], v[168:169]
	v_add_f32_e64 v78, v80, v170
	v_pk_add_f32 v[80:81], v[82:83], v[114:115]
	v_pk_add_f32 v[82:83], v[60:61], v[116:117]
	v_add_f32_e64 v60, v62, v120
	v_pk_add_f32 v[62:63], v[64:65], v[122:123]
	v_pk_add_f32 v[64:65], v[66:67], v[124:125]
	v_add_f32_e64 v66, v68, v126
	v_pk_add_f32 v[68:69], v[70:71], v[136:137]
	v_pk_add_f32 v[70:71], v[72:73], v[138:139]
	v_add_f32_e64 v72, v74, v140
	s_waitcnt lgkmcnt(2)
	v_pk_fma_f32 v[80:81], v[104:105], v[102:103], v[80:81] op_sel_hi:[0,1,1] neg_lo:[1,0,0] neg_hi:[1,0,0]
	v_pk_fma_f32 v[82:83], v[104:105], v[100:101], v[82:83] op_sel_hi:[0,1,1] neg_lo:[1,0,0] neg_hi:[1,0,0]
	v_fma_f32 v60, -v104, v78, v60
	v_pk_fma_f32 v[62:63], v[104:105], v[102:103], v[62:63] op_sel:[1,0,0] neg_lo:[1,0,0] neg_hi:[1,0,0]
	v_pk_fma_f32 v[64:65], v[104:105], v[100:101], v[64:65] op_sel:[1,0,0] neg_lo:[1,0,0] neg_hi:[1,0,0]
	v_fma_f32 v66, -v105, v78, v66
	v_pk_fma_f32 v[68:69], v[106:107], v[102:103], v[68:69] op_sel_hi:[0,1,1] neg_lo:[1,0,0] neg_hi:[1,0,0]
	v_pk_fma_f32 v[70:71], v[106:107], v[100:101], v[70:71] op_sel_hi:[0,1,1] neg_lo:[1,0,0] neg_hi:[1,0,0]
	v_fma_f32 v72, -v106, v78, v72
	v_pk_mul_f32 v[74:75], v[106:107], v[80:81] op_sel:[1,0]
	v_pk_mul_f32 v[198:199], v[106:107], v[82:83] op_sel:[1,0]
	v_mul_f32_e64 v204, v107, v60
	s_waitcnt lgkmcnt(1)
	v_pk_mul_f32 v[112:113], v[108:109], v[80:81] op_sel_hi:[0,1]
	v_pk_mul_f32 v[200:201], v[108:109], v[82:83] op_sel_hi:[0,1]
	v_mul_f32_e64 v206, v108, v60
	v_pk_mul_f32 v[196:197], v[108:109], v[80:81] op_sel:[1,0]
	v_pk_mul_f32 v[202:203], v[108:109], v[82:83] op_sel:[1,0]
	v_mul_f32_e64 v208, v109, v60
	v_pk_fma_f32 v[74:75], v[108:109], v[62:63], v[74:75] op_sel_hi:[0,1,1]
	v_pk_fma_f32 v[198:199], v[108:109], v[64:65], v[198:199] op_sel_hi:[0,1,1]
	v_fma_f32 v204, v108, v66, v204
	v_pk_fma_f32 v[112:113], v[110:111], v[62:63], v[112:113] op_sel_hi:[0,1,1]
	v_pk_fma_f32 v[200:201], v[110:111], v[64:65], v[200:201] op_sel_hi:[0,1,1]
	v_fma_f32 v206, v110, v66, v206
	v_pk_fma_f32 v[196:197], v[110:111], v[62:63], v[196:197] op_sel:[1,0,0]
	v_pk_fma_f32 v[202:203], v[110:111], v[64:65], v[202:203] op_sel:[1,0,0]
	v_fma_f32 v208, v111, v66, v208
	v_pk_fma_f32 v[74:75], v[108:109], v[68:69], v[74:75] op_sel:[1,0,0]
	v_pk_fma_f32 v[198:199], v[108:109], v[70:71], v[198:199] op_sel:[1,0,0]
	v_fma_f32 v204, v109, v72, v204
	v_pk_fma_f32 v[112:113], v[110:111], v[68:69], v[112:113] op_sel:[1,0,0]
	v_pk_fma_f32 v[200:201], v[110:111], v[70:71], v[200:201] op_sel:[1,0,0]
	v_fma_f32 v206, v111, v72, v206
	s_waitcnt lgkmcnt(0)
	v_pk_fma_f32 v[196:197], v[192:193], v[68:69], v[196:197] op_sel_hi:[0,1,1]
	v_pk_fma_f32 v[202:203], v[192:193], v[70:71], v[202:203] op_sel_hi:[0,1,1]
	v_fma_f32 v208, v192, v72, v208
	v_pk_mul_f32 v[210:211], v[104:105], v[74:75] op_sel_hi:[0,1]
	v_pk_mul_f32 v[212:213], v[104:105], v[198:199] op_sel_hi:[0,1]
	v_mul_f32_e64 v214, v104, v204
	v_pk_fma_f32 v[210:211], v[104:105], v[112:113], v[210:211] op_sel:[1,0,0]
	v_pk_fma_f32 v[212:213], v[104:105], v[200:201], v[212:213] op_sel:[1,0,0]
	v_fma_f32 v214, v105, v206, v214
	v_pk_fma_f32 v[210:211], v[106:107], v[196:197], v[210:211] op_sel_hi:[0,1,1]
	v_pk_fma_f32 v[212:213], v[106:107], v[202:203], v[212:213] op_sel_hi:[0,1,1]
	v_fma_f32 v214, v106, v208, v214
	v_pk_fma_f32 v[210:211], v[192:193], v[102:103], v[210:211] op_sel:[1,0,0] neg_lo:[0,0,1] neg_hi:[0,0,1]
	v_pk_fma_f32 v[212:213], v[192:193], v[100:101], v[212:213] op_sel:[1,0,0] neg_lo:[0,0,1] neg_hi:[0,0,1]
	v_fma_f32 v214, v193, v78, -v214
	s_add_i32 s4, s34, 4
	s_min_i32 s4, s4, 0x200
	s_mul_i32 s5, s4, 0x804
	s_add_i32 s5, s5, s35
	s_add_i32 s6, s5, 0x0
	s_add_i32 s7, s5, 0x101004
	s_add_i32 s8, s5, 0x202008
	s_add_i32 s11, s5, 0x30300c
	s_add_i32 s15, s5, 0x404010
	s_mul_i32 s9, s4, 0x180c
	s_add_i32 s9, s9, s33
	buffer_load_dword v12, v28, s[16:19], s6 offen nt
	buffer_load_dword v13, v28, s[16:19], s7 offen nt
	buffer_load_dword v14, v28, s[16:19], s8 offen nt
	buffer_load_dword v15, v28, s[16:19], s11 offen nt
	buffer_load_dword v16, v28, s[16:19], s15 offen nt
	buffer_load_dwordx3 v[32:34], v27, s[24:27], s9 offen nt
	s_waitcnt vmcnt(12)
	v_mov_b32_dpp v60, v96 wave_shr:1 row_mask:0xf bank_mask:0xf bound_ctrl:1
	v_mov_b32_dpp v61, v97 wave_shr:1 row_mask:0xf bank_mask:0xf bound_ctrl:1
	v_mov_b32_dpp v62, v98 wave_shr:1 row_mask:0xf bank_mask:0xf bound_ctrl:1
	v_mov_b32_dpp v64, v96 wave_shl:1 row_mask:0xf bank_mask:0xf bound_ctrl:1
	v_mov_b32_dpp v65, v97 wave_shl:1 row_mask:0xf bank_mask:0xf bound_ctrl:1
	v_mov_b32_dpp v66, v98 wave_shl:1 row_mask:0xf bank_mask:0xf bound_ctrl:1
	v_mov_b32_dpp v68, v54 wave_shr:1 row_mask:0xf bank_mask:0xf bound_ctrl:1
	v_mov_b32_dpp v69, v55 wave_shr:1 row_mask:0xf bank_mask:0xf bound_ctrl:1
	v_mov_b32_dpp v70, v92 wave_shr:1 row_mask:0xf bank_mask:0xf bound_ctrl:1
	v_mov_b32_dpp v71, v93 wave_shr:1 row_mask:0xf bank_mask:0xf bound_ctrl:1
	v_mov_b32_dpp v72, v94 wave_shr:1 row_mask:0xf bank_mask:0xf bound_ctrl:1
	v_mov_b32_dpp v78, v54 wave_shl:1 row_mask:0xf bank_mask:0xf bound_ctrl:1
	v_mov_b32_dpp v79, v55 wave_shl:1 row_mask:0xf bank_mask:0xf bound_ctrl:1
	v_mov_b32_dpp v80, v92 wave_shl:1 row_mask:0xf bank_mask:0xf bound_ctrl:1
	v_mov_b32_dpp v81, v93 wave_shl:1 row_mask:0xf bank_mask:0xf bound_ctrl:1
	v_mov_b32_dpp v82, v94 wave_shl:1 row_mask:0xf bank_mask:0xf bound_ctrl:1
	v_pk_mul_f32 v[84:85], v[54:55], v[96:97] op_sel_hi:[1,0]
	v_pk_mul_f32 v[86:87], v[92:93], v[96:97] op_sel_hi:[1,0]
	v_mul_f32_e64 v88, v94, v96
	v_pk_mul_f32 v[90:91], v[54:55], v[96:97] op_sel:[0,1]
	v_pk_mul_f32 v[100:101], v[92:93], v[96:97] op_sel:[0,1]
	v_mul_f32_e64 v102, v94, v97
	v_pk_mul_f32 v[104:105], v[54:55], v[98:99] op_sel_hi:[1,0]
	v_pk_mul_f32 v[106:107], v[92:93], v[98:99] op_sel_hi:[1,0]
	v_mul_f32_e64 v108, v94, v98
	v_pk_add_f32 v[110:111], v[54:55], v[68:69]
	v_pk_add_f32 v[192:193], v[92:93], v[70:71]
	v_add_f32_e64 v194, v94, v72
	v_pk_fma_f32 v[84:85], v[68:69], v[60:61], v[84:85] op_sel_hi:[1,0,1]
	v_pk_fma_f32 v[86:87], v[70:71], v[60:61], v[86:87] op_sel_hi:[1,0,1]
	v_fma_f32 v88, v72, v60, v88
	v_pk_fma_f32 v[90:91], v[68:69], v[60:61], v[90:91] op_sel:[0,1,0]
	v_pk_fma_f32 v[100:101], v[70:71], v[60:61], v[100:101] op_sel:[0,1,0]
	v_fma_f32 v102, v72, v61, v102
	v_pk_fma_f32 v[104:105], v[68:69], v[62:63], v[104:105] op_sel_hi:[1,0,1]
	v_pk_fma_f32 v[106:107], v[70:71], v[62:63], v[106:107] op_sel_hi:[1,0,1]
	v_fma_f32 v108, v72, v62, v108
	v_pk_add_f32 v[110:111], v[110:111], v[78:79]
	v_pk_add_f32 v[192:193], v[192:193], v[80:81]
	v_add_f32_e64 v194, v194, v82
	v_pk_fma_f32 v[84:85], v[78:79], v[64:65], v[84:85] op_sel_hi:[1,0,1]
	v_pk_fma_f32 v[86:87], v[80:81], v[64:65], v[86:87] op_sel_hi:[1,0,1]
	v_fma_f32 v88, v82, v64, v88
	v_pk_fma_f32 v[90:91], v[78:79], v[64:65], v[90:91] op_sel:[0,1,0]
	v_pk_fma_f32 v[100:101], v[80:81], v[64:65], v[100:101] op_sel:[0,1,0]
	v_fma_f32 v102, v82, v65, v102
	v_pk_fma_f32 v[104:105], v[78:79], v[66:67], v[104:105] op_sel_hi:[1,0,1]
	v_pk_fma_f32 v[106:107], v[80:81], v[66:67], v[106:107] op_sel_hi:[1,0,1]
	v_fma_f32 v108, v82, v66, v108
	s_barrier
	ds_read_b128 v[68:71], v23 offset:0
	ds_read_b128 v[80:83], v23 offset:1024
	ds_read_b128 v[216:219], v23 offset:2048
	v_pk_add_f32 v[72:73], v[142:143], v[110:111]
	v_pk_add_f32 v[78:79], v[162:163], v[72:73]
	v_pk_add_f32 v[142:143], v[168:169], v[192:193]
	v_pk_add_f32 v[162:163], v[164:165], v[142:143]
	v_add_f32_e64 v164, v170, v194
	v_add_f32_e64 v168, v166, v164
	v_pk_add_f32 v[166:167], v[114:115], v[84:85]
	v_pk_add_f32 v[170:171], v[144:145], v[166:167]
	v_pk_add_f32 v[114:115], v[116:117], v[86:87]
	v_pk_add_f32 v[144:145], v[146:147], v[114:115]
	v_add_f32_e64 v116, v120, v88
	v_add_f32_e64 v146, v148, v116
	v_pk_add_f32 v[120:121], v[122:123], v[90:91]
	v_pk_add_f32 v[148:149], v[150:151], v[120:121]
	v_pk_add_f32 v[122:123], v[124:125], v[100:101]
	v_pk_add_f32 v[150:151], v[152:153], v[122:123]
	v_add_f32_e64 v124, v126, v102
	v_add_f32_e64 v152, v154, v124
	v_pk_add_f32 v[126:127], v[136:137], v[104:105]
	v_pk_add_f32 v[154:155], v[156:157], v[126:127]
	v_pk_add_f32 v[136:137], v[138:139], v[106:107]
	v_pk_add_f32 v[156:157], v[158:159], v[136:137]
	v_add_f32_e64 v138, v140, v108
	v_add_f32_e64 v158, v160, v138
	s_waitcnt lgkmcnt(2)
	v_pk_fma_f32 v[170:171], v[68:69], v[78:79], v[170:171] op_sel_hi:[0,1,1] neg_lo:[1,0,0] neg_hi:[1,0,0]
	v_pk_fma_f32 v[144:145], v[68:69], v[162:163], v[144:145] op_sel_hi:[0,1,1] neg_lo:[1,0,0] neg_hi:[1,0,0]
	v_fma_f32 v146, -v68, v168, v146
	v_pk_fma_f32 v[148:149], v[68:69], v[78:79], v[148:149] op_sel:[1,0,0] neg_lo:[1,0,0] neg_hi:[1,0,0]
	v_pk_fma_f32 v[150:151], v[68:69], v[162:163], v[150:151] op_sel:[1,0,0] neg_lo:[1,0,0] neg_hi:[1,0,0]
	v_fma_f32 v152, -v69, v168, v152
	v_pk_fma_f32 v[154:155], v[70:71], v[78:79], v[154:155] op_sel_hi:[0,1,1] neg_lo:[1,0,0] neg_hi:[1,0,0]
	v_pk_fma_f32 v[156:157], v[70:71], v[162:163], v[156:157] op_sel_hi:[0,1,1] neg_lo:[1,0,0] neg_hi:[1,0,0]
	v_fma_f32 v158, -v70, v168, v158
	v_pk_mul_f32 v[140:141], v[70:71], v[170:171] op_sel:[1,0]
	v_pk_mul_f32 v[222:223], v[70:71], v[144:145] op_sel:[1,0]
	v_mul_f32_e64 v228, v71, v146
	s_waitcnt lgkmcnt(1)
	v_pk_mul_f32 v[160:161], v[80:81], v[170:171] op_sel_hi:[0,1]
	v_pk_mul_f32 v[224:225], v[80:81], v[144:145] op_sel_hi:[0,1]
	v_mul_f32_e64 v230, v80, v146
	v_pk_mul_f32 v[220:221], v[80:81], v[170:171] op_sel:[1,0]
	v_pk_mul_f32 v[226:227], v[80:81], v[144:145] op_sel:[1,0]
	v_mul_f32_e64 v232, v81, v146
	v_pk_fma_f32 v[140:141], v[80:81], v[148:149], v[140:141] op_sel_hi:[0,1,1]
	v_pk_fma_f32 v[222:223], v[80:81], v[150:151], v[222:223] op_sel_hi:[0,1,1]
	v_fma_f32 v228, v80, v152, v228
	v_pk_fma_f32 v[160:161], v[82:83], v[148:149], v[160:161] op_sel_hi:[0,1,1]
	v_pk_fma_f32 v[224:225], v[82:83], v[150:151], v[224:225] op_sel_hi:[0,1,1]
	v_fma_f32 v230, v82, v152, v230
	v_pk_fma_f32 v[220:221], v[82:83], v[148:149], v[220:221] op_sel:[1,0,0]
	v_pk_fma_f32 v[226:227], v[82:83], v[150:151], v[226:227] op_sel:[1,0,0]
	v_fma_f32 v232, v83, v152, v232
	v_pk_fma_f32 v[140:141], v[80:81], v[154:155], v[140:141] op_sel:[1,0,0]
	v_pk_fma_f32 v[222:223], v[80:81], v[156:157], v[222:223] op_sel:[1,0,0]
	v_fma_f32 v228, v81, v158, v228
	v_pk_fma_f32 v[160:161], v[82:83], v[154:155], v[160:161] op_sel:[1,0,0]
	v_pk_fma_f32 v[224:225], v[82:83], v[156:157], v[224:225] op_sel:[1,0,0]
	v_fma_f32 v230, v83, v158, v230
	s_waitcnt lgkmcnt(0)
	v_pk_fma_f32 v[220:221], v[216:217], v[154:155], v[220:221] op_sel_hi:[0,1,1]
	v_pk_fma_f32 v[226:227], v[216:217], v[156:157], v[226:227] op_sel_hi:[0,1,1]
	v_fma_f32 v232, v216, v158, v232
	v_pk_mul_f32 v[234:235], v[68:69], v[140:141] op_sel_hi:[0,1]
	v_pk_mul_f32 v[236:237], v[68:69], v[222:223] op_sel_hi:[0,1]
	v_mul_f32_e64 v238, v68, v228
	v_pk_fma_f32 v[234:235], v[68:69], v[160:161], v[234:235] op_sel:[1,0,0]
	v_pk_fma_f32 v[236:237], v[68:69], v[224:225], v[236:237] op_sel:[1,0,0]
	v_fma_f32 v238, v69, v230, v238
	v_pk_fma_f32 v[234:235], v[70:71], v[220:221], v[234:235] op_sel_hi:[0,1,1]
	v_pk_fma_f32 v[236:237], v[70:71], v[226:227], v[236:237] op_sel_hi:[0,1,1]
	v_fma_f32 v238, v70, v232, v238
	v_pk_fma_f32 v[234:235], v[216:217], v[78:79], v[234:235] op_sel:[1,0,0] neg_lo:[0,0,1] neg_hi:[0,0,1]
	v_pk_fma_f32 v[236:237], v[216:217], v[162:163], v[236:237] op_sel:[1,0,0] neg_lo:[0,0,1] neg_hi:[0,0,1]
	v_fma_f32 v238, v217, v168, -v238
	v_cmp_eq_u32_e64 s[10:11], 1, v219
	v_cmp_eq_u32_e64 s[14:15], 2, v219
	v_cmp_eq_u32_e64 s[20:21], 3, v219
	v_cmp_eq_u32_e64 s[22:23], 4, v219
	v_cmp_eq_u32_e64 s[30:31], 5, v219
	v_pk_add_f32 v[78:79], v[74:75], v[140:141]
	v_pk_add_f32 v[144:145], v[76:77], v[78:79]
	v_pk_add_f32 v[74:75], v[198:199], v[222:223]
	v_pk_add_f32 v[76:77], v[174:175], v[74:75]
	v_add_f32_e64 v146, v204, v228
	v_add_f32_e64 v148, v180, v146
	v_pk_add_f32 v[150:151], v[112:113], v[160:161]
	v_pk_add_f32 v[152:153], v[118:119], v[150:151]
	v_pk_add_f32 v[112:113], v[200:201], v[224:225]
	v_pk_add_f32 v[118:119], v[176:177], v[112:113]
	v_add_f32_e64 v154, v206, v230
	v_add_f32_e64 v156, v182, v154
	v_pk_add_f32 v[158:159], v[196:197], v[220:221]
	v_pk_add_f32 v[162:163], v[172:173], v[158:159]
	v_pk_add_f32 v[168:169], v[202:203], v[226:227]
	v_pk_add_f32 v[170:171], v[178:179], v[168:169]
	v_add_f32_e64 v172, v208, v232
	v_add_f32_e64 v174, v184, v172
	v_pk_add_f32 v[176:177], v[210:211], v[234:235]
	v_pk_add_f32 v[178:179], v[186:187], v[176:177]
	v_pk_add_f32 v[180:181], v[212:213], v[236:237]
	v_pk_add_f32 v[182:183], v[188:189], v[180:181]
	v_add_f32_e64 v184, v214, v238
	v_add_f32_e64 v186, v190, v184
	v_pk_fma_f32 v[188:189], v[128:129], v[144:145], v[178:179] op_sel_hi:[0,1,1]
	v_pk_fma_f32 v[190:191], v[128:129], v[76:77], v[182:183] op_sel_hi:[0,1,1]
	v_fma_f32 v196, v128, v148, v186
	v_pk_fma_f32 v[198:199], v[132:133], v[144:145], v[178:179] op_sel_hi:[0,1,1]
	v_pk_fma_f32 v[200:201], v[132:133], v[76:77], v[182:183] op_sel_hi:[0,1,1]
	v_fma_f32 v202, v132, v148, v186
	v_pk_fma_f32 v[188:189], v[128:129], v[152:153], v[188:189] op_sel:[1,0,0]
	v_pk_fma_f32 v[190:191], v[128:129], v[118:119], v[190:191] op_sel:[1,0,0]
	v_fma_f32 v196, v129, v156, v196
	v_pk_fma_f32 v[198:199], v[132:133], v[152:153], v[198:199] op_sel:[1,0,0]
	v_pk_fma_f32 v[200:201], v[132:133], v[118:119], v[200:201] op_sel:[1,0,0]
	v_fma_f32 v202, v133, v156, v202
	v_pk_fma_f32 v[188:189], v[130:131], v[162:163], v[188:189] op_sel_hi:[0,1,1]
	v_pk_fma_f32 v[190:191], v[130:131], v[170:171], v[190:191] op_sel_hi:[0,1,1]
	v_fma_f32 v196, v130, v174, v196
	v_pk_fma_f32 v[198:199], v[134:135], v[162:163], v[198:199] op_sel_hi:[0,1,1]
	v_pk_fma_f32 v[200:201], v[134:135], v[170:171], v[200:201] op_sel_hi:[0,1,1]
	v_fma_f32 v202, v134, v174, v202
	v_pk_fma_f32 v[178:179], v[36:37], v[144:145], v[178:179] op_sel_hi:[0,1,1]
	v_pk_fma_f32 v[182:183], v[36:37], v[76:77], v[182:183] op_sel_hi:[0,1,1]
	v_fma_f32 v186, v36, v148, v186
	v_pk_fma_f32 v[178:179], v[36:37], v[152:153], v[178:179] op_sel:[1,0,0]
	v_pk_fma_f32 v[182:183], v[36:37], v[118:119], v[182:183] op_sel:[1,0,0]
	v_fma_f32 v186, v37, v156, v186
	v_pk_fma_f32 v[178:179], v[38:39], v[162:163], v[178:179] op_sel_hi:[0,1,1]
	v_pk_fma_f32 v[182:183], v[38:39], v[170:171], v[182:183] op_sel_hi:[0,1,1]
	v_fma_f32 v186, v38, v174, v186
	v_cndmask_b32_e64 v204, 0, v1, s[10:11]
	v_cndmask_b32_e64 v205, 0, v1, s[14:15]
	v_cndmask_b32_e64 v206, 0, v1, s[20:21]
	v_cndmask_b32_e64 v207, 0, v1, s[22:23]
	v_cndmask_b32_e64 v208, 0, v1, s[30:31]
	v_add_f32_dpp v178, v188, v178 wave_shl:1 row_mask:0xf bank_mask:0xf bound_ctrl:1
	v_add_f32_dpp v179, v189, v179 wave_shl:1 row_mask:0xf bank_mask:0xf bound_ctrl:1
	v_add_f32_dpp v182, v190, v182 wave_shl:1 row_mask:0xf bank_mask:0xf bound_ctrl:1
	v_add_f32_dpp v183, v191, v183 wave_shl:1 row_mask:0xf bank_mask:0xf bound_ctrl:1
	v_add_f32_dpp v186, v196, v186 wave_shl:1 row_mask:0xf bank_mask:0xf bound_ctrl:1
	s_add_i32 s4, s34, 0
	s_cmpk_lt_i32 s4, 0x201
	s_cselect_b64 s[12:13], s[0:1], 0
	v_add_f32_dpp v178, v198, v178 wave_shr:1 row_mask:0xf bank_mask:0xf bound_ctrl:1
	v_add_f32_dpp v179, v199, v179 wave_shr:1 row_mask:0xf bank_mask:0xf bound_ctrl:1
	v_add_f32_dpp v182, v200, v182 wave_shr:1 row_mask:0xf bank_mask:0xf bound_ctrl:1
	v_add_f32_dpp v183, v201, v183 wave_shr:1 row_mask:0xf bank_mask:0xf bound_ctrl:1
	v_add_f32_dpp v186, v202, v186 wave_shr:1 row_mask:0xf bank_mask:0xf bound_ctrl:1
	v_pk_fma_f32 v[178:179], v[20:21], v[218:219], v[178:179] op_sel_hi:[1,0,1] neg_lo:[0,0,1] neg_hi:[0,0,1]
	v_pk_fma_f32 v[182:183], v[24:25], v[218:219], v[182:183] op_sel_hi:[1,0,1] neg_lo:[0,0,1] neg_hi:[0,0,1]
	v_fma_f32 v186, v30, v218, -v186
	v_pk_add_f32 v[178:179], v[178:179], v[204:205] neg_lo:[0,1] neg_hi:[0,1]
	v_pk_add_f32 v[182:183], v[182:183], v[206:207] neg_lo:[0,1] neg_hi:[0,1]
	v_add_f32_e64 v186, v186, -v208
	v_pk_mul_f32 v[210:211], v[178:179], v[178:179]
	v_pk_fma_f32 v[210:211], v[182:183], v[182:183], v[210:211]
	v_add_f32_e32 v210, v210, v211
	v_fma_f32 v210, v186, v186, v210
	v_cndmask_b32_e64 v211, 0, v210, s[12:13]
	v_add_f32_e32 v0, v0, v211
	s_add_i32 s4, s34, 5
	s_min_i32 s4, s4, 0x200
	s_mul_i32 s5, s4, 0x804
	s_add_i32 s5, s5, s35
	s_add_i32 s6, s5, 0x0
	s_add_i32 s7, s5, 0x101004
	s_add_i32 s8, s5, 0x202008
	s_add_i32 s11, s5, 0x30300c
	s_add_i32 s15, s5, 0x404010
	s_mul_i32 s9, s4, 0x180c
	s_add_i32 s9, s9, s33
	buffer_load_dword v20, v28, s[16:19], s6 offen nt
	buffer_load_dword v21, v28, s[16:19], s7 offen nt
	buffer_load_dword v24, v28, s[16:19], s8 offen nt
	buffer_load_dword v25, v28, s[16:19], s11 offen nt
	buffer_load_dword v30, v28, s[16:19], s15 offen nt
	buffer_load_dwordx3 v[36:38], v27, s[24:27], s9 offen nt
	s_waitcnt vmcnt(12)
	v_mov_b32_dpp v68, v8 wave_shr:1 row_mask:0xf bank_mask:0xf bound_ctrl:1
	v_mov_b32_dpp v69, v9 wave_shr:1 row_mask:0xf bank_mask:0xf bound_ctrl:1
	v_mov_b32_dpp v70, v10 wave_shr:1 row_mask:0xf bank_mask:0xf bound_ctrl:1
	v_mov_b32_dpp v80, v8 wave_shl:1 row_mask:0xf bank_mask:0xf bound_ctrl:1
	v_mov_b32_dpp v81, v9 wave_shl:1 row_mask:0xf bank_mask:0xf bound_ctrl:1
	v_mov_b32_dpp v82, v10 wave_shl:1 row_mask:0xf bank_mask:0xf bound_ctrl:1
	v_mov_b32_dpp v76, v2 wave_shr:1 row_mask:0xf bank_mask:0xf bound_ctrl:1
	v_mov_b32_dpp v77, v3 wave_shr:1 row_mask:0xf bank_mask:0xf bound_ctrl:1
	v_mov_b32_dpp v118, v4 wave_shr:1 row_mask:0xf bank_mask:0xf bound_ctrl:1
	v_mov_b32_dpp v119, v5 wave_shr:1 row_mask:0xf bank_mask:0xf bound_ctrl:1
	v_mov_b32_dpp v128, v6 wave_shr:1 row_mask:0xf bank_mask:0xf bound_ctrl:1
	v_mov_b32_dpp v130, v2 wave_shl:1 row_mask:0xf bank_mask:0xf bound_ctrl:1
	v_mov_b32_dpp v131, v3 wave_shl:1 row_mask:0xf bank_mask:0xf bound_ctrl:1
	v_mov_b32_dpp v132, v4 wave_shl:1 row_mask:0xf bank_mask:0xf bound_ctrl:1
	v_mov_b32_dpp v133, v5 wave_shl:1 row_mask:0xf bank_mask:0xf bound_ctrl:1
	v_mov_b32_dpp v134, v6 wave_shl:1 row_mask:0xf bank_mask:0xf bound_ctrl:1
	v_pk_mul_f32 v[144:145], v[2:3], v[8:9] op_sel_hi:[1,0]
	v_pk_mul_f32 v[148:149], v[4:5], v[8:9] op_sel_hi:[1,0]
	v_mul_f32_e64 v152, v6, v8
	v_pk_mul_f32 v[156:157], v[2:3], v[8:9] op_sel:[0,1]
	v_pk_mul_f32 v[162:163], v[4:5], v[8:9] op_sel:[0,1]
	v_mul_f32_e64 v170, v6, v9
	v_pk_mul_f32 v[174:175], v[2:3], v[10:11] op_sel_hi:[1,0]
	v_pk_mul_f32 v[178:179], v[4:5], v[10:11] op_sel_hi:[1,0]
	v_mul_f32_e64 v182, v6, v10
	v_pk_add_f32 v[186:187], v[2:3], v[76:77]
	v_pk_add_f32 v[188:189], v[4:5], v[118:119]
	v_add_f32_e64 v190, v6, v128
	v_pk_fma_f32 v[144:145], v[76:77], v[68:69], v[144:145] op_sel_hi:[1,0,1]
	v_pk_fma_f32 v[148:149], v[118:119], v[68:69], v[148:149] op_sel_hi:[1,0,1]
	v_fma_f32 v152, v128, v68, v152
	v_pk_fma_f32 v[156:157], v[76:77], v[68:69], v[156:157] op_sel:[0,1,0]
	v_pk_fma_f32 v[162:163], v[118:119], v[68:69], v[162:163] op_sel:[0,1,0]
	v_fma_f32 v170, v128, v69, v170
	v_pk_fma_f32 v[174:175], v[76:77], v[70:71], v[174:175] op_sel_hi:[1,0,1]
	v_pk_fma_f32 v[178:179], v[118:119], v[70:71], v[178:179] op_sel_hi:[1,0,1]
	v_fma_f32 v182, v128, v70, v182
	v_pk_add_f32 v[186:187], v[186:187], v[130:131]
	v_pk_add_f32 v[188:189], v[188:189], v[132:133]
	v_add_f32_e64 v190, v190, v134
	v_pk_fma_f32 v[144:145], v[130:131], v[80:81], v[144:145] op_sel_hi:[1,0,1]
	v_pk_fma_f32 v[148:149], v[132:133], v[80:81], v[148:149] op_sel_hi:[1,0,1]
	v_fma_f32 v152, v134, v80, v152
	v_pk_fma_f32 v[156:157], v[130:131], v[80:81], v[156:157] op_sel:[0,1,0]
	v_pk_fma_f32 v[162:163], v[132:133], v[80:81], v[162:163] op_sel:[0,1,0]
	v_fma_f32 v170, v134, v81, v170
	v_pk_fma_f32 v[174:175], v[130:131], v[82:83], v[174:175] op_sel_hi:[1,0,1]
	v_pk_fma_f32 v[178:179], v[132:133], v[82:83], v[178:179] op_sel_hi:[1,0,1]
	v_fma_f32 v182, v134, v82, v182
	s_barrier
	ds_read_b128 v[128:131], v23 offset:3072
	ds_read_b128 v[132:135], v23 offset:4096
	ds_read_b128 v[196:199], v23 offset:5120
	v_pk_add_f32 v[76:77], v[72:73], v[186:187]
	v_pk_add_f32 v[72:73], v[142:143], v[188:189]
	v_add_f32_e64 v118, v164, v190
	v_pk_add_f32 v[142:143], v[166:167], v[144:145]
	v_pk_add_f32 v[164:165], v[114:115], v[148:149]
	v_add_f32_e64 v114, v116, v152
	v_pk_add_f32 v[116:117], v[120:121], v[156:157]
	v_pk_add_f32 v[120:121], v[122:123], v[162:163]
	v_add_f32_e64 v122, v124, v170
	v_pk_add_f32 v[124:125], v[126:127], v[174:175]
	v_pk_add_f32 v[126:127], v[136:137], v[178:179]
	v_add_f32_e64 v136, v138, v182
	s_waitcnt lgkmcnt(2)
	v_pk_fma_f32 v[142:143], v[128:129], v[76:77], v[142:143] op_sel_hi:[0,1,1] neg_lo:[1,0,0] neg_hi:[1,0,0]
	v_pk_fma_f32 v[164:165], v[128:129], v[72:73], v[164:165] op_sel_hi:[0,1,1] neg_lo:[1,0,0] neg_hi:[1,0,0]
	v_fma_f32 v114, -v128, v118, v114
	v_pk_fma_f32 v[116:117], v[128:129], v[76:77], v[116:117] op_sel:[1,0,0] neg_lo:[1,0,0] neg_hi:[1,0,0]
	v_pk_fma_f32 v[120:121], v[128:129], v[72:73], v[120:121] op_sel:[1,0,0] neg_lo:[1,0,0] neg_hi:[1,0,0]
	v_fma_f32 v122, -v129, v118, v122
	v_pk_fma_f32 v[124:125], v[130:131], v[76:77], v[124:125] op_sel_hi:[0,1,1] neg_lo:[1,0,0] neg_hi:[1,0,0]
	v_pk_fma_f32 v[126:127], v[130:131], v[72:73], v[126:127] op_sel_hi:[0,1,1] neg_lo:[1,0,0] neg_hi:[1,0,0]
	v_fma_f32 v136, -v130, v118, v136
	v_pk_mul_f32 v[138:139], v[130:131], v[142:143] op_sel:[1,0]
	v_pk_mul_f32 v[202:203], v[130:131], v[164:165] op_sel:[1,0]
	v_mul_f32_e64 v208, v131, v114
	s_waitcnt lgkmcnt(1)
	v_pk_mul_f32 v[166:167], v[132:133], v[142:143] op_sel_hi:[0,1]
	v_pk_mul_f32 v[204:205], v[132:133], v[164:165] op_sel_hi:[0,1]
	v_mul_f32_e64 v210, v132, v114
	v_pk_mul_f32 v[200:201], v[132:133], v[142:143] op_sel:[1,0]
	v_pk_mul_f32 v[206:207], v[132:133], v[164:165] op_sel:[1,0]
	v_mul_f32_e64 v212, v133, v114
	v_pk_fma_f32 v[138:139], v[132:133], v[116:117], v[138:139] op_sel_hi:[0,1,1]
	v_pk_fma_f32 v[202:203], v[132:133], v[120:121], v[202:203] op_sel_hi:[0,1,1]
	v_fma_f32 v208, v132, v122, v208
	v_pk_fma_f32 v[166:167], v[134:135], v[116:117], v[166:167] op_sel_hi:[0,1,1]
	v_pk_fma_f32 v[204:205], v[134:135], v[120:121], v[204:205] op_sel_hi:[0,1,1]
	v_fma_f32 v210, v134, v122, v210
	v_pk_fma_f32 v[200:201], v[134:135], v[116:117], v[200:201] op_sel:[1,0,0]
	v_pk_fma_f32 v[206:207], v[134:135], v[120:121], v[206:207] op_sel:[1,0,0]
	v_fma_f32 v212, v135, v122, v212
	v_pk_fma_f32 v[138:139], v[132:133], v[124:125], v[138:139] op_sel:[1,0,0]
	v_pk_fma_f32 v[202:203], v[132:133], v[126:127], v[202:203] op_sel:[1,0,0]
	v_fma_f32 v208, v133, v136, v208
	v_pk_fma_f32 v[166:167], v[134:135], v[124:125], v[166:167] op_sel:[1,0,0]
	v_pk_fma_f32 v[204:205], v[134:135], v[126:127], v[204:205] op_sel:[1,0,0]
	v_fma_f32 v210, v135, v136, v210
	s_waitcnt lgkmcnt(0)
	v_pk_fma_f32 v[200:201], v[196:197], v[124:125], v[200:201] op_sel_hi:[0,1,1]
	v_pk_fma_f32 v[206:207], v[196:197], v[126:127], v[206:207] op_sel_hi:[0,1,1]
	v_fma_f32 v212, v196, v136, v212
	v_pk_mul_f32 v[214:215], v[128:129], v[138:139] op_sel_hi:[0,1]
	v_pk_mul_f32 v[216:217], v[128:129], v[202:203] op_sel_hi:[0,1]
	v_mul_f32_e64 v218, v128, v208
	v_pk_fma_f32 v[214:215], v[128:129], v[166:167], v[214:215] op_sel:[1,0,0]
	v_pk_fma_f32 v[216:217], v[128:129], v[204:205], v[216:217] op_sel:[1,0,0]
	v_fma_f32 v218, v129, v210, v218
	v_pk_fma_f32 v[214:215], v[130:131], v[200:201], v[214:215] op_sel_hi:[0,1,1]
	v_pk_fma_f32 v[216:217], v[130:131], v[206:207], v[216:217] op_sel_hi:[0,1,1]
	v_fma_f32 v218, v130, v212, v218
	v_pk_fma_f32 v[214:215], v[196:197], v[76:77], v[214:215] op_sel:[1,0,0] neg_lo:[0,0,1] neg_hi:[0,0,1]
	v_pk_fma_f32 v[216:217], v[196:197], v[72:73], v[216:217] op_sel:[1,0,0] neg_lo:[0,0,1] neg_hi:[0,0,1]
	v_fma_f32 v218, v197, v118, -v218
	v_cmp_eq_u32_e64 s[10:11], 1, v199
	v_cmp_eq_u32_e64 s[14:15], 2, v199
	v_cmp_eq_u32_e64 s[20:21], 3, v199
	v_cmp_eq_u32_e64 s[22:23], 4, v199
	v_cmp_eq_u32_e64 s[30:31], 5, v199
	v_pk_add_f32 v[72:73], v[78:79], v[138:139]
	v_pk_add_f32 v[76:77], v[74:75], v[202:203]
	v_add_f32_e64 v74, v146, v208
	v_pk_add_f32 v[78:79], v[150:151], v[166:167]
	v_pk_add_f32 v[114:115], v[112:113], v[204:205]
	v_add_f32_e64 v112, v154, v210
	v_pk_add_f32 v[116:117], v[158:159], v[200:201]
	v_pk_add_f32 v[118:119], v[168:169], v[206:207]
	v_add_f32_e64 v120, v172, v212
	v_pk_add_f32 v[122:123], v[176:177], v[214:215]
	v_pk_add_f32 v[124:125], v[180:181], v[216:217]
	v_add_f32_e64 v126, v184, v218
	v_pk_fma_f32 v[136:137], v[40:41], v[72:73], v[122:123] op_sel_hi:[0,1,1]
	v_pk_fma_f32 v[142:143], v[40:41], v[76:77], v[124:125] op_sel_hi:[0,1,1]
	v_fma_f32 v146, v40, v74, v126
	v_pk_fma_f32 v[150:151], v[44:45], v[72:73], v[122:123] op_sel_hi:[0,1,1]
	v_pk_fma_f32 v[154:155], v[44:45], v[76:77], v[124:125] op_sel_hi:[0,1,1]
	v_fma_f32 v158, v44, v74, v126
	v_pk_fma_f32 v[136:137], v[40:41], v[78:79], v[136:137] op_sel:[1,0,0]
	v_pk_fma_f32 v[142:143], v[40:41], v[114:115], v[142:143] op_sel:[1,0,0]
	v_fma_f32 v146, v41, v112, v146
	v_pk_fma_f32 v[150:151], v[44:45], v[78:79], v[150:151] op_sel:[1,0,0]
	v_pk_fma_f32 v[154:155], v[44:45], v[114:115], v[154:155] op_sel:[1,0,0]
	v_fma_f32 v158, v45, v112, v158
	v_pk_fma_f32 v[136:137], v[42:43], v[116:117], v[136:137] op_sel_hi:[0,1,1]
	v_pk_fma_f32 v[142:143], v[42:43], v[118:119], v[142:143] op_sel_hi:[0,1,1]
	v_fma_f32 v146, v42, v120, v146
	v_pk_fma_f32 v[150:151], v[46:47], v[116:117], v[150:151] op_sel_hi:[0,1,1]
	v_pk_fma_f32 v[154:155], v[46:47], v[118:119], v[154:155] op_sel_hi:[0,1,1]
	v_fma_f32 v158, v46, v120, v158
	v_pk_fma_f32 v[122:123], v[56:57], v[72:73], v[122:123] op_sel_hi:[0,1,1]
	v_pk_fma_f32 v[124:125], v[56:57], v[76:77], v[124:125] op_sel_hi:[0,1,1]
	v_fma_f32 v126, v56, v74, v126
	v_pk_fma_f32 v[122:123], v[56:57], v[78:79], v[122:123] op_sel:[1,0,0]
	v_pk_fma_f32 v[124:125], v[56:57], v[114:115], v[124:125] op_sel:[1,0,0]
	v_fma_f32 v126, v57, v112, v126
	v_pk_fma_f32 v[122:123], v[58:59], v[116:117], v[122:123] op_sel_hi:[0,1,1]
	v_pk_fma_f32 v[124:125], v[58:59], v[118:119], v[124:125] op_sel_hi:[0,1,1]
	v_fma_f32 v126, v58, v120, v126
	v_cndmask_b32_e64 v164, 0, v1, s[10:11]
	v_cndmask_b32_e64 v165, 0, v1, s[14:15]
	v_cndmask_b32_e64 v168, 0, v1, s[20:21]
	v_cndmask_b32_e64 v169, 0, v1, s[22:23]
	v_cndmask_b32_e64 v172, 0, v1, s[30:31]
	v_add_f32_dpp v122, v136, v122 wave_shl:1 row_mask:0xf bank_mask:0xf bound_ctrl:1
	v_add_f32_dpp v123, v137, v123 wave_shl:1 row_mask:0xf bank_mask:0xf bound_ctrl:1
	v_add_f32_dpp v124, v142, v124 wave_shl:1 row_mask:0xf bank_mask:0xf bound_ctrl:1
	v_add_f32_dpp v125, v143, v125 wave_shl:1 row_mask:0xf bank_mask:0xf bound_ctrl:1
	v_add_f32_dpp v126, v146, v126 wave_shl:1 row_mask:0xf bank_mask:0xf bound_ctrl:1
	s_add_i32 s4, s34, 1
	s_cmpk_lt_i32 s4, 0x201
	s_cselect_b64 s[12:13], s[0:1], 0
	v_add_f32_dpp v122, v150, v122 wave_shr:1 row_mask:0xf bank_mask:0xf bound_ctrl:1
	v_add_f32_dpp v123, v151, v123 wave_shr:1 row_mask:0xf bank_mask:0xf bound_ctrl:1
	v_add_f32_dpp v124, v154, v124 wave_shr:1 row_mask:0xf bank_mask:0xf bound_ctrl:1
	v_add_f32_dpp v125, v155, v125 wave_shr:1 row_mask:0xf bank_mask:0xf bound_ctrl:1
	v_add_f32_dpp v126, v158, v126 wave_shr:1 row_mask:0xf bank_mask:0xf bound_ctrl:1
	v_pk_fma_f32 v[122:123], v[48:49], v[198:199], v[122:123] op_sel_hi:[1,0,1] neg_lo:[0,0,1] neg_hi:[0,0,1]
	v_pk_fma_f32 v[124:125], v[50:51], v[198:199], v[124:125] op_sel_hi:[1,0,1] neg_lo:[0,0,1] neg_hi:[0,0,1]
	v_fma_f32 v126, v52, v198, -v126
	v_pk_add_f32 v[122:123], v[122:123], v[164:165] neg_lo:[0,1] neg_hi:[0,1]
	v_pk_add_f32 v[124:125], v[124:125], v[168:169] neg_lo:[0,1] neg_hi:[0,1]
	v_add_f32_e64 v126, v126, -v172
	v_pk_mul_f32 v[176:177], v[122:123], v[122:123]
	v_pk_fma_f32 v[176:177], v[124:125], v[124:125], v[176:177]
	v_add_f32_e32 v176, v176, v177
	v_fma_f32 v176, v126, v126, v176
	v_cndmask_b32_e64 v177, 0, v176, s[12:13]
	v_add_f32_e32 v0, v0, v177
	s_add_i32 s4, s34, 6
	s_min_i32 s4, s4, 0x200
	s_mul_i32 s5, s4, 0x804
	s_add_i32 s5, s5, s35
	s_add_i32 s6, s5, 0x0
	s_add_i32 s7, s5, 0x101004
	s_add_i32 s8, s5, 0x202008
	s_add_i32 s11, s5, 0x30300c
	s_add_i32 s15, s5, 0x404010
	s_mul_i32 s9, s4, 0x180c
	s_add_i32 s9, s9, s33
	buffer_load_dword v40, v28, s[16:19], s6 offen nt
	buffer_load_dword v41, v28, s[16:19], s7 offen nt
	buffer_load_dword v42, v28, s[16:19], s8 offen nt
	buffer_load_dword v43, v28, s[16:19], s11 offen nt
	buffer_load_dword v44, v28, s[16:19], s15 offen nt
	buffer_load_dwordx3 v[48:50], v27, s[24:27], s9 offen nt
	s_waitcnt vmcnt(12)
	v_mov_b32_dpp v56, v32 wave_shr:1 row_mask:0xf bank_mask:0xf bound_ctrl:1
	v_mov_b32_dpp v57, v33 wave_shr:1 row_mask:0xf bank_mask:0xf bound_ctrl:1
	v_mov_b32_dpp v58, v34 wave_shr:1 row_mask:0xf bank_mask:0xf bound_ctrl:1
	v_mov_b32_dpp v72, v32 wave_shl:1 row_mask:0xf bank_mask:0xf bound_ctrl:1
	v_mov_b32_dpp v73, v33 wave_shl:1 row_mask:0xf bank_mask:0xf bound_ctrl:1
	v_mov_b32_dpp v74, v34 wave_shl:1 row_mask:0xf bank_mask:0xf bound_ctrl:1
	v_mov_b32_dpp v46, v12 wave_shr:1 row_mask:0xf bank_mask:0xf bound_ctrl:1
	v_mov_b32_dpp v47, v13 wave_shr:1 row_mask:0xf bank_mask:0xf bound_ctrl:1
	v_mov_b32_dpp v52, v14 wave_shr:1 row_mask:0xf bank_mask:0xf bound_ctrl:1
	v_mov_b32_dpp v53, v15 wave_shr:1 row_mask:0xf bank_mask:0xf bound_ctrl:1
	v_mov_b32_dpp v76, v16 wave_shr:1 row_mask:0xf bank_mask:0xf bound_ctrl:1
	v_mov_b32_dpp v78, v12 wave_shl:1 row_mask:0xf bank_mask:0xf bound_ctrl:1
	v_mov_b32_dpp v79, v13 wave_shl:1 row_mask:0xf bank_mask:0xf bound_ctrl:1
	v_mov_b32_dpp v112, v14 wave_shl:1 row_mask:0xf bank_mask:0xf bound_ctrl:1
	v_mov_b32_dpp v113, v15 wave_shl:1 row_mask:0xf bank_mask:0xf bound_ctrl:1
	v_mov_b32_dpp v114, v16 wave_shl:1 row_mask:0xf bank_mask:0xf bound_ctrl:1
	v_pk_mul_f32 v[116:117], v[12:13], v[32:33] op_sel_hi:[1,0]
	v_pk_mul_f32 v[118:119], v[14:15], v[32:33] op_sel_hi:[1,0]
	v_mul_f32_e64 v120, v16, v32
	v_pk_mul_f32 v[122:123], v[12:13], v[32:33] op_sel:[0,1]
	v_pk_mul_f32 v[124:125], v[14:15], v[32:33] op_sel:[0,1]
	v_mul_f32_e64 v126, v16, v33
	v_pk_mul_f32 v[128:129], v[12:13], v[34:35] op_sel_hi:[1,0]
	v_pk_mul_f32 v[130:131], v[14:15], v[34:35] op_sel_hi:[1,0]
	v_mul_f32_e64 v132, v16, v34
	v_pk_add_f32 v[134:135], v[12:13], v[46:47]
	v_pk_add_f32 v[136:137], v[14:15], v[52:53]
	v_add_f32_e64 v142, v16, v76
	v_pk_fma_f32 v[116:117], v[46:47], v[56:57], v[116:117] op_sel_hi:[1,0,1]
	v_pk_fma_f32 v[118:119], v[52:53], v[56:57], v[118:119] op_sel_hi:[1,0,1]
	v_fma_f32 v120, v76, v56, v120
	v_pk_fma_f32 v[122:123], v[46:47], v[56:57], v[122:123] op_sel:[0,1,0]
	v_pk_fma_f32 v[124:125], v[52:53], v[56:57], v[124:125] op_sel:[0,1,0]
	v_fma_f32 v126, v76, v57, v126
	v_pk_fma_f32 v[128:129], v[46:47], v[58:59], v[128:129] op_sel_hi:[1,0,1]
	v_pk_fma_f32 v[130:131], v[52:53], v[58:59], v[130:131] op_sel_hi:[1,0,1]
	v_fma_f32 v132, v76, v58, v132
	v_pk_add_f32 v[134:135], v[134:135], v[78:79]
	v_pk_add_f32 v[136:137], v[136:137], v[112:113]
	v_add_f32_e64 v142, v142, v114
	v_pk_fma_f32 v[116:117], v[78:79], v[72:73], v[116:117] op_sel_hi:[1,0,1]
	v_pk_fma_f32 v[118:119], v[112:113], v[72:73], v[118:119] op_sel_hi:[1,0,1]
	v_fma_f32 v120, v114, v72, v120
	v_pk_fma_f32 v[122:123], v[78:79], v[72:73], v[122:123] op_sel:[0,1,0]
	v_pk_fma_f32 v[124:125], v[112:113], v[72:73], v[124:125] op_sel:[0,1,0]
	v_fma_f32 v126, v114, v73, v126
	v_pk_fma_f32 v[128:129], v[78:79], v[74:75], v[128:129] op_sel_hi:[1,0,1]
	v_pk_fma_f32 v[130:131], v[112:113], v[74:75], v[130:131] op_sel_hi:[1,0,1]
	v_fma_f32 v132, v114, v74, v132
	s_barrier
	ds_read_b128 v[76:79], v23 offset:0
	ds_read_b128 v[112:115], v23 offset:1024
	ds_read_b128 v[196:199], v23 offset:2048
	v_pk_add_f32 v[46:47], v[186:187], v[134:135]
	v_pk_add_f32 v[52:53], v[110:111], v[46:47]
	v_pk_add_f32 v[110:111], v[188:189], v[136:137]
	v_pk_add_f32 v[146:147], v[192:193], v[110:111]
	v_add_f32_e64 v150, v190, v142
	v_add_f32_e64 v154, v194, v150
	v_pk_add_f32 v[158:159], v[144:145], v[116:117]
	v_pk_add_f32 v[164:165], v[84:85], v[158:159]
	v_pk_add_f32 v[84:85], v[148:149], v[118:119]
	v_pk_add_f32 v[144:145], v[86:87], v[84:85]
	v_add_f32_e64 v86, v152, v120
	v_add_f32_e64 v148, v88, v86
	v_pk_add_f32 v[88:89], v[156:157], v[122:123]
	v_pk_add_f32 v[152:153], v[90:91], v[88:89]
	v_pk_add_f32 v[90:91], v[162:163], v[124:125]
	v_pk_add_f32 v[156:157], v[100:101], v[90:91]
	v_add_f32_e64 v100, v170, v126
	v_add_f32_e64 v162, v102, v100
	v_pk_add_f32 v[102:103], v[174:175], v[128:129]
	v_pk_add_f32 v[168:169], v[104:105], v[102:103]
	v_pk_add_f32 v[104:105], v[178:179], v[130:131]
	v_pk_add_f32 v[170:171], v[106:107], v[104:105]
	v_add_f32_e64 v106, v182, v132
	v_add_f32_e64 v172, v108, v106
	s_waitcnt lgkmcnt(2)
	v_pk_fma_f32 v[164:165], v[76:77], v[52:53], v[164:165] op_sel_hi:[0,1,1] neg_lo:[1,0,0] neg_hi:[1,0,0]
	v_pk_fma_f32 v[144:145], v[76:77], v[146:147], v[144:145] op_sel_hi:[0,1,1] neg_lo:[1,0,0] neg_hi:[1,0,0]
	v_fma_f32 v148, -v76, v154, v148
	v_pk_fma_f32 v[152:153], v[76:77], v[52:53], v[152:153] op_sel:[1,0,0] neg_lo:[1,0,0] neg_hi:[1,0,0]
	v_pk_fma_f32 v[156:157], v[76:77], v[146:147], v[156:157] op_sel:[1,0,0] neg_lo:[1,0,0] neg_hi:[1,0,0]
	v_fma_f32 v162, -v77, v154, v162
	v_pk_fma_f32 v[168:169], v[78:79], v[52:53], v[168:169] op_sel_hi:[0,1,1] neg_lo:[1,0,0] neg_hi:[1,0,0]
	v_pk_fma_f32 v[170:171], v[78:79], v[146:147], v[170:171] op_sel_hi:[0,1,1] neg_lo:[1,0,0] neg_hi:[1,0,0]
	v_fma_f32 v172, -v78, v154, v172
	v_pk_mul_f32 v[108:109], v[78:79], v[164:165] op_sel:[1,0]
	v_pk_mul_f32 v[178:179], v[78:79], v[144:145] op_sel:[1,0]
	v_mul_f32_e64 v184, v79, v148
	s_waitcnt lgkmcnt(1)
	v_pk_mul_f32 v[174:175], v[112:113], v[164:165] op_sel_hi:[0,1]
	v_pk_mul_f32 v[180:181], v[112:113], v[144:145] op_sel_hi:[0,1]
	v_mul_f32_e64 v186, v112, v148
	v_pk_mul_f32 v[176:177], v[112:113], v[164:165] op_sel:[1,0]
	v_pk_mul_f32 v[182:183], v[112:113], v[144:145] op_sel:[1,0]
	v_mul_f32_e64 v188, v113, v148
	v_pk_fma_f32 v[108:109], v[112:113], v[152:153], v[108:109] op_sel_hi:[0,1,1]
	v_pk_fma_f32 v[178:179], v[112:113], v[156:157], v[178:179] op_sel_hi:[0,1,1]
	v_fma_f32 v184, v112, v162, v184
	v_pk_fma_f32 v[174:175], v[114:115], v[152:153], v[174:175] op_sel_hi:[0,1,1]
	v_pk_fma_f32 v[180:181], v[114:115], v[156:157], v[180:181] op_sel_hi:[0,1,1]
	v_fma_f32 v186, v114, v162, v186
	v_pk_fma_f32 v[176:177], v[114:115], v[152:153], v[176:177] op_sel:[1,0,0]
	v_pk_fma_f32 v[182:183], v[114:115], v[156:157], v[182:183] op_sel:[1,0,0]
	v_fma_f32 v188, v115, v162, v188
	v_pk_fma_f32 v[108:109], v[112:113], v[168:169], v[108:109] op_sel:[1,0,0]
	v_pk_fma_f32 v[178:179], v[112:113], v[170:171], v[178:179] op_sel:[1,0,0]
	v_fma_f32 v184, v113, v172, v184
	v_pk_fma_f32 v[174:175], v[114:115], v[168:169], v[174:175] op_sel:[1,0,0]
	v_pk_fma_f32 v[180:181], v[114:115], v[170:171], v[180:181] op_sel:[1,0,0]
	v_fma_f32 v186, v115, v172, v186
	s_waitcnt lgkmcnt(0)
	v_pk_fma_f32 v[176:177], v[196:197], v[168:169], v[176:177] op_sel_hi:[0,1,1]
	v_pk_fma_f32 v[182:183], v[196:197], v[170:171], v[182:183] op_sel_hi:[0,1,1]
	v_fma_f32 v188, v196, v172, v188
	v_pk_mul_f32 v[190:191], v[76:77], v[108:109] op_sel_hi:[0,1]
	v_pk_mul_f32 v[192:193], v[76:77], v[178:179] op_sel_hi:[0,1]
	v_mul_f32_e64 v194, v76, v184
	v_pk_fma_f32 v[190:191], v[76:77], v[174:175], v[190:191] op_sel:[1,0,0]
	v_pk_fma_f32 v[192:193], v[76:77], v[180:181], v[192:193] op_sel:[1,0,0]
	v_fma_f32 v194, v77, v186, v194
	v_pk_fma_f32 v[190:191], v[78:79], v[176:177], v[190:191] op_sel_hi:[0,1,1]
	v_pk_fma_f32 v[192:193], v[78:79], v[182:183], v[192:193] op_sel_hi:[0,1,1]
	v_fma_f32 v194, v78, v188, v194
	v_pk_fma_f32 v[190:191], v[196:197], v[52:53], v[190:191] op_sel:[1,0,0] neg_lo:[0,0,1] neg_hi:[0,0,1]
	v_pk_fma_f32 v[192:193], v[196:197], v[146:147], v[192:193] op_sel:[1,0,0] neg_lo:[0,0,1] neg_hi:[0,0,1]
	v_fma_f32 v194, v197, v154, -v194
	v_cmp_eq_u32_e64 s[10:11], 1, v199
	v_cmp_eq_u32_e64 s[14:15], 2, v199
	v_cmp_eq_u32_e64 s[20:21], 3, v199
	v_cmp_eq_u32_e64 s[22:23], 4, v199
	v_cmp_eq_u32_e64 s[30:31], 5, v199
	v_pk_add_f32 v[52:53], v[138:139], v[108:109]
	v_pk_add_f32 v[144:145], v[140:141], v[52:53]
	v_pk_add_f32 v[138:139], v[202:203], v[178:179]
	v_pk_add_f32 v[140:141], v[222:223], v[138:139]
	v_add_f32_e64 v146, v208, v184
	v_add_f32_e64 v148, v228, v146
	v_pk_add_f32 v[152:153], v[166:167], v[174:175]
	v_pk_add_f32 v[154:155], v[160:161], v[152:153]
	v_pk_add_f32 v[156:157], v[204:205], v[180:181]
	v_pk_add_f32 v[160:161], v[224:225], v[156:157]
	v_add_f32_e64 v162, v210, v186
	v_add_f32_e64 v164, v230, v162
	v_pk_add_f32 v[166:167], v[200:201], v[176:177]
	v_pk_add_f32 v[168:169], v[220:221], v[166:167]
	v_pk_add_f32 v[170:171], v[206:207], v[182:183]
	v_pk_add_f32 v[172:173], v[226:227], v[170:171]
	v_add_f32_e64 v200, v212, v188
	v_add_f32_e64 v202, v232, v200
	v_pk_add_f32 v[204:205], v[214:215], v[190:191]
	v_pk_add_f32 v[206:207], v[234:235], v[204:205]
	v_pk_add_f32 v[208:209], v[216:217], v[192:193]
	v_pk_add_f32 v[210:211], v[236:237], v[208:209]
	v_add_f32_e64 v212, v218, v194
	v_add_f32_e64 v214, v238, v212
	v_pk_fma_f32 v[216:217], v[60:61], v[144:145], v[206:207] op_sel_hi:[0,1,1]
	v_pk_fma_f32 v[218:219], v[60:61], v[140:141], v[210:211] op_sel_hi:[0,1,1]
	v_fma_f32 v220, v60, v148, v214
	v_pk_fma_f32 v[222:223], v[64:65], v[144:145], v[206:207] op_sel_hi:[0,1,1]
	v_pk_fma_f32 v[224:225], v[64:65], v[140:141], v[210:211] op_sel_hi:[0,1,1]
	v_fma_f32 v226, v64, v148, v214
	v_pk_fma_f32 v[216:217], v[60:61], v[154:155], v[216:217] op_sel:[1,0,0]
	v_pk_fma_f32 v[218:219], v[60:61], v[160:161], v[218:219] op_sel:[1,0,0]
	v_fma_f32 v220, v61, v164, v220
	v_pk_fma_f32 v[222:223], v[64:65], v[154:155], v[222:223] op_sel:[1,0,0]
	v_pk_fma_f32 v[224:225], v[64:65], v[160:161], v[224:225] op_sel:[1,0,0]
	v_fma_f32 v226, v65, v164, v226
	v_pk_fma_f32 v[216:217], v[62:63], v[168:169], v[216:217] op_sel_hi:[0,1,1]
	v_pk_fma_f32 v[218:219], v[62:63], v[172:173], v[218:219] op_sel_hi:[0,1,1]
	v_fma_f32 v220, v62, v202, v220
	v_pk_fma_f32 v[222:223], v[66:67], v[168:169], v[222:223] op_sel_hi:[0,1,1]
	v_pk_fma_f32 v[224:225], v[66:67], v[172:173], v[224:225] op_sel_hi:[0,1,1]
	v_fma_f32 v226, v66, v202, v226
	v_pk_fma_f32 v[206:207], v[96:97], v[144:145], v[206:207] op_sel_hi:[0,1,1]
	v_pk_fma_f32 v[210:211], v[96:97], v[140:141], v[210:211] op_sel_hi:[0,1,1]
	v_fma_f32 v214, v96, v148, v214
	v_pk_fma_f32 v[206:207], v[96:97], v[154:155], v[206:207] op_sel:[1,0,0]
	v_pk_fma_f32 v[210:211], v[96:97], v[160:161], v[210:211] op_sel:[1,0,0]
	v_fma_f32 v214, v97, v164, v214
	v_pk_fma_f32 v[206:207], v[98:99], v[168:169], v[206:207] op_sel_hi:[0,1,1]
	v_pk_fma_f32 v[210:211], v[98:99], v[172:173], v[210:211] op_sel_hi:[0,1,1]
	v_fma_f32 v214, v98, v202, v214
	v_cndmask_b32_e64 v228, 0, v1, s[10:11]
	v_cndmask_b32_e64 v229, 0, v1, s[14:15]
	v_cndmask_b32_e64 v230, 0, v1, s[20:21]
	v_cndmask_b32_e64 v231, 0, v1, s[22:23]
	v_cndmask_b32_e64 v232, 0, v1, s[30:31]
	v_add_f32_dpp v206, v216, v206 wave_shl:1 row_mask:0xf bank_mask:0xf bound_ctrl:1
	v_add_f32_dpp v207, v217, v207 wave_shl:1 row_mask:0xf bank_mask:0xf bound_ctrl:1
	v_add_f32_dpp v210, v218, v210 wave_shl:1 row_mask:0xf bank_mask:0xf bound_ctrl:1
	v_add_f32_dpp v211, v219, v211 wave_shl:1 row_mask:0xf bank_mask:0xf bound_ctrl:1
	v_add_f32_dpp v214, v220, v214 wave_shl:1 row_mask:0xf bank_mask:0xf bound_ctrl:1
	s_add_i32 s4, s34, 2
	s_cmpk_lt_i32 s4, 0x201
	s_cselect_b64 s[12:13], s[0:1], 0
	v_add_f32_dpp v206, v222, v206 wave_shr:1 row_mask:0xf bank_mask:0xf bound_ctrl:1
	v_add_f32_dpp v207, v223, v207 wave_shr:1 row_mask:0xf bank_mask:0xf bound_ctrl:1
	v_add_f32_dpp v210, v224, v210 wave_shr:1 row_mask:0xf bank_mask:0xf bound_ctrl:1
	v_add_f32_dpp v211, v225, v211 wave_shr:1 row_mask:0xf bank_mask:0xf bound_ctrl:1
	v_add_f32_dpp v214, v226, v214 wave_shr:1 row_mask:0xf bank_mask:0xf bound_ctrl:1
	v_pk_fma_f32 v[206:207], v[54:55], v[198:199], v[206:207] op_sel_hi:[1,0,1] neg_lo:[0,0,1] neg_hi:[0,0,1]
	v_pk_fma_f32 v[210:211], v[92:93], v[198:199], v[210:211] op_sel_hi:[1,0,1] neg_lo:[0,0,1] neg_hi:[0,0,1]
	v_fma_f32 v214, v94, v198, -v214
	v_pk_add_f32 v[206:207], v[206:207], v[228:229] neg_lo:[0,1] neg_hi:[0,1]
	v_pk_add_f32 v[210:211], v[210:211], v[230:231] neg_lo:[0,1] neg_hi:[0,1]
	v_add_f32_e64 v214, v214, -v232
	v_pk_mul_f32 v[234:235], v[206:207], v[206:207]
	v_pk_fma_f32 v[234:235], v[210:211], v[210:211], v[234:235]
	v_add_f32_e32 v234, v234, v235
	v_fma_f32 v234, v214, v214, v234
	v_cndmask_b32_e64 v235, 0, v234, s[12:13]
	v_add_f32_e32 v0, v0, v235
	s_add_i32 s4, s34, 7
	s_min_i32 s4, s4, 0x200
	s_mul_i32 s5, s4, 0x804
	s_add_i32 s5, s5, s35
	s_add_i32 s6, s5, 0x0
	s_add_i32 s7, s5, 0x101004
	s_add_i32 s8, s5, 0x202008
	s_add_i32 s11, s5, 0x30300c
	s_add_i32 s15, s5, 0x404010
	s_mul_i32 s9, s4, 0x180c
	s_add_i32 s9, s9, s33
	buffer_load_dword v54, v28, s[16:19], s6 offen nt
	buffer_load_dword v55, v28, s[16:19], s7 offen nt
	buffer_load_dword v60, v28, s[16:19], s8 offen nt
	buffer_load_dword v61, v28, s[16:19], s11 offen nt
	buffer_load_dword v62, v28, s[16:19], s15 offen nt
	buffer_load_dwordx3 v[64:66], v27, s[24:27], s9 offen nt
	s_waitcnt vmcnt(12)
	v_mov_b32_dpp v76, v36 wave_shr:1 row_mask:0xf bank_mask:0xf bound_ctrl:1
	v_mov_b32_dpp v77, v37 wave_shr:1 row_mask:0xf bank_mask:0xf bound_ctrl:1
	v_mov_b32_dpp v78, v38 wave_shr:1 row_mask:0xf bank_mask:0xf bound_ctrl:1
	v_mov_b32_dpp v92, v36 wave_shl:1 row_mask:0xf bank_mask:0xf bound_ctrl:1
	v_mov_b32_dpp v93, v37 wave_shl:1 row_mask:0xf bank_mask:0xf bound_ctrl:1
	v_mov_b32_dpp v94, v38 wave_shl:1 row_mask:0xf bank_mask:0xf bound_ctrl:1
	v_mov_b32_dpp v96, v20 wave_shr:1 row_mask:0xf bank_mask:0xf bound_ctrl:1
	v_mov_b32_dpp v97, v21 wave_shr:1 row_mask:0xf bank_mask:0xf bound_ctrl:1
	v_mov_b32_dpp v98, v24 wave_shr:1 row_mask:0xf bank_mask:0xf bound_ctrl:1
	v_mov_b32_dpp v99, v25 wave_shr:1 row_mask:0xf bank_mask:0xf bound_ctrl:1
	v_mov_b32_dpp v112, v30 wave_shr:1 row_mask:0xf bank_mask:0xf bound_ctrl:1
	v_mov_b32_dpp v114, v20 wave_shl:1 row_mask:0xf bank_mask:0xf bound_ctrl:1
	v_mov_b32_dpp v115, v21 wave_shl:1 row_mask:0xf bank_mask:0xf bound_ctrl:1
	v_mov_b32_dpp v140, v24 wave_shl:1 row_mask:0xf bank_mask:0xf bound_ctrl:1
	v_mov_b32_dpp v141, v25 wave_shl:1 row_mask:0xf bank_mask:0xf bound_ctrl:1
	v_mov_b32_dpp v144, v30 wave_shl:1 row_mask:0xf bank_mask:0xf bound_ctrl:1
	v_pk_mul_f32 v[148:149], v[20:21], v[36:37] op_sel_hi:[1,0]
	v_pk_mul_f32 v[154:155], v[24:25], v[36:37] op_sel_hi:[1,0]
	v_mul_f32_e64 v160, v30, v36
	v_pk_mul_f32 v[164:165], v[20:21], v[36:37] op_sel:[0,1]
	v_pk_mul_f32 v[168:169], v[24:25], v[36:37] op_sel:[0,1]
	v_mul_f32_e64 v172, v30, v37
	v_pk_mul_f32 v[196:197], v[20:21], v[38:39] op_sel_hi:[1,0]
	v_pk_mul_f32 v[198:199], v[24:25], v[38:39] op_sel_hi:[1,0]
	v_mul_f32_e64 v202, v30, v38
	v_pk_add_f32 v[206:207], v[20:21], v[96:97]
	v_pk_add_f32 v[210:211], v[24:25], v[98:99]
	v_add_f32_e64 v214, v30, v112
	v_pk_fma_f32 v[148:149], v[96:97], v[76:77], v[148:149] op_sel_hi:[1,0,1]
	v_pk_fma_f32 v[154:155], v[98:99], v[76:77], v[154:155] op_sel_hi:[1,0,1]
	v_fma_f32 v160, v112, v76, v160
	v_pk_fma_f32 v[164:165], v[96:97], v[76:77], v[164:165] op_sel:[0,1,0]
	v_pk_fma_f32 v[168:169], v[98:99], v[76:77], v[168:169] op_sel:[0,1,0]
	v_fma_f32 v172, v112, v77, v172
	v_pk_fma_f32 v[196:197], v[96:97], v[78:79], v[196:197] op_sel_hi:[1,0,1]
	v_pk_fma_f32 v[198:199], v[98:99], v[78:79], v[198:199] op_sel_hi:[1,0,1]
	v_fma_f32 v202, v112, v78, v202
	v_pk_add_f32 v[206:207], v[206:207], v[114:115]
	v_pk_add_f32 v[210:211], v[210:211], v[140:141]
	v_add_f32_e64 v214, v214, v144
	v_pk_fma_f32 v[148:149], v[114:115], v[92:93], v[148:149] op_sel_hi:[1,0,1]
	v_pk_fma_f32 v[154:155], v[140:141], v[92:93], v[154:155] op_sel_hi:[1,0,1]
	v_fma_f32 v160, v144, v92, v160
	v_pk_fma_f32 v[164:165], v[114:115], v[92:93], v[164:165] op_sel:[0,1,0]
	v_pk_fma_f32 v[168:169], v[140:141], v[92:93], v[168:169] op_sel:[0,1,0]
	v_fma_f32 v172, v144, v93, v172
	v_pk_fma_f32 v[196:197], v[114:115], v[94:95], v[196:197] op_sel_hi:[1,0,1]
	v_pk_fma_f32 v[198:199], v[140:141], v[94:95], v[198:199] op_sel_hi:[1,0,1]
	v_fma_f32 v202, v144, v94, v202
	s_barrier
	ds_read_b128 v[96:99], v23 offset:3072
	ds_read_b128 v[112:115], v23 offset:4096
	ds_read_b128 v[216:219], v23 offset:5120
	v_pk_add_f32 v[140:141], v[46:47], v[206:207]
	v_pk_add_f32 v[46:47], v[110:111], v[210:211]
	v_add_f32_e64 v110, v150, v214
	v_pk_add_f32 v[144:145], v[158:159], v[148:149]
	v_pk_add_f32 v[150:151], v[84:85], v[154:155]
	v_add_f32_e64 v84, v86, v160
	v_pk_add_f32 v[86:87], v[88:89], v[164:165]
	v_pk_add_f32 v[88:89], v[90:91], v[168:169]
	v_add_f32_e64 v90, v100, v172
	v_pk_add_f32 v[100:101], v[102:103], v[196:197]
	v_pk_add_f32 v[102:103], v[104:105], v[198:199]
	v_add_f32_e64 v104, v106, v202
	s_waitcnt lgkmcnt(2)
	v_pk_fma_f32 v[144:145], v[96:97], v[140:141], v[144:145] op_sel_hi:[0,1,1] neg_lo:[1,0,0] neg_hi:[1,0,0]
	v_pk_fma_f32 v[150:151], v[96:97], v[46:47], v[150:151] op_sel_hi:[0,1,1] neg_lo:[1,0,0] neg_hi:[1,0,0]
	v_fma_f32 v84, -v96, v110, v84
	v_pk_fma_f32 v[86:87], v[96:97], v[140:141], v[86:87] op_sel:[1,0,0] neg_lo:[1,0,0] neg_hi:[1,0,0]
	v_pk_fma_f32 v[88:89], v[96:97], v[46:47], v[88:89] op_sel:[1,0,0] neg_lo:[1,0,0] neg_hi:[1,0,0]
	v_fma_f32 v90, -v97, v110, v90
	v_pk_fma_f32 v[100:101], v[98:99], v[140:141], v[100:101] op_sel_hi:[0,1,1] neg_lo:[1,0,0] neg_hi:[1,0,0]
	v_pk_fma_f32 v[102:103], v[98:99], v[46:47], v[102:103] op_sel_hi:[0,1,1] neg_lo:[1,0,0] neg_hi:[1,0,0]
	v_fma_f32 v104, -v98, v110, v104
	v_pk_mul_f32 v[106:107], v[98:99], v[144:145] op_sel:[1,0]
	v_pk_mul_f32 v[222:223], v[98:99], v[150:151] op_sel:[1,0]
	v_mul_f32_e64 v228, v99, v84
	s_waitcnt lgkmcnt(1)
	v_pk_mul_f32 v[158:159], v[112:113], v[144:145] op_sel_hi:[0,1]
	v_pk_mul_f32 v[224:225], v[112:113], v[150:151] op_sel_hi:[0,1]
	v_mul_f32_e64 v230, v112, v84
	v_pk_mul_f32 v[220:221], v[112:113], v[144:145] op_sel:[1,0]
	v_pk_mul_f32 v[226:227], v[112:113], v[150:151] op_sel:[1,0]
	v_mul_f32_e64 v232, v113, v84
	v_pk_fma_f32 v[106:107], v[112:113], v[86:87], v[106:107] op_sel_hi:[0,1,1]
	v_pk_fma_f32 v[222:223], v[112:113], v[88:89], v[222:223] op_sel_hi:[0,1,1]
	v_fma_f32 v228, v112, v90, v228
	v_pk_fma_f32 v[158:159], v[114:115], v[86:87], v[158:159] op_sel_hi:[0,1,1]
	v_pk_fma_f32 v[224:225], v[114:115], v[88:89], v[224:225] op_sel_hi:[0,1,1]
	v_fma_f32 v230, v114, v90, v230
	v_pk_fma_f32 v[220:221], v[114:115], v[86:87], v[220:221] op_sel:[1,0,0]
	v_pk_fma_f32 v[226:227], v[114:115], v[88:89], v[226:227] op_sel:[1,0,0]
	v_fma_f32 v232, v115, v90, v232
	v_pk_fma_f32 v[106:107], v[112:113], v[100:101], v[106:107] op_sel:[1,0,0]
	v_pk_fma_f32 v[222:223], v[112:113], v[102:103], v[222:223] op_sel:[1,0,0]
	v_fma_f32 v228, v113, v104, v228
	v_pk_fma_f32 v[158:159], v[114:115], v[100:101], v[158:159] op_sel:[1,0,0]
	v_pk_fma_f32 v[224:225], v[114:115], v[102:103], v[224:225] op_sel:[1,0,0]
	v_fma_f32 v230, v115, v104, v230
	s_waitcnt lgkmcnt(0)
	v_pk_fma_f32 v[220:221], v[216:217], v[100:101], v[220:221] op_sel_hi:[0,1,1]
	v_pk_fma_f32 v[226:227], v[216:217], v[102:103], v[226:227] op_sel_hi:[0,1,1]
	v_fma_f32 v232, v216, v104, v232
	v_pk_mul_f32 v[234:235], v[96:97], v[106:107] op_sel_hi:[0,1]
	v_pk_mul_f32 v[236:237], v[96:97], v[222:223] op_sel_hi:[0,1]
	v_mul_f32_e64 v238, v96, v228
	v_pk_fma_f32 v[234:235], v[96:97], v[158:159], v[234:235] op_sel:[1,0,0]
	v_pk_fma_f32 v[236:237], v[96:97], v[224:225], v[236:237] op_sel:[1,0,0]
	v_fma_f32 v238, v97, v230, v238
	v_pk_fma_f32 v[234:235], v[98:99], v[220:221], v[234:235] op_sel_hi:[0,1,1]
	v_pk_fma_f32 v[236:237], v[98:99], v[226:227], v[236:237] op_sel_hi:[0,1,1]
	v_fma_f32 v238, v98, v232, v238
	v_pk_fma_f32 v[234:235], v[216:217], v[140:141], v[234:235] op_sel:[1,0,0] neg_lo:[0,0,1] neg_hi:[0,0,1]
	v_pk_fma_f32 v[236:237], v[216:217], v[46:47], v[236:237] op_sel:[1,0,0] neg_lo:[0,0,1] neg_hi:[0,0,1]
	v_fma_f32 v238, v217, v110, -v238
	v_cmp_eq_u32_e64 s[10:11], 1, v219
	v_cmp_eq_u32_e64 s[14:15], 2, v219
	v_cmp_eq_u32_e64 s[20:21], 3, v219
	v_cmp_eq_u32_e64 s[22:23], 4, v219
	v_cmp_eq_u32_e64 s[30:31], 5, v219
	v_pk_add_f32 v[46:47], v[52:53], v[106:107]
	v_pk_add_f32 v[52:53], v[138:139], v[222:223]
	v_add_f32_e64 v84, v146, v228
	v_pk_add_f32 v[86:87], v[152:153], v[158:159]
	v_pk_add_f32 v[88:89], v[156:157], v[224:225]
	v_add_f32_e64 v90, v162, v230
	v_pk_add_f32 v[100:101], v[166:167], v[220:221]
	v_pk_add_f32 v[102:103], v[170:171], v[226:227]
	v_add_f32_e64 v104, v200, v232
	v_pk_add_f32 v[110:111], v[204:205], v[234:235]
	v_pk_add_f32 v[138:139], v[208:209], v[236:237]
	v_add_f32_e64 v140, v212, v238
	v_pk_fma_f32 v[144:145], v[68:69], v[46:47], v[110:111] op_sel_hi:[0,1,1]
	v_pk_fma_f32 v[146:147], v[68:69], v[52:53], v[138:139] op_sel_hi:[0,1,1]
	v_fma_f32 v150, v68, v84, v140
	v_pk_fma_f32 v[152:153], v[80:81], v[46:47], v[110:111] op_sel_hi:[0,1,1]
	v_pk_fma_f32 v[156:157], v[80:81], v[52:53], v[138:139] op_sel_hi:[0,1,1]
	v_fma_f32 v162, v80, v84, v140
	v_pk_fma_f32 v[144:145], v[68:69], v[86:87], v[144:145] op_sel:[1,0,0]
	v_pk_fma_f32 v[146:147], v[68:69], v[88:89], v[146:147] op_sel:[1,0,0]
	v_fma_f32 v150, v69, v90, v150
	v_pk_fma_f32 v[152:153], v[80:81], v[86:87], v[152:153] op_sel:[1,0,0]
	v_pk_fma_f32 v[156:157], v[80:81], v[88:89], v[156:157] op_sel:[1,0,0]
	v_fma_f32 v162, v81, v90, v162
	v_pk_fma_f32 v[144:145], v[70:71], v[100:101], v[144:145] op_sel_hi:[0,1,1]
	v_pk_fma_f32 v[146:147], v[70:71], v[102:103], v[146:147] op_sel_hi:[0,1,1]
	v_fma_f32 v150, v70, v104, v150
	v_pk_fma_f32 v[152:153], v[82:83], v[100:101], v[152:153] op_sel_hi:[0,1,1]
	v_pk_fma_f32 v[156:157], v[82:83], v[102:103], v[156:157] op_sel_hi:[0,1,1]
	v_fma_f32 v162, v82, v104, v162
	v_pk_fma_f32 v[110:111], v[8:9], v[46:47], v[110:111] op_sel_hi:[0,1,1]
	v_pk_fma_f32 v[138:139], v[8:9], v[52:53], v[138:139] op_sel_hi:[0,1,1]
	v_fma_f32 v140, v8, v84, v140
	v_pk_fma_f32 v[110:111], v[8:9], v[86:87], v[110:111] op_sel:[1,0,0]
	v_pk_fma_f32 v[138:139], v[8:9], v[88:89], v[138:139] op_sel:[1,0,0]
	v_fma_f32 v140, v9, v90, v140
	v_pk_fma_f32 v[110:111], v[10:11], v[100:101], v[110:111] op_sel_hi:[0,1,1]
	v_pk_fma_f32 v[138:139], v[10:11], v[102:103], v[138:139] op_sel_hi:[0,1,1]
	v_fma_f32 v140, v10, v104, v140
	v_cndmask_b32_e64 v166, 0, v1, s[10:11]
	v_cndmask_b32_e64 v167, 0, v1, s[14:15]
	v_cndmask_b32_e64 v170, 0, v1, s[20:21]
	v_cndmask_b32_e64 v171, 0, v1, s[22:23]
	v_cndmask_b32_e64 v200, 0, v1, s[30:31]
	v_add_f32_dpp v110, v144, v110 wave_shl:1 row_mask:0xf bank_mask:0xf bound_ctrl:1
	v_add_f32_dpp v111, v145, v111 wave_shl:1 row_mask:0xf bank_mask:0xf bound_ctrl:1
	v_add_f32_dpp v138, v146, v138 wave_shl:1 row_mask:0xf bank_mask:0xf bound_ctrl:1
	v_add_f32_dpp v139, v147, v139 wave_shl:1 row_mask:0xf bank_mask:0xf bound_ctrl:1
	v_add_f32_dpp v140, v150, v140 wave_shl:1 row_mask:0xf bank_mask:0xf bound_ctrl:1
	s_add_i32 s4, s34, 3
	s_cmpk_lt_i32 s4, 0x201
	s_cselect_b64 s[12:13], s[0:1], 0
	v_add_f32_dpp v110, v152, v110 wave_shr:1 row_mask:0xf bank_mask:0xf bound_ctrl:1
	v_add_f32_dpp v111, v153, v111 wave_shr:1 row_mask:0xf bank_mask:0xf bound_ctrl:1
	v_add_f32_dpp v138, v156, v138 wave_shr:1 row_mask:0xf bank_mask:0xf bound_ctrl:1
	v_add_f32_dpp v139, v157, v139 wave_shr:1 row_mask:0xf bank_mask:0xf bound_ctrl:1
	v_add_f32_dpp v140, v162, v140 wave_shr:1 row_mask:0xf bank_mask:0xf bound_ctrl:1
	v_pk_fma_f32 v[110:111], v[2:3], v[218:219], v[110:111] op_sel_hi:[1,0,1] neg_lo:[0,0,1] neg_hi:[0,0,1]
	v_pk_fma_f32 v[138:139], v[4:5], v[218:219], v[138:139] op_sel_hi:[1,0,1] neg_lo:[0,0,1] neg_hi:[0,0,1]
	v_fma_f32 v140, v6, v218, -v140
	v_pk_add_f32 v[110:111], v[110:111], v[166:167] neg_lo:[0,1] neg_hi:[0,1]
	v_pk_add_f32 v[138:139], v[138:139], v[170:171] neg_lo:[0,1] neg_hi:[0,1]
	v_add_f32_e64 v140, v140, -v200
	v_pk_mul_f32 v[204:205], v[110:111], v[110:111]
	v_pk_fma_f32 v[204:205], v[138:139], v[138:139], v[204:205]
	v_add_f32_e32 v204, v204, v205
	v_fma_f32 v204, v140, v140, v204
	v_cndmask_b32_e64 v205, 0, v204, s[12:13]
	v_add_f32_e32 v0, v0, v205
	s_add_i32 s4, s34, 8
	s_min_i32 s4, s4, 0x200
	s_mul_i32 s5, s4, 0x804
	s_add_i32 s5, s5, s35
	s_add_i32 s6, s5, 0x0
	s_add_i32 s7, s5, 0x101004
	s_add_i32 s8, s5, 0x202008
	s_add_i32 s11, s5, 0x30300c
	s_add_i32 s15, s5, 0x404010
	s_mul_i32 s9, s4, 0x180c
	s_add_i32 s9, s9, s33
	buffer_load_dword v2, v28, s[16:19], s6 offen nt
	buffer_load_dword v3, v28, s[16:19], s7 offen nt
	buffer_load_dword v4, v28, s[16:19], s8 offen nt
	buffer_load_dword v5, v28, s[16:19], s11 offen nt
	buffer_load_dword v6, v28, s[16:19], s15 offen nt
	buffer_load_dwordx3 v[8:10], v27, s[24:27], s9 offen nt
	s_waitcnt vmcnt(12)
	v_mov_b32_dpp v68, v48 wave_shr:1 row_mask:0xf bank_mask:0xf bound_ctrl:1
	v_mov_b32_dpp v69, v49 wave_shr:1 row_mask:0xf bank_mask:0xf bound_ctrl:1
	v_mov_b32_dpp v70, v50 wave_shr:1 row_mask:0xf bank_mask:0xf bound_ctrl:1
	v_mov_b32_dpp v80, v48 wave_shl:1 row_mask:0xf bank_mask:0xf bound_ctrl:1
	v_mov_b32_dpp v81, v49 wave_shl:1 row_mask:0xf bank_mask:0xf bound_ctrl:1
	v_mov_b32_dpp v82, v50 wave_shl:1 row_mask:0xf bank_mask:0xf bound_ctrl:1
	v_mov_b32_dpp v46, v40 wave_shr:1 row_mask:0xf bank_mask:0xf bound_ctrl:1
	v_mov_b32_dpp v47, v41 wave_shr:1 row_mask:0xf bank_mask:0xf bound_ctrl:1
	v_mov_b32_dpp v52, v42 wave_shr:1 row_mask:0xf bank_mask:0xf bound_ctrl:1
	v_mov_b32_dpp v53, v43 wave_shr:1 row_mask:0xf bank_mask:0xf bound_ctrl:1
	v_mov_b32_dpp v84, v44 wave_shr:1 row_mask:0xf bank_mask:0xf bound_ctrl:1
	v_mov_b32_dpp v86, v40 wave_shl:1 row_mask:0xf bank_mask:0xf bound_ctrl:1
	v_mov_b32_dpp v87, v41 wave_shl:1 row_mask:0xf bank_mask:0xf bound_ctrl:1
	v_mov_b32_dpp v88, v42 wave_shl:1 row_mask:0xf bank_mask:0xf bound_ctrl:1
	v_mov_b32_dpp v89, v43 wave_shl:1 row_mask:0xf bank_mask:0xf bound_ctrl:1
	v_mov_b32_dpp v90, v44 wave_shl:1 row_mask:0xf bank_mask:0xf bound_ctrl:1
	v_pk_mul_f32 v[96:97], v[40:41], v[48:49] op_sel_hi:[1,0]
	v_pk_mul_f32 v[98:99], v[42:43], v[48:49] op_sel_hi:[1,0]
	v_mul_f32_e64 v100, v44, v48
	v_pk_mul_f32 v[102:103], v[40:41], v[48:49] op_sel:[0,1]
	v_pk_mul_f32 v[104:105], v[42:43], v[48:49] op_sel:[0,1]
	v_mul_f32_e64 v110, v44, v49
	v_pk_mul_f32 v[112:113], v[40:41], v[50:51] op_sel_hi:[1,0]
	v_pk_mul_f32 v[114:115], v[42:43], v[50:51] op_sel_hi:[1,0]
	v_mul_f32_e64 v138, v44, v50
	v_pk_add_f32 v[140:141], v[40:41], v[46:47]
	v_pk_add_f32 v[144:145], v[42:43], v[52:53]
	v_add_f32_e64 v146, v44, v84
	v_pk_fma_f32 v[96:97], v[46:47], v[68:69], v[96:97] op_sel_hi:[1,0,1]
	v_pk_fma_f32 v[98:99], v[52:53], v[68:69], v[98:99] op_sel_hi:[1,0,1]
	v_fma_f32 v100, v84, v68, v100
	v_pk_fma_f32 v[102:103], v[46:47], v[68:69], v[102:103] op_sel:[0,1,0]
	v_pk_fma_f32 v[104:105], v[52:53], v[68:69], v[104:105] op_sel:[0,1,0]
	v_fma_f32 v110, v84, v69, v110
	v_pk_fma_f32 v[112:113], v[46:47], v[70:71], v[112:113] op_sel_hi:[1,0,1]
	v_pk_fma_f32 v[114:115], v[52:53], v[70:71], v[114:115] op_sel_hi:[1,0,1]
	v_fma_f32 v138, v84, v70, v138
	v_pk_add_f32 v[140:141], v[140:141], v[86:87]
	v_pk_add_f32 v[144:145], v[144:145], v[88:89]
	v_add_f32_e64 v146, v146, v90
	v_pk_fma_f32 v[96:97], v[86:87], v[80:81], v[96:97] op_sel_hi:[1,0,1]
	v_pk_fma_f32 v[98:99], v[88:89], v[80:81], v[98:99] op_sel_hi:[1,0,1]
	v_fma_f32 v100, v90, v80, v100
	v_pk_fma_f32 v[102:103], v[86:87], v[80:81], v[102:103] op_sel:[0,1,0]
	v_pk_fma_f32 v[104:105], v[88:89], v[80:81], v[104:105] op_sel:[0,1,0]
	v_fma_f32 v110, v90, v81, v110
	v_pk_fma_f32 v[112:113], v[86:87], v[82:83], v[112:113] op_sel_hi:[1,0,1]
	v_pk_fma_f32 v[114:115], v[88:89], v[82:83], v[114:115] op_sel_hi:[1,0,1]
	v_fma_f32 v138, v90, v82, v138
	s_barrier
	ds_read_b128 v[84:87], v23 offset:0
	ds_read_b128 v[88:91], v23 offset:1024
	ds_read_b128 v[216:219], v23 offset:2048
	v_pk_add_f32 v[46:47], v[206:207], v[140:141]
	v_pk_add_f32 v[52:53], v[134:135], v[46:47]
	v_pk_add_f32 v[134:135], v[210:211], v[144:145]
	v_pk_add_f32 v[150:151], v[136:137], v[134:135]
	v_add_f32_e64 v136, v214, v146
	v_add_f32_e64 v152, v142, v136
	v_pk_add_f32 v[142:143], v[148:149], v[96:97]
	v_pk_add_f32 v[156:157], v[116:117], v[142:143]
	v_pk_add_f32 v[116:117], v[154:155], v[98:99]
	v_pk_add_f32 v[148:149], v[118:119], v[116:117]
	v_add_f32_e64 v118, v160, v100
	v_add_f32_e64 v154, v120, v118
	v_pk_add_f32 v[120:121], v[164:165], v[102:103]
	v_pk_add_f32 v[160:161], v[122:123], v[120:121]
	v_pk_add_f32 v[122:123], v[168:169], v[104:105]
	v_pk_add_f32 v[162:163], v[124:125], v[122:123]
	v_add_f32_e64 v124, v172, v110
	v_add_f32_e64 v164, v126, v124
	v_pk_add_f32 v[126:127], v[196:197], v[112:113]
	v_pk_add_f32 v[166:167], v[128:129], v[126:127]
	v_pk_add_f32 v[128:129], v[198:199], v[114:115]
	v_pk_add_f32 v[168:169], v[130:131], v[128:129]
	v_add_f32_e64 v130, v202, v138
	v_add_f32_e64 v170, v132, v130
	s_waitcnt lgkmcnt(2)
	v_pk_fma_f32 v[156:157], v[84:85], v[52:53], v[156:157] op_sel_hi:[0,1,1] neg_lo:[1,0,0] neg_hi:[1,0,0]
	v_pk_fma_f32 v[148:149], v[84:85], v[150:151], v[148:149] op_sel_hi:[0,1,1] neg_lo:[1,0,0] neg_hi:[1,0,0]
	v_fma_f32 v154, -v84, v152, v154
	v_pk_fma_f32 v[160:161], v[84:85], v[52:53], v[160:161] op_sel:[1,0,0] neg_lo:[1,0,0] neg_hi:[1,0,0]
	v_pk_fma_f32 v[162:163], v[84:85], v[150:151], v[162:163] op_sel:[1,0,0] neg_lo:[1,0,0] neg_hi:[1,0,0]
	v_fma_f32 v164, -v85, v152, v164
	v_pk_fma_f32 v[166:167], v[86:87], v[52:53], v[166:167] op_sel_hi:[0,1,1] neg_lo:[1,0,0] neg_hi:[1,0,0]
	v_pk_fma_f32 v[168:169], v[86:87], v[150:151], v[168:169] op_sel_hi:[0,1,1] neg_lo:[1,0,0] neg_hi:[1,0,0]
	v_fma_f32 v170, -v86, v152, v170
	v_pk_mul_f32 v[132:133], v[86:87], v[156:157] op_sel:[1,0]
	v_pk_mul_f32 v[198:199], v[86:87], v[148:149] op_sel:[1,0]
	v_mul_f32_e64 v204, v87, v154
	s_waitcnt lgkmcnt(1)
	v_pk_mul_f32 v[172:173], v[88:89], v[156:157] op_sel_hi:[0,1]
	v_pk_mul_f32 v[200:201], v[88:89], v[148:149] op_sel_hi:[0,1]
	v_mul_f32_e64 v206, v88, v154
	v_pk_mul_f32 v[196:197], v[88:89], v[156:157] op_sel:[1,0]
	v_pk_mul_f32 v[202:203], v[88:89], v[148:149] op_sel:[1,0]
	v_mul_f32_e64 v208, v89, v154
	v_pk_fma_f32 v[132:133], v[88:89], v[160:161], v[132:133] op_sel_hi:[0,1,1]
	v_pk_fma_f32 v[198:199], v[88:89], v[162:163], v[198:199] op_sel_hi:[0,1,1]
	v_fma_f32 v204, v88, v164, v204
	v_pk_fma_f32 v[172:173], v[90:91], v[160:161], v[172:173] op_sel_hi:[0,1,1]
	v_pk_fma_f32 v[200:201], v[90:91], v[162:163], v[200:201] op_sel_hi:[0,1,1]
	v_fma_f32 v206, v90, v164, v206
	v_pk_fma_f32 v[196:197], v[90:91], v[160:161], v[196:197] op_sel:[1,0,0]
	v_pk_fma_f32 v[202:203], v[90:91], v[162:163], v[202:203] op_sel:[1,0,0]
	v_fma_f32 v208, v91, v164, v208
	v_pk_fma_f32 v[132:133], v[88:89], v[166:167], v[132:133] op_sel:[1,0,0]
	v_pk_fma_f32 v[198:199], v[88:89], v[168:169], v[198:199] op_sel:[1,0,0]
	v_fma_f32 v204, v89, v170, v204
	v_pk_fma_f32 v[172:173], v[90:91], v[166:167], v[172:173] op_sel:[1,0,0]
	v_pk_fma_f32 v[200:201], v[90:91], v[168:169], v[200:201] op_sel:[1,0,0]
	v_fma_f32 v206, v91, v170, v206
	s_waitcnt lgkmcnt(0)
	v_pk_fma_f32 v[196:197], v[216:217], v[166:167], v[196:197] op_sel_hi:[0,1,1]
	v_pk_fma_f32 v[202:203], v[216:217], v[168:169], v[202:203] op_sel_hi:[0,1,1]
	v_fma_f32 v208, v216, v170, v208
	v_pk_mul_f32 v[210:211], v[84:85], v[132:133] op_sel_hi:[0,1]
	v_pk_mul_f32 v[212:213], v[84:85], v[198:199] op_sel_hi:[0,1]
	v_mul_f32_e64 v214, v84, v204
	v_pk_fma_f32 v[210:211], v[84:85], v[172:173], v[210:211] op_sel:[1,0,0]
	v_pk_fma_f32 v[212:213], v[84:85], v[200:201], v[212:213] op_sel:[1,0,0]
	v_fma_f32 v214, v85, v206, v214
	v_pk_fma_f32 v[210:211], v[86:87], v[196:197], v[210:211] op_sel_hi:[0,1,1]
	v_pk_fma_f32 v[212:213], v[86:87], v[202:203], v[212:213] op_sel_hi:[0,1,1]
	v_fma_f32 v214, v86, v208, v214
	v_pk_fma_f32 v[210:211], v[216:217], v[52:53], v[210:211] op_sel:[1,0,0] neg_lo:[0,0,1] neg_hi:[0,0,1]
	v_pk_fma_f32 v[212:213], v[216:217], v[150:151], v[212:213] op_sel:[1,0,0] neg_lo:[0,0,1] neg_hi:[0,0,1]
	v_fma_f32 v214, v217, v152, -v214
	v_cmp_eq_u32_e64 s[10:11], 1, v219
	v_cmp_eq_u32_e64 s[14:15], 2, v219
	v_cmp_eq_u32_e64 s[20:21], 3, v219
	v_cmp_eq_u32_e64 s[22:23], 4, v219
	v_cmp_eq_u32_e64 s[30:31], 5, v219
	v_pk_add_f32 v[52:53], v[106:107], v[132:133]
	v_pk_add_f32 v[148:149], v[108:109], v[52:53]
	v_pk_add_f32 v[106:107], v[222:223], v[198:199]
	v_pk_add_f32 v[108:109], v[178:179], v[106:107]
	v_add_f32_e64 v150, v228, v204
	v_add_f32_e64 v152, v184, v150
	v_pk_add_f32 v[154:155], v[158:159], v[172:173]
	v_pk_add_f32 v[156:157], v[174:175], v[154:155]
	v_pk_add_f32 v[158:159], v[224:225], v[200:201]
	v_pk_add_f32 v[160:161], v[180:181], v[158:159]
	v_add_f32_e64 v162, v230, v206
	v_add_f32_e64 v164, v186, v162
	v_pk_add_f32 v[166:167], v[220:221], v[196:197]
	v_pk_add_f32 v[168:169], v[176:177], v[166:167]
	v_pk_add_f32 v[170:171], v[226:227], v[202:203]
	v_pk_add_f32 v[174:175], v[182:183], v[170:171]
	v_add_f32_e64 v176, v232, v208
	v_add_f32_e64 v178, v188, v176
	v_pk_add_f32 v[180:181], v[234:235], v[210:211]
	v_pk_add_f32 v[182:183], v[190:191], v[180:181]
	v_pk_add_f32 v[184:185], v[236:237], v[212:213]
	v_pk_add_f32 v[186:187], v[192:193], v[184:185]
	v_add_f32_e64 v188, v238, v214
	v_add_f32_e64 v190, v194, v188
	v_pk_fma_f32 v[192:193], v[56:57], v[148:149], v[182:183] op_sel_hi:[0,1,1]
	v_pk_fma_f32 v[194:195], v[56:57], v[108:109], v[186:187] op_sel_hi:[0,1,1]
	v_fma_f32 v220, v56, v152, v190
	v_pk_fma_f32 v[222:223], v[72:73], v[148:149], v[182:183] op_sel_hi:[0,1,1]
	v_pk_fma_f32 v[224:225], v[72:73], v[108:109], v[186:187] op_sel_hi:[0,1,1]
	v_fma_f32 v226, v72, v152, v190
	v_pk_fma_f32 v[192:193], v[56:57], v[156:157], v[192:193] op_sel:[1,0,0]
	v_pk_fma_f32 v[194:195], v[56:57], v[160:161], v[194:195] op_sel:[1,0,0]
	v_fma_f32 v220, v57, v164, v220
	v_pk_fma_f32 v[222:223], v[72:73], v[156:157], v[222:223] op_sel:[1,0,0]
	v_pk_fma_f32 v[224:225], v[72:73], v[160:161], v[224:225] op_sel:[1,0,0]
	v_fma_f32 v226, v73, v164, v226
	v_pk_fma_f32 v[192:193], v[58:59], v[168:169], v[192:193] op_sel_hi:[0,1,1]
	v_pk_fma_f32 v[194:195], v[58:59], v[174:175], v[194:195] op_sel_hi:[0,1,1]
	v_fma_f32 v220, v58, v178, v220
	v_pk_fma_f32 v[222:223], v[74:75], v[168:169], v[222:223] op_sel_hi:[0,1,1]
	v_pk_fma_f32 v[224:225], v[74:75], v[174:175], v[224:225] op_sel_hi:[0,1,1]
	v_fma_f32 v226, v74, v178, v226
	v_pk_fma_f32 v[182:183], v[32:33], v[148:149], v[182:183] op_sel_hi:[0,1,1]
	v_pk_fma_f32 v[186:187], v[32:33], v[108:109], v[186:187] op_sel_hi:[0,1,1]
	v_fma_f32 v190, v32, v152, v190
	v_pk_fma_f32 v[182:183], v[32:33], v[156:157], v[182:183] op_sel:[1,0,0]
	v_pk_fma_f32 v[186:187], v[32:33], v[160:161], v[186:187] op_sel:[1,0,0]
	v_fma_f32 v190, v33, v164, v190
	v_pk_fma_f32 v[182:183], v[34:35], v[168:169], v[182:183] op_sel_hi:[0,1,1]
	v_pk_fma_f32 v[186:187], v[34:35], v[174:175], v[186:187] op_sel_hi:[0,1,1]
	v_fma_f32 v190, v34, v178, v190
	v_cndmask_b32_e64 v228, 0, v1, s[10:11]
	v_cndmask_b32_e64 v229, 0, v1, s[14:15]
	v_cndmask_b32_e64 v230, 0, v1, s[20:21]
	v_cndmask_b32_e64 v231, 0, v1, s[22:23]
	v_cndmask_b32_e64 v232, 0, v1, s[30:31]
	v_add_f32_dpp v182, v192, v182 wave_shl:1 row_mask:0xf bank_mask:0xf bound_ctrl:1
	v_add_f32_dpp v183, v193, v183 wave_shl:1 row_mask:0xf bank_mask:0xf bound_ctrl:1
	v_add_f32_dpp v186, v194, v186 wave_shl:1 row_mask:0xf bank_mask:0xf bound_ctrl:1
	v_add_f32_dpp v187, v195, v187 wave_shl:1 row_mask:0xf bank_mask:0xf bound_ctrl:1
	v_add_f32_dpp v190, v220, v190 wave_shl:1 row_mask:0xf bank_mask:0xf bound_ctrl:1
	s_add_i32 s4, s34, 4
	s_cmpk_lt_i32 s4, 0x201
	s_cselect_b64 s[12:13], s[0:1], 0
	v_add_f32_dpp v182, v222, v182 wave_shr:1 row_mask:0xf bank_mask:0xf bound_ctrl:1
	v_add_f32_dpp v183, v223, v183 wave_shr:1 row_mask:0xf bank_mask:0xf bound_ctrl:1
	v_add_f32_dpp v186, v224, v186 wave_shr:1 row_mask:0xf bank_mask:0xf bound_ctrl:1
	v_add_f32_dpp v187, v225, v187 wave_shr:1 row_mask:0xf bank_mask:0xf bound_ctrl:1
	v_add_f32_dpp v190, v226, v190 wave_shr:1 row_mask:0xf bank_mask:0xf bound_ctrl:1
	v_pk_fma_f32 v[182:183], v[12:13], v[218:219], v[182:183] op_sel_hi:[1,0,1] neg_lo:[0,0,1] neg_hi:[0,0,1]
	v_pk_fma_f32 v[186:187], v[14:15], v[218:219], v[186:187] op_sel_hi:[1,0,1] neg_lo:[0,0,1] neg_hi:[0,0,1]
	v_fma_f32 v190, v16, v218, -v190
	v_pk_add_f32 v[182:183], v[182:183], v[228:229] neg_lo:[0,1] neg_hi:[0,1]
	v_pk_add_f32 v[186:187], v[186:187], v[230:231] neg_lo:[0,1] neg_hi:[0,1]
	v_add_f32_e64 v190, v190, -v232
	v_pk_mul_f32 v[234:235], v[182:183], v[182:183]
	v_pk_fma_f32 v[234:235], v[186:187], v[186:187], v[234:235]
	v_add_f32_e32 v234, v234, v235
	v_fma_f32 v234, v190, v190, v234
	v_cndmask_b32_e64 v235, 0, v234, s[12:13]
	v_add_f32_e32 v0, v0, v235
	s_add_i32 s4, s34, 9
	s_min_i32 s4, s4, 0x200
	s_mul_i32 s5, s4, 0x804
	s_add_i32 s5, s5, s35
	s_add_i32 s6, s5, 0x0
	s_add_i32 s7, s5, 0x101004
	s_add_i32 s8, s5, 0x202008
	s_add_i32 s11, s5, 0x30300c
	s_add_i32 s15, s5, 0x404010
	s_mul_i32 s9, s4, 0x180c
	s_add_i32 s9, s9, s33
	buffer_load_dword v12, v28, s[16:19], s6 offen nt
	buffer_load_dword v13, v28, s[16:19], s7 offen nt
	buffer_load_dword v14, v28, s[16:19], s8 offen nt
	buffer_load_dword v15, v28, s[16:19], s11 offen nt
	buffer_load_dword v16, v28, s[16:19], s15 offen nt
	buffer_load_dwordx3 v[32:34], v27, s[24:27], s9 offen nt
	s_waitcnt vmcnt(12)
	v_mov_b32_dpp v56, v64 wave_shr:1 row_mask:0xf bank_mask:0xf bound_ctrl:1
	v_mov_b32_dpp v57, v65 wave_shr:1 row_mask:0xf bank_mask:0xf bound_ctrl:1
	v_mov_b32_dpp v58, v66 wave_shr:1 row_mask:0xf bank_mask:0xf bound_ctrl:1
	v_mov_b32_dpp v72, v64 wave_shl:1 row_mask:0xf bank_mask:0xf bound_ctrl:1
	v_mov_b32_dpp v73, v65 wave_shl:1 row_mask:0xf bank_mask:0xf bound_ctrl:1
	v_mov_b32_dpp v74, v66 wave_shl:1 row_mask:0xf bank_mask:0xf bound_ctrl:1
	v_mov_b32_dpp v84, v54 wave_shr:1 row_mask:0xf bank_mask:0xf bound_ctrl:1
	v_mov_b32_dpp v85, v55 wave_shr:1 row_mask:0xf bank_mask:0xf bound_ctrl:1
	v_mov_b32_dpp v86, v60 wave_shr:1 row_mask:0xf bank_mask:0xf bound_ctrl:1
	v_mov_b32_dpp v87, v61 wave_shr:1 row_mask:0xf bank_mask:0xf bound_ctrl:1
	v_mov_b32_dpp v88, v62 wave_shr:1 row_mask:0xf bank_mask:0xf bound_ctrl:1
	v_mov_b32_dpp v90, v54 wave_shl:1 row_mask:0xf bank_mask:0xf bound_ctrl:1
	v_mov_b32_dpp v91, v55 wave_shl:1 row_mask:0xf bank_mask:0xf bound_ctrl:1
	v_mov_b32_dpp v108, v60 wave_shl:1 row_mask:0xf bank_mask:0xf bound_ctrl:1
	v_mov_b32_dpp v109, v61 wave_shl:1 row_mask:0xf bank_mask:0xf bound_ctrl:1
	v_mov_b32_dpp v148, v62 wave_shl:1 row_mask:0xf bank_mask:0xf bound_ctrl:1
	v_pk_mul_f32 v[152:153], v[54:55], v[64:65] op_sel_hi:[1,0]
	v_pk_mul_f32 v[156:157], v[60:61], v[64:65] op_sel_hi:[1,0]
	v_mul_f32_e64 v160, v62, v64
	v_pk_mul_f32 v[164:165], v[54:55], v[64:65] op_sel:[0,1]
	v_pk_mul_f32 v[168:169], v[60:61], v[64:65] op_sel:[0,1]
	v_mul_f32_e64 v174, v62, v65
	v_pk_mul_f32 v[178:179], v[54:55], v[66:67] op_sel_hi:[1,0]
	v_pk_mul_f32 v[182:183], v[60:61], v[66:67] op_sel_hi:[1,0]
	v_mul_f32_e64 v186, v62, v66
	v_pk_add_f32 v[190:191], v[54:55], v[84:85]
	v_pk_add_f32 v[192:193], v[60:61], v[86:87]
	v_add_f32_e64 v194, v62, v88
	v_pk_fma_f32 v[152:153], v[84:85], v[56:57], v[152:153] op_sel_hi:[1,0,1]
	v_pk_fma_f32 v[156:157], v[86:87], v[56:57], v[156:157] op_sel_hi:[1,0,1]
	v_fma_f32 v160, v88, v56, v160
	v_pk_fma_f32 v[164:165], v[84:85], v[56:57], v[164:165] op_sel:[0,1,0]
	v_pk_fma_f32 v[168:169], v[86:87], v[56:57], v[168:169] op_sel:[0,1,0]
	v_fma_f32 v174, v88, v57, v174
	v_pk_fma_f32 v[178:179], v[84:85], v[58:59], v[178:179] op_sel_hi:[1,0,1]
	v_pk_fma_f32 v[182:183], v[86:87], v[58:59], v[182:183] op_sel_hi:[1,0,1]
	v_fma_f32 v186, v88, v58, v186
	v_pk_add_f32 v[190:191], v[190:191], v[90:91]
	v_pk_add_f32 v[192:193], v[192:193], v[108:109]
	v_add_f32_e64 v194, v194, v148
	v_pk_fma_f32 v[152:153], v[90:91], v[72:73], v[152:153] op_sel_hi:[1,0,1]
	v_pk_fma_f32 v[156:157], v[108:109], v[72:73], v[156:157] op_sel_hi:[1,0,1]
	v_fma_f32 v160, v148, v72, v160
	v_pk_fma_f32 v[164:165], v[90:91], v[72:73], v[164:165] op_sel:[0,1,0]
	v_pk_fma_f32 v[168:169], v[108:109], v[72:73], v[168:169] op_sel:[0,1,0]
	v_fma_f32 v174, v148, v73, v174
	v_pk_fma_f32 v[178:179], v[90:91], v[74:75], v[178:179] op_sel_hi:[1,0,1]
	v_pk_fma_f32 v[182:183], v[108:109], v[74:75], v[182:183] op_sel_hi:[1,0,1]
	v_fma_f32 v186, v148, v74, v186
	s_barrier
	ds_read_b128 v[84:87], v23 offset:3072
	ds_read_b128 v[88:91], v23 offset:4096
	ds_read_b128 v[216:219], v23 offset:5120
	v_pk_add_f32 v[108:109], v[46:47], v[190:191]
	v_pk_add_f32 v[46:47], v[134:135], v[192:193]
	v_add_f32_e64 v134, v136, v194
	v_pk_add_f32 v[136:137], v[142:143], v[152:153]
	v_pk_add_f32 v[142:143], v[116:117], v[156:157]
	v_add_f32_e64 v116, v118, v160
	v_pk_add_f32 v[118:119], v[120:121], v[164:165]
	v_pk_add_f32 v[120:121], v[122:123], v[168:169]
	v_add_f32_e64 v122, v124, v174
	v_pk_add_f32 v[124:125], v[126:127], v[178:179]
	v_pk_add_f32 v[126:127], v[128:129], v[182:183]
	v_add_f32_e64 v128, v130, v186
	s_waitcnt lgkmcnt(2)
	v_pk_fma_f32 v[136:137], v[84:85], v[108:109], v[136:137] op_sel_hi:[0,1,1] neg_lo:[1,0,0] neg_hi:[1,0,0]
	v_pk_fma_f32 v[142:143], v[84:85], v[46:47], v[142:143] op_sel_hi:[0,1,1] neg_lo:[1,0,0] neg_hi:[1,0,0]
	v_fma_f32 v116, -v84, v134, v116
	v_pk_fma_f32 v[118:119], v[84:85], v[108:109], v[118:119] op_sel:[1,0,0] neg_lo:[1,0,0] neg_hi:[1,0,0]
	v_pk_fma_f32 v[120:121], v[84:85], v[46:47], v[120:121] op_sel:[1,0,0] neg_lo:[1,0,0] neg_hi:[1,0,0]
	v_fma_f32 v122, -v85, v134, v122
	v_pk_fma_f32 v[124:125], v[86:87], v[108:109], v[124:125] op_sel_hi:[0,1,1] neg_lo:[1,0,0] neg_hi:[1,0,0]
	v_pk_fma_f32 v[126:127], v[86:87], v[46:47], v[126:127] op_sel_hi:[0,1,1] neg_lo:[1,0,0] neg_hi:[1,0,0]
	v_fma_f32 v128, -v86, v134, v128
	v_pk_mul_f32 v[130:131], v[86:87], v[136:137] op_sel:[1,0]
	v_pk_mul_f32 v[222:223], v[86:87], v[142:143] op_sel:[1,0]
	v_mul_f32_e64 v228, v87, v116
	s_waitcnt lgkmcnt(1)
	v_pk_mul_f32 v[148:149], v[88:89], v[136:137] op_sel_hi:[0,1]
	v_pk_mul_f32 v[224:225], v[88:89], v[142:143] op_sel_hi:[0,1]
	v_mul_f32_e64 v230, v88, v116
	v_pk_mul_f32 v[220:221], v[88:89], v[136:137] op_sel:[1,0]
	v_pk_mul_f32 v[226:227], v[88:89], v[142:143] op_sel:[1,0]
	v_mul_f32_e64 v232, v89, v116
	v_pk_fma_f32 v[130:131], v[88:89], v[118:119], v[130:131] op_sel_hi:[0,1,1]
	v_pk_fma_f32 v[222:223], v[88:89], v[120:121], v[222:223] op_sel_hi:[0,1,1]
	v_fma_f32 v228, v88, v122, v228
	v_pk_fma_f32 v[148:149], v[90:91], v[118:119], v[148:149] op_sel_hi:[0,1,1]
	v_pk_fma_f32 v[224:225], v[90:91], v[120:121], v[224:225] op_sel_hi:[0,1,1]
	v_fma_f32 v230, v90, v122, v230
	v_pk_fma_f32 v[220:221], v[90:91], v[118:119], v[220:221] op_sel:[1,0,0]
	v_pk_fma_f32 v[226:227], v[90:91], v[120:121], v[226:227] op_sel:[1,0,0]
	v_fma_f32 v232, v91, v122, v232
	v_pk_fma_f32 v[130:131], v[88:89], v[124:125], v[130:131] op_sel:[1,0,0]
	v_pk_fma_f32 v[222:223], v[88:89], v[126:127], v[222:223] op_sel:[1,0,0]
	v_fma_f32 v228, v89, v128, v228
	v_pk_fma_f32 v[148:149], v[90:91], v[124:125], v[148:149] op_sel:[1,0,0]
	v_pk_fma_f32 v[224:225], v[90:91], v[126:127], v[224:225] op_sel:[1,0,0]
	v_fma_f32 v230, v91, v128, v230
	s_waitcnt lgkmcnt(0)
	v_pk_fma_f32 v[220:221], v[216:217], v[124:125], v[220:221] op_sel_hi:[0,1,1]
	v_pk_fma_f32 v[226:227], v[216:217], v[126:127], v[226:227] op_sel_hi:[0,1,1]
	v_fma_f32 v232, v216, v128, v232
	v_pk_mul_f32 v[234:235], v[84:85], v[130:131] op_sel_hi:[0,1]
	v_pk_mul_f32 v[236:237], v[84:85], v[222:223] op_sel_hi:[0,1]
	v_mul_f32_e64 v238, v84, v228
	v_pk_fma_f32 v[234:235], v[84:85], v[148:149], v[234:235] op_sel:[1,0,0]
	v_pk_fma_f32 v[236:237], v[84:85], v[224:225], v[236:237] op_sel:[1,0,0]
	v_fma_f32 v238, v85, v230, v238
	v_pk_fma_f32 v[234:235], v[86:87], v[220:221], v[234:235] op_sel_hi:[0,1,1]
	v_pk_fma_f32 v[236:237], v[86:87], v[226:227], v[236:237] op_sel_hi:[0,1,1]
	v_fma_f32 v238, v86, v232, v238
	v_pk_fma_f32 v[234:235], v[216:217], v[108:109], v[234:235] op_sel:[1,0,0] neg_lo:[0,0,1] neg_hi:[0,0,1]
	v_pk_fma_f32 v[236:237], v[216:217], v[46:47], v[236:237] op_sel:[1,0,0] neg_lo:[0,0,1] neg_hi:[0,0,1]
	v_fma_f32 v238, v217, v134, -v238
	v_cmp_eq_u32_e64 s[10:11], 1, v219
	v_cmp_eq_u32_e64 s[14:15], 2, v219
	v_cmp_eq_u32_e64 s[20:21], 3, v219
	v_cmp_eq_u32_e64 s[22:23], 4, v219
	v_cmp_eq_u32_e64 s[30:31], 5, v219
	v_pk_add_f32 v[46:47], v[52:53], v[130:131]
	v_pk_add_f32 v[52:53], v[106:107], v[222:223]
	v_add_f32_e64 v106, v150, v228
	v_pk_add_f32 v[108:109], v[154:155], v[148:149]
	v_pk_add_f32 v[116:117], v[158:159], v[224:225]
	v_add_f32_e64 v118, v162, v230
	v_pk_add_f32 v[120:121], v[166:167], v[220:221]
	v_pk_add_f32 v[122:123], v[170:171], v[226:227]
	v_add_f32_e64 v124, v176, v232
	v_pk_add_f32 v[126:127], v[180:181], v[234:235]
	v_pk_add_f32 v[128:129], v[184:185], v[236:237]
	v_add_f32_e64 v134, v188, v238
	v_pk_fma_f32 v[136:137], v[76:77], v[46:47], v[126:127] op_sel_hi:[0,1,1]
	v_pk_fma_f32 v[142:143], v[76:77], v[52:53], v[128:129] op_sel_hi:[0,1,1]
	v_fma_f32 v150, v76, v106, v134
	v_pk_fma_f32 v[154:155], v[92:93], v[46:47], v[126:127] op_sel_hi:[0,1,1]
	v_pk_fma_f32 v[158:159], v[92:93], v[52:53], v[128:129] op_sel_hi:[0,1,1]
	v_fma_f32 v162, v92, v106, v134
	v_pk_fma_f32 v[136:137], v[76:77], v[108:109], v[136:137] op_sel:[1,0,0]
	v_pk_fma_f32 v[142:143], v[76:77], v[116:117], v[142:143] op_sel:[1,0,0]
	v_fma_f32 v150, v77, v118, v150
	v_pk_fma_f32 v[154:155], v[92:93], v[108:109], v[154:155] op_sel:[1,0,0]
	v_pk_fma_f32 v[158:159], v[92:93], v[116:117], v[158:159] op_sel:[1,0,0]
	v_fma_f32 v162, v93, v118, v162
	v_pk_fma_f32 v[136:137], v[78:79], v[120:121], v[136:137] op_sel_hi:[0,1,1]
	v_pk_fma_f32 v[142:143], v[78:79], v[122:123], v[142:143] op_sel_hi:[0,1,1]
	v_fma_f32 v150, v78, v124, v150
	v_pk_fma_f32 v[154:155], v[94:95], v[120:121], v[154:155] op_sel_hi:[0,1,1]
	v_pk_fma_f32 v[158:159], v[94:95], v[122:123], v[158:159] op_sel_hi:[0,1,1]
	v_fma_f32 v162, v94, v124, v162
	v_pk_fma_f32 v[126:127], v[36:37], v[46:47], v[126:127] op_sel_hi:[0,1,1]
	v_pk_fma_f32 v[128:129], v[36:37], v[52:53], v[128:129] op_sel_hi:[0,1,1]
	v_fma_f32 v134, v36, v106, v134
	v_pk_fma_f32 v[126:127], v[36:37], v[108:109], v[126:127] op_sel:[1,0,0]
	v_pk_fma_f32 v[128:129], v[36:37], v[116:117], v[128:129] op_sel:[1,0,0]
	v_fma_f32 v134, v37, v118, v134
	v_pk_fma_f32 v[126:127], v[38:39], v[120:121], v[126:127] op_sel_hi:[0,1,1]
	v_pk_fma_f32 v[128:129], v[38:39], v[122:123], v[128:129] op_sel_hi:[0,1,1]
	v_fma_f32 v134, v38, v124, v134
	v_cndmask_b32_e64 v166, 0, v1, s[10:11]
	v_cndmask_b32_e64 v167, 0, v1, s[14:15]
	v_cndmask_b32_e64 v170, 0, v1, s[20:21]
	v_cndmask_b32_e64 v171, 0, v1, s[22:23]
	v_cndmask_b32_e64 v176, 0, v1, s[30:31]
	v_add_f32_dpp v126, v136, v126 wave_shl:1 row_mask:0xf bank_mask:0xf bound_ctrl:1
	v_add_f32_dpp v127, v137, v127 wave_shl:1 row_mask:0xf bank_mask:0xf bound_ctrl:1
	v_add_f32_dpp v128, v142, v128 wave_shl:1 row_mask:0xf bank_mask:0xf bound_ctrl:1
	v_add_f32_dpp v129, v143, v129 wave_shl:1 row_mask:0xf bank_mask:0xf bound_ctrl:1
	v_add_f32_dpp v134, v150, v134 wave_shl:1 row_mask:0xf bank_mask:0xf bound_ctrl:1
	s_add_i32 s4, s34, 5
	s_cmpk_lt_i32 s4, 0x201
	s_cselect_b64 s[12:13], s[0:1], 0
	v_add_f32_dpp v126, v154, v126 wave_shr:1 row_mask:0xf bank_mask:0xf bound_ctrl:1
	v_add_f32_dpp v127, v155, v127 wave_shr:1 row_mask:0xf bank_mask:0xf bound_ctrl:1
	v_add_f32_dpp v128, v158, v128 wave_shr:1 row_mask:0xf bank_mask:0xf bound_ctrl:1
	v_add_f32_dpp v129, v159, v129 wave_shr:1 row_mask:0xf bank_mask:0xf bound_ctrl:1
	v_add_f32_dpp v134, v162, v134 wave_shr:1 row_mask:0xf bank_mask:0xf bound_ctrl:1
	v_pk_fma_f32 v[126:127], v[20:21], v[218:219], v[126:127] op_sel_hi:[1,0,1] neg_lo:[0,0,1] neg_hi:[0,0,1]
	v_pk_fma_f32 v[128:129], v[24:25], v[218:219], v[128:129] op_sel_hi:[1,0,1] neg_lo:[0,0,1] neg_hi:[0,0,1]
	v_fma_f32 v134, v30, v218, -v134
	v_pk_add_f32 v[126:127], v[126:127], v[166:167] neg_lo:[0,1] neg_hi:[0,1]
	v_pk_add_f32 v[128:129], v[128:129], v[170:171] neg_lo:[0,1] neg_hi:[0,1]
	v_add_f32_e64 v134, v134, -v176
	v_pk_mul_f32 v[180:181], v[126:127], v[126:127]
	v_pk_fma_f32 v[180:181], v[128:129], v[128:129], v[180:181]
	v_add_f32_e32 v180, v180, v181
	v_fma_f32 v180, v134, v134, v180
	v_cndmask_b32_e64 v181, 0, v180, s[12:13]
	v_add_f32_e32 v0, v0, v181
	s_add_i32 s4, s34, 10
	s_min_i32 s4, s4, 0x200
	s_mul_i32 s5, s4, 0x804
	s_add_i32 s5, s5, s35
	s_add_i32 s6, s5, 0x0
	s_add_i32 s7, s5, 0x101004
	s_add_i32 s8, s5, 0x202008
	s_add_i32 s11, s5, 0x30300c
	s_add_i32 s15, s5, 0x404010
	s_mul_i32 s9, s4, 0x180c
	s_add_i32 s9, s9, s33
	buffer_load_dword v20, v28, s[16:19], s6 offen nt
	buffer_load_dword v21, v28, s[16:19], s7 offen nt
	buffer_load_dword v24, v28, s[16:19], s8 offen nt
	buffer_load_dword v25, v28, s[16:19], s11 offen nt
	buffer_load_dword v30, v28, s[16:19], s15 offen nt
	buffer_load_dwordx3 v[36:38], v27, s[24:27], s9 offen nt
	s_waitcnt vmcnt(12)
	v_mov_b32_dpp v76, v8 wave_shr:1 row_mask:0xf bank_mask:0xf bound_ctrl:1
	v_mov_b32_dpp v77, v9 wave_shr:1 row_mask:0xf bank_mask:0xf bound_ctrl:1
	v_mov_b32_dpp v78, v10 wave_shr:1 row_mask:0xf bank_mask:0xf bound_ctrl:1
	v_mov_b32_dpp v84, v8 wave_shl:1 row_mask:0xf bank_mask:0xf bound_ctrl:1
	v_mov_b32_dpp v85, v9 wave_shl:1 row_mask:0xf bank_mask:0xf bound_ctrl:1
	v_mov_b32_dpp v86, v10 wave_shl:1 row_mask:0xf bank_mask:0xf bound_ctrl:1
	v_mov_b32_dpp v46, v2 wave_shr:1 row_mask:0xf bank_mask:0xf bound_ctrl:1
	v_mov_b32_dpp v47, v3 wave_shr:1 row_mask:0xf bank_mask:0xf bound_ctrl:1
	v_mov_b32_dpp v52, v4 wave_shr:1 row_mask:0xf bank_mask:0xf bound_ctrl:1
	v_mov_b32_dpp v53, v5 wave_shr:1 row_mask:0xf bank_mask:0xf bound_ctrl:1
	v_mov_b32_dpp v88, v6 wave_shr:1 row_mask:0xf bank_mask:0xf bound_ctrl:1
	v_mov_b32_dpp v90, v2 wave_shl:1 row_mask:0xf bank_mask:0xf bound_ctrl:1
	v_mov_b32_dpp v91, v3 wave_shl:1 row_mask:0xf bank_mask:0xf bound_ctrl:1
	v_mov_b32_dpp v92, v4 wave_shl:1 row_mask:0xf bank_mask:0xf bound_ctrl:1
	v_mov_b32_dpp v93, v5 wave_shl:1 row_mask:0xf bank_mask:0xf bound_ctrl:1
	v_mov_b32_dpp v94, v6 wave_shl:1 row_mask:0xf bank_mask:0xf bound_ctrl:1
	v_pk_mul_f32 v[106:107], v[2:3], v[8:9] op_sel_hi:[1,0]
	v_pk_mul_f32 v[108:109], v[4:5], v[8:9] op_sel_hi:[1,0]
	v_mul_f32_e64 v116, v6, v8
	v_pk_mul_f32 v[118:119], v[2:3], v[8:9] op_sel:[0,1]
	v_pk_mul_f32 v[120:121], v[4:5], v[8:9] op_sel:[0,1]
	v_mul_f32_e64 v122, v6, v9
	v_pk_mul_f32 v[124:125], v[2:3], v[10:11] op_sel_hi:[1,0]
	v_pk_mul_f32 v[126:127], v[4:5], v[10:11] op_sel_hi:[1,0]
	v_mul_f32_e64 v128, v6, v10
	v_pk_add_f32 v[134:135], v[2:3], v[46:47]
	v_pk_add_f32 v[136:137], v[4:5], v[52:53]
	v_add_f32_e64 v142, v6, v88
	v_pk_fma_f32 v[106:107], v[46:47], v[76:77], v[106:107] op_sel_hi:[1,0,1]
	v_pk_fma_f32 v[108:109], v[52:53], v[76:77], v[108:109] op_sel_hi:[1,0,1]
	v_fma_f32 v116, v88, v76, v116
	v_pk_fma_f32 v[118:119], v[46:47], v[76:77], v[118:119] op_sel:[0,1,0]
	v_pk_fma_f32 v[120:121], v[52:53], v[76:77], v[120:121] op_sel:[0,1,0]
	v_fma_f32 v122, v88, v77, v122
	v_pk_fma_f32 v[124:125], v[46:47], v[78:79], v[124:125] op_sel_hi:[1,0,1]
	v_pk_fma_f32 v[126:127], v[52:53], v[78:79], v[126:127] op_sel_hi:[1,0,1]
	v_fma_f32 v128, v88, v78, v128
	v_pk_add_f32 v[134:135], v[134:135], v[90:91]
	v_pk_add_f32 v[136:137], v[136:137], v[92:93]
	v_add_f32_e64 v142, v142, v94
	v_pk_fma_f32 v[106:107], v[90:91], v[84:85], v[106:107] op_sel_hi:[1,0,1]
	v_pk_fma_f32 v[108:109], v[92:93], v[84:85], v[108:109] op_sel_hi:[1,0,1]
	v_fma_f32 v116, v94, v84, v116
	v_pk_fma_f32 v[118:119], v[90:91], v[84:85], v[118:119] op_sel:[0,1,0]
	v_pk_fma_f32 v[120:121], v[92:93], v[84:85], v[120:121] op_sel:[0,1,0]
	v_fma_f32 v122, v94, v85, v122
	v_pk_fma_f32 v[124:125], v[90:91], v[86:87], v[124:125] op_sel_hi:[1,0,1]
	v_pk_fma_f32 v[126:127], v[92:93], v[86:87], v[126:127] op_sel_hi:[1,0,1]
	v_fma_f32 v128, v94, v86, v128
	s_barrier
	ds_read_b128 v[88:91], v23 offset:0
	ds_read_b128 v[92:95], v23 offset:1024
	ds_read_b128 v[216:219], v23 offset:2048
	v_pk_add_f32 v[46:47], v[190:191], v[134:135]
	v_pk_add_f32 v[52:53], v[140:141], v[46:47]
	v_pk_add_f32 v[140:141], v[192:193], v[136:137]
	v_pk_add_f32 v[150:151], v[144:145], v[140:141]
	v_add_f32_e64 v144, v194, v142
	v_add_f32_e64 v154, v146, v144
	v_pk_add_f32 v[146:147], v[152:153], v[106:107]
	v_pk_add_f32 v[158:159], v[96:97], v[146:147]
	v_pk_add_f32 v[96:97], v[156:157], v[108:109]
	v_pk_add_f32 v[152:153], v[98:99], v[96:97]
	v_add_f32_e64 v98, v160, v116
	v_add_f32_e64 v156, v100, v98
	v_pk_add_f32 v[100:101], v[164:165], v[118:119]
	v_pk_add_f32 v[160:161], v[102:103], v[100:101]
	v_pk_add_f32 v[102:103], v[168:169], v[120:121]
	v_pk_add_f32 v[162:163], v[104:105], v[102:103]
	v_add_f32_e64 v104, v174, v122
	v_add_f32_e64 v164, v110, v104
	v_pk_add_f32 v[110:111], v[178:179], v[124:125]
	v_pk_add_f32 v[166:167], v[112:113], v[110:111]
	v_pk_add_f32 v[112:113], v[182:183], v[126:127]
	v_pk_add_f32 v[168:169], v[114:115], v[112:113]
	v_add_f32_e64 v114, v186, v128
	v_add_f32_e64 v170, v138, v114
	s_waitcnt lgkmcnt(2)
	v_pk_fma_f32 v[158:159], v[88:89], v[52:53], v[158:159] op_sel_hi:[0,1,1] neg_lo:[1,0,0] neg_hi:[1,0,0]
	v_pk_fma_f32 v[152:153], v[88:89], v[150:151], v[152:153] op_sel_hi:[0,1,1] neg_lo:[1,0,0] neg_hi:[1,0,0]
	v_fma_f32 v156, -v88, v154, v156
	v_pk_fma_f32 v[160:161], v[88:89], v[52:53], v[160:161] op_sel:[1,0,0] neg_lo:[1,0,0] neg_hi:[1,0,0]
	v_pk_fma_f32 v[162:163], v[88:89], v[150:151], v[162:163] op_sel:[1,0,0] neg_lo:[1,0,0] neg_hi:[1,0,0]
	v_fma_f32 v164, -v89, v154, v164
	v_pk_fma_f32 v[166:167], v[90:91], v[52:53], v[166:167] op_sel_hi:[0,1,1] neg_lo:[1,0,0] neg_hi:[1,0,0]
	v_pk_fma_f32 v[168:169], v[90:91], v[150:151], v[168:169] op_sel_hi:[0,1,1] neg_lo:[1,0,0] neg_hi:[1,0,0]
	v_fma_f32 v170, -v90, v154, v170
	v_pk_mul_f32 v[138:139], v[90:91], v[158:159] op_sel:[1,0]
	v_pk_mul_f32 v[178:179], v[90:91], v[152:153] op_sel:[1,0]
	v_mul_f32_e64 v184, v91, v156
	s_waitcnt lgkmcnt(1)
	v_pk_mul_f32 v[174:175], v[92:93], v[158:159] op_sel_hi:[0,1]
	v_pk_mul_f32 v[180:181], v[92:93], v[152:153] op_sel_hi:[0,1]
	v_mul_f32_e64 v186, v92, v156
	v_pk_mul_f32 v[176:177], v[92:93], v[158:159] op_sel:[1,0]
	v_pk_mul_f32 v[182:183], v[92:93], v[152:153] op_sel:[1,0]
	v_mul_f32_e64 v188, v93, v156
	v_pk_fma_f32 v[138:139], v[92:93], v[160:161], v[138:139] op_sel_hi:[0,1,1]
	v_pk_fma_f32 v[178:179], v[92:93], v[162:163], v[178:179] op_sel_hi:[0,1,1]
	v_fma_f32 v184, v92, v164, v184
	v_pk_fma_f32 v[174:175], v[94:95], v[160:161], v[174:175] op_sel_hi:[0,1,1]
	v_pk_fma_f32 v[180:181], v[94:95], v[162:163], v[180:181] op_sel_hi:[0,1,1]
	v_fma_f32 v186, v94, v164, v186
	v_pk_fma_f32 v[176:177], v[94:95], v[160:161], v[176:177] op_sel:[1,0,0]
	v_pk_fma_f32 v[182:183], v[94:95], v[162:163], v[182:183] op_sel:[1,0,0]
	v_fma_f32 v188, v95, v164, v188
	v_pk_fma_f32 v[138:139], v[92:93], v[166:167], v[138:139] op_sel:[1,0,0]
	v_pk_fma_f32 v[178:179], v[92:93], v[168:169], v[178:179] op_sel:[1,0,0]
	v_fma_f32 v184, v93, v170, v184
	v_pk_fma_f32 v[174:175], v[94:95], v[166:167], v[174:175] op_sel:[1,0,0]
	v_pk_fma_f32 v[180:181], v[94:95], v[168:169], v[180:181] op_sel:[1,0,0]
	v_fma_f32 v186, v95, v170, v186
	s_waitcnt lgkmcnt(0)
	v_pk_fma_f32 v[176:177], v[216:217], v[166:167], v[176:177] op_sel_hi:[0,1,1]
	v_pk_fma_f32 v[182:183], v[216:217], v[168:169], v[182:183] op_sel_hi:[0,1,1]
	v_fma_f32 v188, v216, v170, v188
	v_pk_mul_f32 v[190:191], v[88:89], v[138:139] op_sel_hi:[0,1]
	v_pk_mul_f32 v[192:193], v[88:89], v[178:179] op_sel_hi:[0,1]
	v_mul_f32_e64 v194, v88, v184
	v_pk_fma_f32 v[190:191], v[88:89], v[174:175], v[190:191] op_sel:[1,0,0]
	v_pk_fma_f32 v[192:193], v[88:89], v[180:181], v[192:193] op_sel:[1,0,0]
	v_fma_f32 v194, v89, v186, v194
	v_pk_fma_f32 v[190:191], v[90:91], v[176:177], v[190:191] op_sel_hi:[0,1,1]
	v_pk_fma_f32 v[192:193], v[90:91], v[182:183], v[192:193] op_sel_hi:[0,1,1]
	v_fma_f32 v194, v90, v188, v194
	v_pk_fma_f32 v[190:191], v[216:217], v[52:53], v[190:191] op_sel:[1,0,0] neg_lo:[0,0,1] neg_hi:[0,0,1]
	v_pk_fma_f32 v[192:193], v[216:217], v[150:151], v[192:193] op_sel:[1,0,0] neg_lo:[0,0,1] neg_hi:[0,0,1]
	v_fma_f32 v194, v217, v154, -v194
	v_cmp_eq_u32_e64 s[10:11], 1, v219
	v_cmp_eq_u32_e64 s[14:15], 2, v219
	v_cmp_eq_u32_e64 s[20:21], 3, v219
	v_cmp_eq_u32_e64 s[22:23], 4, v219
	v_cmp_eq_u32_e64 s[30:31], 5, v219
	v_pk_add_f32 v[52:53], v[130:131], v[138:139]
	v_pk_add_f32 v[150:151], v[132:133], v[52:53]
	v_pk_add_f32 v[130:131], v[222:223], v[178:179]
	v_pk_add_f32 v[132:133], v[198:199], v[130:131]
	v_add_f32_e64 v152, v228, v184
	v_add_f32_e64 v154, v204, v152
	v_pk_add_f32 v[156:157], v[148:149], v[174:175]
	v_pk_add_f32 v[158:159], v[172:173], v[156:157]
	v_pk_add_f32 v[148:149], v[224:225], v[180:181]
	v_pk_add_f32 v[160:161], v[200:201], v[148:149]
	v_add_f32_e64 v162, v230, v186
	v_add_f32_e64 v164, v206, v162
	v_pk_add_f32 v[166:167], v[220:221], v[176:177]
	v_pk_add_f32 v[168:169], v[196:197], v[166:167]
	v_pk_add_f32 v[170:171], v[226:227], v[182:183]
	v_pk_add_f32 v[172:173], v[202:203], v[170:171]
	v_add_f32_e64 v196, v232, v188
	v_add_f32_e64 v198, v208, v196
	v_pk_add_f32 v[200:201], v[234:235], v[190:191]
	v_pk_add_f32 v[202:203], v[210:211], v[200:201]
	v_pk_add_f32 v[204:205], v[236:237], v[192:193]
	v_pk_add_f32 v[206:207], v[212:213], v[204:205]
	v_add_f32_e64 v208, v238, v194
	v_add_f32_e64 v210, v214, v208
	v_pk_fma_f32 v[212:213], v[68:69], v[150:151], v[202:203] op_sel_hi:[0,1,1]
	v_pk_fma_f32 v[214:215], v[68:69], v[132:133], v[206:207] op_sel_hi:[0,1,1]
	v_fma_f32 v220, v68, v154, v210
	v_pk_fma_f32 v[222:223], v[80:81], v[150:151], v[202:203] op_sel_hi:[0,1,1]
	v_pk_fma_f32 v[224:225], v[80:81], v[132:133], v[206:207] op_sel_hi:[0,1,1]
	v_fma_f32 v226, v80, v154, v210
	v_pk_fma_f32 v[212:213], v[68:69], v[158:159], v[212:213] op_sel:[1,0,0]
	v_pk_fma_f32 v[214:215], v[68:69], v[160:161], v[214:215] op_sel:[1,0,0]
	v_fma_f32 v220, v69, v164, v220
	v_pk_fma_f32 v[222:223], v[80:81], v[158:159], v[222:223] op_sel:[1,0,0]
	v_pk_fma_f32 v[224:225], v[80:81], v[160:161], v[224:225] op_sel:[1,0,0]
	v_fma_f32 v226, v81, v164, v226
	v_pk_fma_f32 v[212:213], v[70:71], v[168:169], v[212:213] op_sel_hi:[0,1,1]
	v_pk_fma_f32 v[214:215], v[70:71], v[172:173], v[214:215] op_sel_hi:[0,1,1]
	v_fma_f32 v220, v70, v198, v220
	v_pk_fma_f32 v[222:223], v[82:83], v[168:169], v[222:223] op_sel_hi:[0,1,1]
	v_pk_fma_f32 v[224:225], v[82:83], v[172:173], v[224:225] op_sel_hi:[0,1,1]
	v_fma_f32 v226, v82, v198, v226
	v_pk_fma_f32 v[202:203], v[48:49], v[150:151], v[202:203] op_sel_hi:[0,1,1]
	v_pk_fma_f32 v[206:207], v[48:49], v[132:133], v[206:207] op_sel_hi:[0,1,1]
	v_fma_f32 v210, v48, v154, v210
	v_pk_fma_f32 v[202:203], v[48:49], v[158:159], v[202:203] op_sel:[1,0,0]
	v_pk_fma_f32 v[206:207], v[48:49], v[160:161], v[206:207] op_sel:[1,0,0]
	v_fma_f32 v210, v49, v164, v210
	v_pk_fma_f32 v[202:203], v[50:51], v[168:169], v[202:203] op_sel_hi:[0,1,1]
	v_pk_fma_f32 v[206:207], v[50:51], v[172:173], v[206:207] op_sel_hi:[0,1,1]
	v_fma_f32 v210, v50, v198, v210
	v_cndmask_b32_e64 v228, 0, v1, s[10:11]
	v_cndmask_b32_e64 v229, 0, v1, s[14:15]
	v_cndmask_b32_e64 v230, 0, v1, s[20:21]
	v_cndmask_b32_e64 v231, 0, v1, s[22:23]
	v_cndmask_b32_e64 v232, 0, v1, s[30:31]
	v_add_f32_dpp v202, v212, v202 wave_shl:1 row_mask:0xf bank_mask:0xf bound_ctrl:1
	v_add_f32_dpp v203, v213, v203 wave_shl:1 row_mask:0xf bank_mask:0xf bound_ctrl:1
	v_add_f32_dpp v206, v214, v206 wave_shl:1 row_mask:0xf bank_mask:0xf bound_ctrl:1
	v_add_f32_dpp v207, v215, v207 wave_shl:1 row_mask:0xf bank_mask:0xf bound_ctrl:1
	v_add_f32_dpp v210, v220, v210 wave_shl:1 row_mask:0xf bank_mask:0xf bound_ctrl:1
	s_add_i32 s4, s34, 6
	s_cmpk_lt_i32 s4, 0x201
	s_cselect_b64 s[12:13], s[0:1], 0
	v_add_f32_dpp v202, v222, v202 wave_shr:1 row_mask:0xf bank_mask:0xf bound_ctrl:1
	v_add_f32_dpp v203, v223, v203 wave_shr:1 row_mask:0xf bank_mask:0xf bound_ctrl:1
	v_add_f32_dpp v206, v224, v206 wave_shr:1 row_mask:0xf bank_mask:0xf bound_ctrl:1
	v_add_f32_dpp v207, v225, v207 wave_shr:1 row_mask:0xf bank_mask:0xf bound_ctrl:1
	v_add_f32_dpp v210, v226, v210 wave_shr:1 row_mask:0xf bank_mask:0xf bound_ctrl:1
	v_pk_fma_f32 v[202:203], v[40:41], v[218:219], v[202:203] op_sel_hi:[1,0,1] neg_lo:[0,0,1] neg_hi:[0,0,1]
	v_pk_fma_f32 v[206:207], v[42:43], v[218:219], v[206:207] op_sel_hi:[1,0,1] neg_lo:[0,0,1] neg_hi:[0,0,1]
	v_fma_f32 v210, v44, v218, -v210
	v_pk_add_f32 v[202:203], v[202:203], v[228:229] neg_lo:[0,1] neg_hi:[0,1]
	v_pk_add_f32 v[206:207], v[206:207], v[230:231] neg_lo:[0,1] neg_hi:[0,1]
	v_add_f32_e64 v210, v210, -v232
	v_pk_mul_f32 v[234:235], v[202:203], v[202:203]
	v_pk_fma_f32 v[234:235], v[206:207], v[206:207], v[234:235]
	v_add_f32_e32 v234, v234, v235
	v_fma_f32 v234, v210, v210, v234
	v_cndmask_b32_e64 v235, 0, v234, s[12:13]
	v_add_f32_e32 v0, v0, v235
	s_add_i32 s4, s34, 11
	s_min_i32 s4, s4, 0x200
	s_mul_i32 s5, s4, 0x804
	s_add_i32 s5, s5, s35
	s_add_i32 s6, s5, 0x0
	s_add_i32 s7, s5, 0x101004
	s_add_i32 s8, s5, 0x202008
	s_add_i32 s11, s5, 0x30300c
	s_add_i32 s15, s5, 0x404010
	s_mul_i32 s9, s4, 0x180c
	s_add_i32 s9, s9, s33
	buffer_load_dword v40, v28, s[16:19], s6 offen nt
	buffer_load_dword v41, v28, s[16:19], s7 offen nt
	buffer_load_dword v42, v28, s[16:19], s8 offen nt
	buffer_load_dword v43, v28, s[16:19], s11 offen nt
	buffer_load_dword v44, v28, s[16:19], s15 offen nt
	buffer_load_dwordx3 v[48:50], v27, s[24:27], s9 offen nt
	s_waitcnt vmcnt(12)
	v_mov_b32_dpp v68, v32 wave_shr:1 row_mask:0xf bank_mask:0xf bound_ctrl:1
	v_mov_b32_dpp v69, v33 wave_shr:1 row_mask:0xf bank_mask:0xf bound_ctrl:1
	v_mov_b32_dpp v70, v34 wave_shr:1 row_mask:0xf bank_mask:0xf bound_ctrl:1
	v_mov_b32_dpp v80, v32 wave_shl:1 row_mask:0xf bank_mask:0xf bound_ctrl:1
	v_mov_b32_dpp v81, v33 wave_shl:1 row_mask:0xf bank_mask:0xf bound_ctrl:1
	v_mov_b32_dpp v82, v34 wave_shl:1 row_mask:0xf bank_mask:0xf bound_ctrl:1
	v_mov_b32_dpp v88, v12 wave_shr:1 row_mask:0xf bank_mask:0xf bound_ctrl:1
	v_mov_b32_dpp v89, v13 wave_shr:1 row_mask:0xf bank_mask:0xf bound_ctrl:1
	v_mov_b32_dpp v90, v14 wave_shr:1 row_mask:0xf bank_mask:0xf bound_ctrl:1
	v_mov_b32_dpp v91, v15 wave_shr:1 row_mask:0xf bank_mask:0xf bound_ctrl:1
	v_mov_b32_dpp v92, v16 wave_shr:1 row_mask:0xf bank_mask:0xf bound_ctrl:1
	v_mov_b32_dpp v94, v12 wave_shl:1 row_mask:0xf bank_mask:0xf bound_ctrl:1
	v_mov_b32_dpp v95, v13 wave_shl:1 row_mask:0xf bank_mask:0xf bound_ctrl:1
	v_mov_b32_dpp v132, v14 wave_shl:1 row_mask:0xf bank_mask:0xf bound_ctrl:1
	v_mov_b32_dpp v133, v15 wave_shl:1 row_mask:0xf bank_mask:0xf bound_ctrl:1
	v_mov_b32_dpp v150, v16 wave_shl:1 row_mask:0xf bank_mask:0xf bound_ctrl:1
	v_pk_mul_f32 v[154:155], v[12:13], v[32:33] op_sel_hi:[1,0]
	v_pk_mul_f32 v[158:159], v[14:15], v[32:33] op_sel_hi:[1,0]
	v_mul_f32_e64 v160, v16, v32
	v_pk_mul_f32 v[164:165], v[12:13], v[32:33] op_sel:[0,1]
	v_pk_mul_f32 v[168:169], v[14:15], v[32:33] op_sel:[0,1]
	v_mul_f32_e64 v172, v16, v33
	v_pk_mul_f32 v[198:199], v[12:13], v[34:35] op_sel_hi:[1,0]
	v_pk_mul_f32 v[202:203], v[14:15], v[34:35] op_sel_hi:[1,0]
	v_mul_f32_e64 v206, v16, v34
	v_pk_add_f32 v[210:211], v[12:13], v[88:89]
	v_pk_add_f32 v[212:213], v[14:15], v[90:91]
	v_add_f32_e64 v214, v16, v92
	v_pk_fma_f32 v[154:155], v[88:89], v[68:69], v[154:155] op_sel_hi:[1,0,1]
	v_pk_fma_f32 v[158:159], v[90:91], v[68:69], v[158:159] op_sel_hi:[1,0,1]
	v_fma_f32 v160, v92, v68, v160
	v_pk_fma_f32 v[164:165], v[88:89], v[68:69], v[164:165] op_sel:[0,1,0]
	v_pk_fma_f32 v[168:169], v[90:91], v[68:69], v[168:169] op_sel:[0,1,0]
	v_fma_f32 v172, v92, v69, v172
	v_pk_fma_f32 v[198:199], v[88:89], v[70:71], v[198:199] op_sel_hi:[1,0,1]
	v_pk_fma_f32 v[202:203], v[90:91], v[70:71], v[202:203] op_sel_hi:[1,0,1]
	v_fma_f32 v206, v92, v70, v206
	v_pk_add_f32 v[210:211], v[210:211], v[94:95]
	v_pk_add_f32 v[212:213], v[212:213], v[132:133]
	v_add_f32_e64 v214, v214, v150
	v_pk_fma_f32 v[154:155], v[94:95], v[80:81], v[154:155] op_sel_hi:[1,0,1]
	v_pk_fma_f32 v[158:159], v[132:133], v[80:81], v[158:159] op_sel_hi:[1,0,1]
	v_fma_f32 v160, v150, v80, v160
	v_pk_fma_f32 v[164:165], v[94:95], v[80:81], v[164:165] op_sel:[0,1,0]
	v_pk_fma_f32 v[168:169], v[132:133], v[80:81], v[168:169] op_sel:[0,1,0]
	v_fma_f32 v172, v150, v81, v172
	v_pk_fma_f32 v[198:199], v[94:95], v[82:83], v[198:199] op_sel_hi:[1,0,1]
	v_pk_fma_f32 v[202:203], v[132:133], v[82:83], v[202:203] op_sel_hi:[1,0,1]
	v_fma_f32 v206, v150, v82, v206
	s_barrier
	ds_read_b128 v[88:91], v23 offset:3072
	ds_read_b128 v[92:95], v23 offset:4096
	ds_read_b128 v[216:219], v23 offset:5120
	v_pk_add_f32 v[132:133], v[46:47], v[210:211]
	v_pk_add_f32 v[46:47], v[140:141], v[212:213]
	v_add_f32_e64 v140, v144, v214
	v_pk_add_f32 v[144:145], v[146:147], v[154:155]
	v_pk_add_f32 v[146:147], v[96:97], v[158:159]
	v_add_f32_e64 v96, v98, v160
	v_pk_add_f32 v[98:99], v[100:101], v[164:165]
	v_pk_add_f32 v[100:101], v[102:103], v[168:169]
	v_add_f32_e64 v102, v104, v172
	v_pk_add_f32 v[104:105], v[110:111], v[198:199]
	v_pk_add_f32 v[110:111], v[112:113], v[202:203]
	v_add_f32_e64 v112, v114, v206
	s_waitcnt lgkmcnt(2)
	v_pk_fma_f32 v[144:145], v[88:89], v[132:133], v[144:145] op_sel_hi:[0,1,1] neg_lo:[1,0,0] neg_hi:[1,0,0]
	v_pk_fma_f32 v[146:147], v[88:89], v[46:47], v[146:147] op_sel_hi:[0,1,1] neg_lo:[1,0,0] neg_hi:[1,0,0]
	v_fma_f32 v96, -v88, v140, v96
	v_pk_fma_f32 v[98:99], v[88:89], v[132:133], v[98:99] op_sel:[1,0,0] neg_lo:[1,0,0] neg_hi:[1,0,0]
	v_pk_fma_f32 v[100:101], v[88:89], v[46:47], v[100:101] op_sel:[1,0,0] neg_lo:[1,0,0] neg_hi:[1,0,0]
	v_fma_f32 v102, -v89, v140, v102
	v_pk_fma_f32 v[104:105], v[90:91], v[132:133], v[104:105] op_sel_hi:[0,1,1] neg_lo:[1,0,0] neg_hi:[1,0,0]
	v_pk_fma_f32 v[110:111], v[90:91], v[46:47], v[110:111] op_sel_hi:[0,1,1] neg_lo:[1,0,0] neg_hi:[1,0,0]
	v_fma_f32 v112, -v90, v140, v112
	v_pk_mul_f32 v[114:115], v[90:91], v[144:145] op_sel:[1,0]
	v_pk_mul_f32 v[222:223], v[90:91], v[146:147] op_sel:[1,0]
	v_mul_f32_e64 v228, v91, v96
	s_waitcnt lgkmcnt(1)
	v_pk_mul_f32 v[150:151], v[92:93], v[144:145] op_sel_hi:[0,1]
	v_pk_mul_f32 v[224:225], v[92:93], v[146:147] op_sel_hi:[0,1]
	v_mul_f32_e64 v230, v92, v96
	v_pk_mul_f32 v[220:221], v[92:93], v[144:145] op_sel:[1,0]
	v_pk_mul_f32 v[226:227], v[92:93], v[146:147] op_sel:[1,0]
	v_mul_f32_e64 v232, v93, v96
	v_pk_fma_f32 v[114:115], v[92:93], v[98:99], v[114:115] op_sel_hi:[0,1,1]
	v_pk_fma_f32 v[222:223], v[92:93], v[100:101], v[222:223] op_sel_hi:[0,1,1]
	v_fma_f32 v228, v92, v102, v228
	v_pk_fma_f32 v[150:151], v[94:95], v[98:99], v[150:151] op_sel_hi:[0,1,1]
	v_pk_fma_f32 v[224:225], v[94:95], v[100:101], v[224:225] op_sel_hi:[0,1,1]
	v_fma_f32 v230, v94, v102, v230
	v_pk_fma_f32 v[220:221], v[94:95], v[98:99], v[220:221] op_sel:[1,0,0]
	v_pk_fma_f32 v[226:227], v[94:95], v[100:101], v[226:227] op_sel:[1,0,0]
	v_fma_f32 v232, v95, v102, v232
	v_pk_fma_f32 v[114:115], v[92:93], v[104:105], v[114:115] op_sel:[1,0,0]
	v_pk_fma_f32 v[222:223], v[92:93], v[110:111], v[222:223] op_sel:[1,0,0]
	v_fma_f32 v228, v93, v112, v228
	v_pk_fma_f32 v[150:151], v[94:95], v[104:105], v[150:151] op_sel:[1,0,0]
	v_pk_fma_f32 v[224:225], v[94:95], v[110:111], v[224:225] op_sel:[1,0,0]
	v_fma_f32 v230, v95, v112, v230
	s_waitcnt lgkmcnt(0)
	v_pk_fma_f32 v[220:221], v[216:217], v[104:105], v[220:221] op_sel_hi:[0,1,1]
	v_pk_fma_f32 v[226:227], v[216:217], v[110:111], v[226:227] op_sel_hi:[0,1,1]
	v_fma_f32 v232, v216, v112, v232
	v_pk_mul_f32 v[234:235], v[88:89], v[114:115] op_sel_hi:[0,1]
	v_pk_mul_f32 v[236:237], v[88:89], v[222:223] op_sel_hi:[0,1]
	v_mul_f32_e64 v238, v88, v228
	v_pk_fma_f32 v[234:235], v[88:89], v[150:151], v[234:235] op_sel:[1,0,0]
	v_pk_fma_f32 v[236:237], v[88:89], v[224:225], v[236:237] op_sel:[1,0,0]
	v_fma_f32 v238, v89, v230, v238
	v_pk_fma_f32 v[234:235], v[90:91], v[220:221], v[234:235] op_sel_hi:[0,1,1]
	v_pk_fma_f32 v[236:237], v[90:91], v[226:227], v[236:237] op_sel_hi:[0,1,1]
	v_fma_f32 v238, v90, v232, v238
	v_pk_fma_f32 v[234:235], v[216:217], v[132:133], v[234:235] op_sel:[1,0,0] neg_lo:[0,0,1] neg_hi:[0,0,1]
	v_pk_fma_f32 v[236:237], v[216:217], v[46:47], v[236:237] op_sel:[1,0,0] neg_lo:[0,0,1] neg_hi:[0,0,1]
	v_fma_f32 v238, v217, v140, -v238
	v_cmp_eq_u32_e64 s[10:11], 1, v219
	v_cmp_eq_u32_e64 s[14:15], 2, v219
	v_cmp_eq_u32_e64 s[20:21], 3, v219
	v_cmp_eq_u32_e64 s[22:23], 4, v219
	v_cmp_eq_u32_e64 s[30:31], 5, v219
	v_pk_add_f32 v[46:47], v[52:53], v[114:115]
	v_pk_add_f32 v[52:53], v[130:131], v[222:223]
	v_add_f32_e64 v96, v152, v228
	v_pk_add_f32 v[98:99], v[156:157], v[150:151]
	v_pk_add_f32 v[100:101], v[148:149], v[224:225]
	v_add_f32_e64 v102, v162, v230
	v_pk_add_f32 v[104:105], v[166:167], v[220:221]
	v_pk_add_f32 v[110:111], v[170:171], v[226:227]
	v_add_f32_e64 v112, v196, v232
	v_pk_add_f32 v[130:131], v[200:201], v[234:235]
	v_pk_add_f32 v[132:133], v[204:205], v[236:237]
	v_add_f32_e64 v140, v208, v238
	v_pk_fma_f32 v[144:145], v[56:57], v[46:47], v[130:131] op_sel_hi:[0,1,1]
	v_pk_fma_f32 v[146:147], v[56:57], v[52:53], v[132:133] op_sel_hi:[0,1,1]
	v_fma_f32 v148, v56, v96, v140
	v_pk_fma_f32 v[152:153], v[72:73], v[46:47], v[130:131] op_sel_hi:[0,1,1]
	v_pk_fma_f32 v[156:157], v[72:73], v[52:53], v[132:133] op_sel_hi:[0,1,1]
	v_fma_f32 v162, v72, v96, v140
	v_pk_fma_f32 v[144:145], v[56:57], v[98:99], v[144:145] op_sel:[1,0,0]
	v_pk_fma_f32 v[146:147], v[56:57], v[100:101], v[146:147] op_sel:[1,0,0]
	v_fma_f32 v148, v57, v102, v148
	v_pk_fma_f32 v[152:153], v[72:73], v[98:99], v[152:153] op_sel:[1,0,0]
	v_pk_fma_f32 v[156:157], v[72:73], v[100:101], v[156:157] op_sel:[1,0,0]
	v_fma_f32 v162, v73, v102, v162
	v_pk_fma_f32 v[144:145], v[58:59], v[104:105], v[144:145] op_sel_hi:[0,1,1]
	v_pk_fma_f32 v[146:147], v[58:59], v[110:111], v[146:147] op_sel_hi:[0,1,1]
	v_fma_f32 v148, v58, v112, v148
	v_pk_fma_f32 v[152:153], v[74:75], v[104:105], v[152:153] op_sel_hi:[0,1,1]
	v_pk_fma_f32 v[156:157], v[74:75], v[110:111], v[156:157] op_sel_hi:[0,1,1]
	v_fma_f32 v162, v74, v112, v162
	v_pk_fma_f32 v[130:131], v[64:65], v[46:47], v[130:131] op_sel_hi:[0,1,1]
	v_pk_fma_f32 v[132:133], v[64:65], v[52:53], v[132:133] op_sel_hi:[0,1,1]
	v_fma_f32 v140, v64, v96, v140
	v_pk_fma_f32 v[130:131], v[64:65], v[98:99], v[130:131] op_sel:[1,0,0]
	v_pk_fma_f32 v[132:133], v[64:65], v[100:101], v[132:133] op_sel:[1,0,0]
	v_fma_f32 v140, v65, v102, v140
	v_pk_fma_f32 v[130:131], v[66:67], v[104:105], v[130:131] op_sel_hi:[0,1,1]
	v_pk_fma_f32 v[132:133], v[66:67], v[110:111], v[132:133] op_sel_hi:[0,1,1]
	v_fma_f32 v140, v66, v112, v140
	v_cndmask_b32_e64 v166, 0, v1, s[10:11]
	v_cndmask_b32_e64 v167, 0, v1, s[14:15]
	v_cndmask_b32_e64 v170, 0, v1, s[20:21]
	v_cndmask_b32_e64 v171, 0, v1, s[22:23]
	v_cndmask_b32_e64 v196, 0, v1, s[30:31]
	v_add_f32_dpp v130, v144, v130 wave_shl:1 row_mask:0xf bank_mask:0xf bound_ctrl:1
	v_add_f32_dpp v131, v145, v131 wave_shl:1 row_mask:0xf bank_mask:0xf bound_ctrl:1
	v_add_f32_dpp v132, v146, v132 wave_shl:1 row_mask:0xf bank_mask:0xf bound_ctrl:1
	v_add_f32_dpp v133, v147, v133 wave_shl:1 row_mask:0xf bank_mask:0xf bound_ctrl:1
	v_add_f32_dpp v140, v148, v140 wave_shl:1 row_mask:0xf bank_mask:0xf bound_ctrl:1
	s_add_i32 s4, s34, 7
	s_cmpk_lt_i32 s4, 0x201
	s_cselect_b64 s[12:13], s[0:1], 0
	v_add_f32_dpp v130, v152, v130 wave_shr:1 row_mask:0xf bank_mask:0xf bound_ctrl:1
	v_add_f32_dpp v131, v153, v131 wave_shr:1 row_mask:0xf bank_mask:0xf bound_ctrl:1
	v_add_f32_dpp v132, v156, v132 wave_shr:1 row_mask:0xf bank_mask:0xf bound_ctrl:1
	v_add_f32_dpp v133, v157, v133 wave_shr:1 row_mask:0xf bank_mask:0xf bound_ctrl:1
	v_add_f32_dpp v140, v162, v140 wave_shr:1 row_mask:0xf bank_mask:0xf bound_ctrl:1
	v_pk_fma_f32 v[130:131], v[54:55], v[218:219], v[130:131] op_sel_hi:[1,0,1] neg_lo:[0,0,1] neg_hi:[0,0,1]
	v_pk_fma_f32 v[132:133], v[60:61], v[218:219], v[132:133] op_sel_hi:[1,0,1] neg_lo:[0,0,1] neg_hi:[0,0,1]
	v_fma_f32 v140, v62, v218, -v140
	v_pk_add_f32 v[130:131], v[130:131], v[166:167] neg_lo:[0,1] neg_hi:[0,1]
	v_pk_add_f32 v[132:133], v[132:133], v[170:171] neg_lo:[0,1] neg_hi:[0,1]
	v_add_f32_e64 v140, v140, -v196
	v_pk_mul_f32 v[200:201], v[130:131], v[130:131]
	v_pk_fma_f32 v[200:201], v[132:133], v[132:133], v[200:201]
	v_add_f32_e32 v200, v200, v201
	v_fma_f32 v200, v140, v140, v200
	v_cndmask_b32_e64 v201, 0, v200, s[12:13]
	v_add_f32_e32 v0, v0, v201
	s_waitcnt vmcnt(6)
	v_mov_b32_dpp v52, v36 wave_shr:1 row_mask:0xf bank_mask:0xf bound_ctrl:1
	v_mov_b32_dpp v53, v37 wave_shr:1 row_mask:0xf bank_mask:0xf bound_ctrl:1
	v_mov_b32_dpp v54, v38 wave_shr:1 row_mask:0xf bank_mask:0xf bound_ctrl:1
	v_mov_b32_dpp v56, v36 wave_shl:1 row_mask:0xf bank_mask:0xf bound_ctrl:1
	v_mov_b32_dpp v57, v37 wave_shl:1 row_mask:0xf bank_mask:0xf bound_ctrl:1
	v_mov_b32_dpp v58, v38 wave_shl:1 row_mask:0xf bank_mask:0xf bound_ctrl:1
	v_mov_b32_dpp v46, v20 wave_shr:1 row_mask:0xf bank_mask:0xf bound_ctrl:1
	v_mov_b32_dpp v47, v21 wave_shr:1 row_mask:0xf bank_mask:0xf bound_ctrl:1
	v_mov_b32_dpp v60, v24 wave_shr:1 row_mask:0xf bank_mask:0xf bound_ctrl:1
	v_mov_b32_dpp v61, v25 wave_shr:1 row_mask:0xf bank_mask:0xf bound_ctrl:1
	v_mov_b32_dpp v62, v30 wave_shr:1 row_mask:0xf bank_mask:0xf bound_ctrl:1
	v_mov_b32_dpp v64, v20 wave_shl:1 row_mask:0xf bank_mask:0xf bound_ctrl:1
	v_mov_b32_dpp v65, v21 wave_shl:1 row_mask:0xf bank_mask:0xf bound_ctrl:1
	v_mov_b32_dpp v66, v24 wave_shl:1 row_mask:0xf bank_mask:0xf bound_ctrl:1
	v_mov_b32_dpp v67, v25 wave_shl:1 row_mask:0xf bank_mask:0xf bound_ctrl:1
	v_mov_b32_dpp v72, v30 wave_shl:1 row_mask:0xf bank_mask:0xf bound_ctrl:1
	v_pk_mul_f32 v[74:75], v[20:21], v[36:37] op_sel_hi:[1,0]
	v_pk_mul_f32 v[88:89], v[24:25], v[36:37] op_sel_hi:[1,0]
	v_mul_f32_e64 v90, v30, v36
	v_pk_mul_f32 v[92:93], v[20:21], v[36:37] op_sel:[0,1]
	v_pk_mul_f32 v[94:95], v[24:25], v[36:37] op_sel:[0,1]
	v_mul_f32_e64 v96, v30, v37
	v_pk_mul_f32 v[98:99], v[20:21], v[38:39] op_sel_hi:[1,0]
	v_pk_mul_f32 v[100:101], v[24:25], v[38:39] op_sel_hi:[1,0]
	v_mul_f32_e64 v102, v30, v38
	v_pk_add_f32 v[104:105], v[20:21], v[46:47]
	v_pk_add_f32 v[110:111], v[24:25], v[60:61]
	v_add_f32_e64 v112, v30, v62
	v_pk_fma_f32 v[74:75], v[46:47], v[52:53], v[74:75] op_sel_hi:[1,0,1]
	v_pk_fma_f32 v[88:89], v[60:61], v[52:53], v[88:89] op_sel_hi:[1,0,1]
	v_fma_f32 v90, v62, v52, v90
	v_pk_fma_f32 v[92:93], v[46:47], v[52:53], v[92:93] op_sel:[0,1,0]
	v_pk_fma_f32 v[94:95], v[60:61], v[52:53], v[94:95] op_sel:[0,1,0]
	v_fma_f32 v96, v62, v53, v96
	v_pk_fma_f32 v[98:99], v[46:47], v[54:55], v[98:99] op_sel_hi:[1,0,1]
	v_pk_fma_f32 v[100:101], v[60:61], v[54:55], v[100:101] op_sel_hi:[1,0,1]
	v_fma_f32 v102, v62, v54, v102
	v_pk_add_f32 v[104:105], v[104:105], v[64:65]
	v_pk_add_f32 v[110:111], v[110:111], v[66:67]
	v_add_f32_e64 v112, v112, v72
	v_pk_fma_f32 v[74:75], v[64:65], v[56:57], v[74:75] op_sel_hi:[1,0,1]
	v_pk_fma_f32 v[88:89], v[66:67], v[56:57], v[88:89] op_sel_hi:[1,0,1]
	v_fma_f32 v90, v72, v56, v90
	v_pk_fma_f32 v[92:93], v[64:65], v[56:57], v[92:93] op_sel:[0,1,0]
	v_pk_fma_f32 v[94:95], v[66:67], v[56:57], v[94:95] op_sel:[0,1,0]
	v_fma_f32 v96, v72, v57, v96
	v_pk_fma_f32 v[98:99], v[64:65], v[58:59], v[98:99] op_sel_hi:[1,0,1]
	v_pk_fma_f32 v[100:101], v[66:67], v[58:59], v[100:101] op_sel_hi:[1,0,1]
	v_fma_f32 v102, v72, v58, v102
	s_barrier
	ds_read_b128 v[60:63], v23 offset:0
	ds_read_b128 v[64:67], v23 offset:1024
	ds_read_b128 v[144:147], v23 offset:2048
	v_pk_add_f32 v[46:47], v[210:211], v[104:105]
	v_pk_add_f32 v[72:73], v[134:135], v[46:47]
	v_pk_add_f32 v[130:131], v[212:213], v[110:111]
	v_pk_add_f32 v[132:133], v[136:137], v[130:131]
	v_add_f32_e64 v134, v214, v112
	v_add_f32_e64 v136, v142, v134
	v_pk_add_f32 v[140:141], v[154:155], v[74:75]
	v_pk_add_f32 v[142:143], v[106:107], v[140:141]
	v_pk_add_f32 v[106:107], v[158:159], v[88:89]
	v_pk_add_f32 v[148:149], v[108:109], v[106:107]
	v_add_f32_e64 v108, v160, v90
	v_add_f32_e64 v152, v116, v108
	v_pk_add_f32 v[116:117], v[164:165], v[92:93]
	v_pk_add_f32 v[154:155], v[118:119], v[116:117]
	v_pk_add_f32 v[118:119], v[168:169], v[94:95]
	v_pk_add_f32 v[156:157], v[120:121], v[118:119]
	v_add_f32_e64 v120, v172, v96
	v_add_f32_e64 v158, v122, v120
	v_pk_add_f32 v[122:123], v[198:199], v[98:99]
	v_pk_add_f32 v[160:161], v[124:125], v[122:123]
	v_pk_add_f32 v[124:125], v[202:203], v[100:101]
	v_pk_add_f32 v[162:163], v[126:127], v[124:125]
	v_add_f32_e64 v126, v206, v102
	v_add_f32_e64 v164, v128, v126
	s_waitcnt lgkmcnt(2)
	v_pk_fma_f32 v[142:143], v[60:61], v[72:73], v[142:143] op_sel_hi:[0,1,1] neg_lo:[1,0,0] neg_hi:[1,0,0]
	v_pk_fma_f32 v[148:149], v[60:61], v[132:133], v[148:149] op_sel_hi:[0,1,1] neg_lo:[1,0,0] neg_hi:[1,0,0]
	v_fma_f32 v152, -v60, v136, v152
	v_pk_fma_f32 v[154:155], v[60:61], v[72:73], v[154:155] op_sel:[1,0,0] neg_lo:[1,0,0] neg_hi:[1,0,0]
	v_pk_fma_f32 v[156:157], v[60:61], v[132:133], v[156:157] op_sel:[1,0,0] neg_lo:[1,0,0] neg_hi:[1,0,0]
	v_fma_f32 v158, -v61, v136, v158
	v_pk_fma_f32 v[160:161], v[62:63], v[72:73], v[160:161] op_sel_hi:[0,1,1] neg_lo:[1,0,0] neg_hi:[1,0,0]
	v_pk_fma_f32 v[162:163], v[62:63], v[132:133], v[162:163] op_sel_hi:[0,1,1] neg_lo:[1,0,0] neg_hi:[1,0,0]
	v_fma_f32 v164, -v62, v136, v164
	v_pk_mul_f32 v[128:129], v[62:63], v[142:143] op_sel:[1,0]
	v_pk_mul_f32 v[170:171], v[62:63], v[148:149] op_sel:[1,0]
	v_mul_f32_e64 v198, v63, v152
	s_waitcnt lgkmcnt(1)
	v_pk_mul_f32 v[166:167], v[64:65], v[142:143] op_sel_hi:[0,1]
	v_pk_mul_f32 v[172:173], v[64:65], v[148:149] op_sel_hi:[0,1]
	v_mul_f32_e64 v200, v64, v152
	v_pk_mul_f32 v[168:169], v[64:65], v[142:143] op_sel:[1,0]
	v_pk_mul_f32 v[196:197], v[64:65], v[148:149] op_sel:[1,0]
	v_mul_f32_e64 v202, v65, v152
	v_pk_fma_f32 v[128:129], v[64:65], v[154:155], v[128:129] op_sel_hi:[0,1,1]
	v_pk_fma_f32 v[170:171], v[64:65], v[156:157], v[170:171] op_sel_hi:[0,1,1]
	v_fma_f32 v198, v64, v158, v198
	v_pk_fma_f32 v[166:167], v[66:67], v[154:155], v[166:167] op_sel_hi:[0,1,1]
	v_pk_fma_f32 v[172:173], v[66:67], v[156:157], v[172:173] op_sel_hi:[0,1,1]
	v_fma_f32 v200, v66, v158, v200
	v_pk_fma_f32 v[168:169], v[66:67], v[154:155], v[168:169] op_sel:[1,0,0]
	v_pk_fma_f32 v[196:197], v[66:67], v[156:157], v[196:197] op_sel:[1,0,0]
	v_fma_f32 v202, v67, v158, v202
	v_pk_fma_f32 v[128:129], v[64:65], v[160:161], v[128:129] op_sel:[1,0,0]
	v_pk_fma_f32 v[170:171], v[64:65], v[162:163], v[170:171] op_sel:[1,0,0]
	v_fma_f32 v198, v65, v164, v198
	v_pk_fma_f32 v[166:167], v[66:67], v[160:161], v[166:167] op_sel:[1,0,0]
	v_pk_fma_f32 v[172:173], v[66:67], v[162:163], v[172:173] op_sel:[1,0,0]
	v_fma_f32 v200, v67, v164, v200
	s_waitcnt lgkmcnt(0)
	v_pk_fma_f32 v[168:169], v[144:145], v[160:161], v[168:169] op_sel_hi:[0,1,1]
	v_pk_fma_f32 v[196:197], v[144:145], v[162:163], v[196:197] op_sel_hi:[0,1,1]
	v_fma_f32 v202, v144, v164, v202
	v_pk_mul_f32 v[204:205], v[60:61], v[128:129] op_sel_hi:[0,1]
	v_pk_mul_f32 v[206:207], v[60:61], v[170:171] op_sel_hi:[0,1]
	v_mul_f32_e64 v208, v60, v198
	v_pk_fma_f32 v[204:205], v[60:61], v[166:167], v[204:205] op_sel:[1,0,0]
	v_pk_fma_f32 v[206:207], v[60:61], v[172:173], v[206:207] op_sel:[1,0,0]
	v_fma_f32 v208, v61, v200, v208
	v_pk_fma_f32 v[204:205], v[62:63], v[168:169], v[204:205] op_sel_hi:[0,1,1]
	v_pk_fma_f32 v[206:207], v[62:63], v[196:197], v[206:207] op_sel_hi:[0,1,1]
	v_fma_f32 v208, v62, v202, v208
	v_pk_fma_f32 v[204:205], v[144:145], v[72:73], v[204:205] op_sel:[1,0,0] neg_lo:[0,0,1] neg_hi:[0,0,1]
	v_pk_fma_f32 v[206:207], v[144:145], v[132:133], v[206:207] op_sel:[1,0,0] neg_lo:[0,0,1] neg_hi:[0,0,1]
	v_fma_f32 v208, v145, v136, -v208
	v_cmp_eq_u32_e64 s[10:11], 1, v147
	v_cmp_eq_u32_e64 s[14:15], 2, v147
	v_cmp_eq_u32_e64 s[20:21], 3, v147
	v_cmp_eq_u32_e64 s[22:23], 4, v147
	v_cmp_eq_u32_e64 s[30:31], 5, v147
	v_pk_add_f32 v[72:73], v[114:115], v[128:129]
	v_pk_add_f32 v[132:133], v[138:139], v[72:73]
	v_pk_add_f32 v[114:115], v[222:223], v[170:171]
	v_pk_add_f32 v[136:137], v[178:179], v[114:115]
	v_add_f32_e64 v138, v228, v198
	v_add_f32_e64 v142, v184, v138
	v_pk_add_f32 v[148:149], v[150:151], v[166:167]
	v_pk_add_f32 v[152:153], v[174:175], v[148:149]
	v_pk_add_f32 v[150:151], v[224:225], v[172:173]
	v_pk_add_f32 v[154:155], v[180:181], v[150:151]
	v_add_f32_e64 v156, v230, v200
	v_add_f32_e64 v158, v186, v156
	v_pk_add_f32 v[160:161], v[220:221], v[168:169]
	v_pk_add_f32 v[162:163], v[176:177], v[160:161]
	v_pk_add_f32 v[164:165], v[226:227], v[196:197]
	v_pk_add_f32 v[174:175], v[182:183], v[164:165]
	v_add_f32_e64 v176, v232, v202
	v_add_f32_e64 v178, v188, v176
	v_pk_add_f32 v[180:181], v[234:235], v[204:205]
	v_pk_add_f32 v[182:183], v[190:191], v[180:181]
	v_pk_add_f32 v[184:185], v[236:237], v[206:207]
	v_pk_add_f32 v[186:187], v[192:193], v[184:185]
	v_add_f32_e64 v188, v238, v208
	v_add_f32_e64 v190, v194, v188
	v_pk_fma_f32 v[192:193], v[76:77], v[132:133], v[182:183] op_sel_hi:[0,1,1]
	v_pk_fma_f32 v[194:195], v[76:77], v[136:137], v[186:187] op_sel_hi:[0,1,1]
	v_fma_f32 v210, v76, v142, v190
	v_pk_fma_f32 v[212:213], v[84:85], v[132:133], v[182:183] op_sel_hi:[0,1,1]
	v_pk_fma_f32 v[214:215], v[84:85], v[136:137], v[186:187] op_sel_hi:[0,1,1]
	v_fma_f32 v216, v84, v142, v190
	v_pk_fma_f32 v[192:193], v[76:77], v[152:153], v[192:193] op_sel:[1,0,0]
	v_pk_fma_f32 v[194:195], v[76:77], v[154:155], v[194:195] op_sel:[1,0,0]
	v_fma_f32 v210, v77, v158, v210
	v_pk_fma_f32 v[212:213], v[84:85], v[152:153], v[212:213] op_sel:[1,0,0]
	v_pk_fma_f32 v[214:215], v[84:85], v[154:155], v[214:215] op_sel:[1,0,0]
	v_fma_f32 v216, v85, v158, v216
	v_pk_fma_f32 v[192:193], v[78:79], v[162:163], v[192:193] op_sel_hi:[0,1,1]
	v_pk_fma_f32 v[194:195], v[78:79], v[174:175], v[194:195] op_sel_hi:[0,1,1]
	v_fma_f32 v210, v78, v178, v210
	v_pk_fma_f32 v[212:213], v[86:87], v[162:163], v[212:213] op_sel_hi:[0,1,1]
	v_pk_fma_f32 v[214:215], v[86:87], v[174:175], v[214:215] op_sel_hi:[0,1,1]
	v_fma_f32 v216, v86, v178, v216
	v_pk_fma_f32 v[182:183], v[8:9], v[132:133], v[182:183] op_sel_hi:[0,1,1]
	v_pk_fma_f32 v[186:187], v[8:9], v[136:137], v[186:187] op_sel_hi:[0,1,1]
	v_fma_f32 v190, v8, v142, v190
	v_pk_fma_f32 v[182:183], v[8:9], v[152:153], v[182:183] op_sel:[1,0,0]
	v_pk_fma_f32 v[186:187], v[8:9], v[154:155], v[186:187] op_sel:[1,0,0]
	v_fma_f32 v190, v9, v158, v190
	v_pk_fma_f32 v[182:183], v[10:11], v[162:163], v[182:183] op_sel_hi:[0,1,1]
	v_pk_fma_f32 v[186:187], v[10:11], v[174:175], v[186:187] op_sel_hi:[0,1,1]
	v_fma_f32 v190, v10, v178, v190
	v_cndmask_b32_e64 v218, 0, v1, s[10:11]
	v_cndmask_b32_e64 v219, 0, v1, s[14:15]
	v_cndmask_b32_e64 v220, 0, v1, s[20:21]
	v_cndmask_b32_e64 v221, 0, v1, s[22:23]
	v_cndmask_b32_e64 v222, 0, v1, s[30:31]
	v_add_f32_dpp v182, v192, v182 wave_shl:1 row_mask:0xf bank_mask:0xf bound_ctrl:1
	v_add_f32_dpp v183, v193, v183 wave_shl:1 row_mask:0xf bank_mask:0xf bound_ctrl:1
	v_add_f32_dpp v186, v194, v186 wave_shl:1 row_mask:0xf bank_mask:0xf bound_ctrl:1
	v_add_f32_dpp v187, v195, v187 wave_shl:1 row_mask:0xf bank_mask:0xf bound_ctrl:1
	v_add_f32_dpp v190, v210, v190 wave_shl:1 row_mask:0xf bank_mask:0xf bound_ctrl:1
	s_add_i32 s4, s34, 8
	s_cmpk_lt_i32 s4, 0x201
	s_cselect_b64 s[12:13], s[0:1], 0
	v_add_f32_dpp v182, v212, v182 wave_shr:1 row_mask:0xf bank_mask:0xf bound_ctrl:1
	v_add_f32_dpp v183, v213, v183 wave_shr:1 row_mask:0xf bank_mask:0xf bound_ctrl:1
	v_add_f32_dpp v186, v214, v186 wave_shr:1 row_mask:0xf bank_mask:0xf bound_ctrl:1
	v_add_f32_dpp v187, v215, v187 wave_shr:1 row_mask:0xf bank_mask:0xf bound_ctrl:1
	v_add_f32_dpp v190, v216, v190 wave_shr:1 row_mask:0xf bank_mask:0xf bound_ctrl:1
	v_pk_fma_f32 v[182:183], v[2:3], v[146:147], v[182:183] op_sel_hi:[1,0,1] neg_lo:[0,0,1] neg_hi:[0,0,1]
	v_pk_fma_f32 v[186:187], v[4:5], v[146:147], v[186:187] op_sel_hi:[1,0,1] neg_lo:[0,0,1] neg_hi:[0,0,1]
	v_fma_f32 v190, v6, v146, -v190
	v_pk_add_f32 v[182:183], v[182:183], v[218:219] neg_lo:[0,1] neg_hi:[0,1]
	v_pk_add_f32 v[186:187], v[186:187], v[220:221] neg_lo:[0,1] neg_hi:[0,1]
	v_add_f32_e64 v190, v190, -v222
	v_pk_mul_f32 v[224:225], v[182:183], v[182:183]
	v_pk_fma_f32 v[224:225], v[186:187], v[186:187], v[224:225]
	v_add_f32_e32 v224, v224, v225
	v_fma_f32 v224, v190, v190, v224
	v_cndmask_b32_e64 v225, 0, v224, s[12:13]
	v_add_f32_e32 v0, v0, v225
	s_waitcnt vmcnt(0)
	v_mov_b32_dpp v4, v48 wave_shr:1 row_mask:0xf bank_mask:0xf bound_ctrl:1
	v_mov_b32_dpp v5, v49 wave_shr:1 row_mask:0xf bank_mask:0xf bound_ctrl:1
	v_mov_b32_dpp v6, v50 wave_shr:1 row_mask:0xf bank_mask:0xf bound_ctrl:1
	v_mov_b32_dpp v8, v48 wave_shl:1 row_mask:0xf bank_mask:0xf bound_ctrl:1
	v_mov_b32_dpp v9, v49 wave_shl:1 row_mask:0xf bank_mask:0xf bound_ctrl:1
	v_mov_b32_dpp v10, v50 wave_shl:1 row_mask:0xf bank_mask:0xf bound_ctrl:1
	v_mov_b32_dpp v2, v40 wave_shr:1 row_mask:0xf bank_mask:0xf bound_ctrl:1
	v_mov_b32_dpp v3, v41 wave_shr:1 row_mask:0xf bank_mask:0xf bound_ctrl:1
	v_mov_b32_dpp v60, v42 wave_shr:1 row_mask:0xf bank_mask:0xf bound_ctrl:1
	v_mov_b32_dpp v61, v43 wave_shr:1 row_mask:0xf bank_mask:0xf bound_ctrl:1
	v_mov_b32_dpp v62, v44 wave_shr:1 row_mask:0xf bank_mask:0xf bound_ctrl:1
	v_mov_b32_dpp v64, v40 wave_shl:1 row_mask:0xf bank_mask:0xf bound_ctrl:1
	v_mov_b32_dpp v65, v41 wave_shl:1 row_mask:0xf bank_mask:0xf bound_ctrl:1
	v_mov_b32_dpp v66, v42 wave_shl:1 row_mask:0xf bank_mask:0xf bound_ctrl:1
	v_mov_b32_dpp v67, v43 wave_shl:1 row_mask:0xf bank_mask:0xf bound_ctrl:1
	v_mov_b32_dpp v76, v44 wave_shl:1 row_mask:0xf bank_mask:0xf bound_ctrl:1
	v_pk_mul_f32 v[78:79], v[40:41], v[48:49] op_sel_hi:[1,0]
	v_pk_mul_f32 v[84:85], v[42:43], v[48:49] op_sel_hi:[1,0]
	v_mul_f32_e64 v86, v44, v48
	v_pk_mul_f32 v[132:133], v[40:41], v[48:49] op_sel:[0,1]
	v_pk_mul_f32 v[136:137], v[42:43], v[48:49] op_sel:[0,1]
	v_mul_f32_e64 v142, v44, v49
	v_pk_mul_f32 v[144:145], v[40:41], v[50:51] op_sel_hi:[1,0]
	v_pk_mul_f32 v[146:147], v[42:43], v[50:51] op_sel_hi:[1,0]
	v_mul_f32_e64 v152, v44, v50
	v_pk_add_f32 v[154:155], v[40:41], v[2:3]
	v_pk_add_f32 v[158:159], v[42:43], v[60:61]
	v_add_f32_e64 v162, v44, v62
	v_pk_fma_f32 v[78:79], v[2:3], v[4:5], v[78:79] op_sel_hi:[1,0,1]
	v_pk_fma_f32 v[84:85], v[60:61], v[4:5], v[84:85] op_sel_hi:[1,0,1]
	v_fma_f32 v86, v62, v4, v86
	v_pk_fma_f32 v[132:133], v[2:3], v[4:5], v[132:133] op_sel:[0,1,0]
	v_pk_fma_f32 v[136:137], v[60:61], v[4:5], v[136:137] op_sel:[0,1,0]
	v_fma_f32 v142, v62, v5, v142
	v_pk_fma_f32 v[144:145], v[2:3], v[6:7], v[144:145] op_sel_hi:[1,0,1]
	v_pk_fma_f32 v[146:147], v[60:61], v[6:7], v[146:147] op_sel_hi:[1,0,1]
	v_fma_f32 v152, v62, v6, v152
	v_pk_add_f32 v[154:155], v[154:155], v[64:65]
	v_pk_add_f32 v[158:159], v[158:159], v[66:67]
	v_add_f32_e64 v162, v162, v76
	v_pk_fma_f32 v[78:79], v[64:65], v[8:9], v[78:79] op_sel_hi:[1,0,1]
	v_pk_fma_f32 v[84:85], v[66:67], v[8:9], v[84:85] op_sel_hi:[1,0,1]
	v_fma_f32 v86, v76, v8, v86
	v_pk_fma_f32 v[132:133], v[64:65], v[8:9], v[132:133] op_sel:[0,1,0]
	v_pk_fma_f32 v[136:137], v[66:67], v[8:9], v[136:137] op_sel:[0,1,0]
	v_fma_f32 v142, v76, v9, v142
	v_pk_fma_f32 v[144:145], v[64:65], v[10:11], v[144:145] op_sel_hi:[1,0,1]
	v_pk_fma_f32 v[146:147], v[66:67], v[10:11], v[146:147] op_sel_hi:[1,0,1]
	v_fma_f32 v152, v76, v10, v152
	s_barrier
	ds_read_b128 v[60:63], v23 offset:3072
	ds_read_b128 v[64:67], v23 offset:4096
	ds_read_b128 v[192:195], v23 offset:5120
	v_pk_add_f32 v[2:3], v[46:47], v[154:155]
	v_pk_add_f32 v[46:47], v[130:131], v[158:159]
	v_add_f32_e64 v76, v134, v162
	v_pk_add_f32 v[130:131], v[140:141], v[78:79]
	v_pk_add_f32 v[134:135], v[106:107], v[84:85]
	v_add_f32_e64 v106, v108, v86
	v_pk_add_f32 v[108:109], v[116:117], v[132:133]
	v_pk_add_f32 v[116:117], v[118:119], v[136:137]
	v_add_f32_e64 v118, v120, v142
	v_pk_add_f32 v[120:121], v[122:123], v[144:145]
	v_pk_add_f32 v[122:123], v[124:125], v[146:147]
	v_add_f32_e64 v124, v126, v152
	s_waitcnt lgkmcnt(2)
	v_pk_fma_f32 v[130:131], v[60:61], v[2:3], v[130:131] op_sel_hi:[0,1,1] neg_lo:[1,0,0] neg_hi:[1,0,0]
	v_pk_fma_f32 v[134:135], v[60:61], v[46:47], v[134:135] op_sel_hi:[0,1,1] neg_lo:[1,0,0] neg_hi:[1,0,0]
	v_fma_f32 v106, -v60, v76, v106
	v_pk_fma_f32 v[108:109], v[60:61], v[2:3], v[108:109] op_sel:[1,0,0] neg_lo:[1,0,0] neg_hi:[1,0,0]
	v_pk_fma_f32 v[116:117], v[60:61], v[46:47], v[116:117] op_sel:[1,0,0] neg_lo:[1,0,0] neg_hi:[1,0,0]
	v_fma_f32 v118, -v61, v76, v118
	v_pk_fma_f32 v[120:121], v[62:63], v[2:3], v[120:121] op_sel_hi:[0,1,1] neg_lo:[1,0,0] neg_hi:[1,0,0]
	v_pk_fma_f32 v[122:123], v[62:63], v[46:47], v[122:123] op_sel_hi:[0,1,1] neg_lo:[1,0,0] neg_hi:[1,0,0]
	v_fma_f32 v124, -v62, v76, v124
	v_pk_mul_f32 v[126:127], v[62:63], v[130:131] op_sel:[1,0]
	v_pk_mul_f32 v[178:179], v[62:63], v[134:135] op_sel:[1,0]
	v_mul_f32_e64 v190, v63, v106
	s_waitcnt lgkmcnt(1)
	v_pk_mul_f32 v[140:141], v[64:65], v[130:131] op_sel_hi:[0,1]
	v_pk_mul_f32 v[182:183], v[64:65], v[134:135] op_sel_hi:[0,1]
	v_mul_f32_e64 v210, v64, v106
	v_pk_mul_f32 v[174:175], v[64:65], v[130:131] op_sel:[1,0]
	v_pk_mul_f32 v[186:187], v[64:65], v[134:135] op_sel:[1,0]
	v_mul_f32_e64 v212, v65, v106
	v_pk_fma_f32 v[126:127], v[64:65], v[108:109], v[126:127] op_sel_hi:[0,1,1]
	v_pk_fma_f32 v[178:179], v[64:65], v[116:117], v[178:179] op_sel_hi:[0,1,1]
	v_fma_f32 v190, v64, v118, v190
	v_pk_fma_f32 v[140:141], v[66:67], v[108:109], v[140:141] op_sel_hi:[0,1,1]
	v_pk_fma_f32 v[182:183], v[66:67], v[116:117], v[182:183] op_sel_hi:[0,1,1]
	v_fma_f32 v210, v66, v118, v210
	v_pk_fma_f32 v[174:175], v[66:67], v[108:109], v[174:175] op_sel:[1,0,0]
	v_pk_fma_f32 v[186:187], v[66:67], v[116:117], v[186:187] op_sel:[1,0,0]
	v_fma_f32 v212, v67, v118, v212
	v_pk_fma_f32 v[126:127], v[64:65], v[120:121], v[126:127] op_sel:[1,0,0]
	v_pk_fma_f32 v[178:179], v[64:65], v[122:123], v[178:179] op_sel:[1,0,0]
	v_fma_f32 v190, v65, v124, v190
	v_pk_fma_f32 v[140:141], v[66:67], v[120:121], v[140:141] op_sel:[1,0,0]
	v_pk_fma_f32 v[182:183], v[66:67], v[122:123], v[182:183] op_sel:[1,0,0]
	v_fma_f32 v210, v67, v124, v210
	s_waitcnt lgkmcnt(0)
	v_pk_fma_f32 v[174:175], v[192:193], v[120:121], v[174:175] op_sel_hi:[0,1,1]
	v_pk_fma_f32 v[186:187], v[192:193], v[122:123], v[186:187] op_sel_hi:[0,1,1]
	v_fma_f32 v212, v192, v124, v212
	v_pk_mul_f32 v[214:215], v[60:61], v[126:127] op_sel_hi:[0,1]
	v_pk_mul_f32 v[216:217], v[60:61], v[178:179] op_sel_hi:[0,1]
	v_mul_f32_e64 v218, v60, v190
	v_pk_fma_f32 v[214:215], v[60:61], v[140:141], v[214:215] op_sel:[1,0,0]
	v_pk_fma_f32 v[216:217], v[60:61], v[182:183], v[216:217] op_sel:[1,0,0]
	v_fma_f32 v218, v61, v210, v218
	v_pk_fma_f32 v[214:215], v[62:63], v[174:175], v[214:215] op_sel_hi:[0,1,1]
	v_pk_fma_f32 v[216:217], v[62:63], v[186:187], v[216:217] op_sel_hi:[0,1,1]
	v_fma_f32 v218, v62, v212, v218
	v_pk_fma_f32 v[214:215], v[192:193], v[2:3], v[214:215] op_sel:[1,0,0] neg_lo:[0,0,1] neg_hi:[0,0,1]
	v_pk_fma_f32 v[216:217], v[192:193], v[46:47], v[216:217] op_sel:[1,0,0] neg_lo:[0,0,1] neg_hi:[0,0,1]
	v_fma_f32 v218, v193, v76, -v218
	v_cmp_eq_u32_e64 s[10:11], 1, v195
	v_cmp_eq_u32_e64 s[14:15], 2, v195
	v_cmp_eq_u32_e64 s[20:21], 3, v195
	v_cmp_eq_u32_e64 s[22:23], 4, v195
	v_cmp_eq_u32_e64 s[30:31], 5, v195
	v_pk_add_f32 v[2:3], v[72:73], v[126:127]
	v_pk_add_f32 v[46:47], v[114:115], v[178:179]
	v_add_f32_e64 v72, v138, v190
	v_pk_add_f32 v[76:77], v[148:149], v[140:141]
	v_pk_add_f32 v[106:107], v[150:151], v[182:183]
	v_add_f32_e64 v108, v156, v210
	v_pk_add_f32 v[114:115], v[160:161], v[174:175]
	v_pk_add_f32 v[116:117], v[164:165], v[186:187]
	v_add_f32_e64 v118, v176, v212
	v_pk_add_f32 v[120:121], v[180:181], v[214:215]
	v_pk_add_f32 v[122:123], v[184:185], v[216:217]
	v_add_f32_e64 v124, v188, v218
	v_pk_fma_f32 v[130:131], v[68:69], v[2:3], v[120:121] op_sel_hi:[0,1,1]
	v_pk_fma_f32 v[134:135], v[68:69], v[46:47], v[122:123] op_sel_hi:[0,1,1]
	v_fma_f32 v138, v68, v72, v124
	v_pk_fma_f32 v[148:149], v[80:81], v[2:3], v[120:121] op_sel_hi:[0,1,1]
	v_pk_fma_f32 v[150:151], v[80:81], v[46:47], v[122:123] op_sel_hi:[0,1,1]
	v_fma_f32 v156, v80, v72, v124
	v_pk_fma_f32 v[130:131], v[68:69], v[76:77], v[130:131] op_sel:[1,0,0]
	v_pk_fma_f32 v[134:135], v[68:69], v[106:107], v[134:135] op_sel:[1,0,0]
	v_fma_f32 v138, v69, v108, v138
	v_pk_fma_f32 v[148:149], v[80:81], v[76:77], v[148:149] op_sel:[1,0,0]
	v_pk_fma_f32 v[150:151], v[80:81], v[106:107], v[150:151] op_sel:[1,0,0]
	v_fma_f32 v156, v81, v108, v156
	v_pk_fma_f32 v[130:131], v[70:71], v[114:115], v[130:131] op_sel_hi:[0,1,1]
	v_pk_fma_f32 v[134:135], v[70:71], v[116:117], v[134:135] op_sel_hi:[0,1,1]
	v_fma_f32 v138, v70, v118, v138
	v_pk_fma_f32 v[148:149], v[82:83], v[114:115], v[148:149] op_sel_hi:[0,1,1]
	v_pk_fma_f32 v[150:151], v[82:83], v[116:117], v[150:151] op_sel_hi:[0,1,1]
	v_fma_f32 v156, v82, v118, v156
	v_pk_fma_f32 v[120:121], v[32:33], v[2:3], v[120:121] op_sel_hi:[0,1,1]
	v_pk_fma_f32 v[122:123], v[32:33], v[46:47], v[122:123] op_sel_hi:[0,1,1]
	v_fma_f32 v124, v32, v72, v124
	v_pk_fma_f32 v[120:121], v[32:33], v[76:77], v[120:121] op_sel:[1,0,0]
	v_pk_fma_f32 v[122:123], v[32:33], v[106:107], v[122:123] op_sel:[1,0,0]
	v_fma_f32 v124, v33, v108, v124
	v_pk_fma_f32 v[120:121], v[34:35], v[114:115], v[120:121] op_sel_hi:[0,1,1]
	v_pk_fma_f32 v[122:123], v[34:35], v[116:117], v[122:123] op_sel_hi:[0,1,1]
	v_fma_f32 v124, v34, v118, v124
	v_cndmask_b32_e64 v160, 0, v1, s[10:11]
	v_cndmask_b32_e64 v161, 0, v1, s[14:15]
	v_cndmask_b32_e64 v164, 0, v1, s[20:21]
	v_cndmask_b32_e64 v165, 0, v1, s[22:23]
	v_cndmask_b32_e64 v176, 0, v1, s[30:31]
	v_add_f32_dpp v120, v130, v120 wave_shl:1 row_mask:0xf bank_mask:0xf bound_ctrl:1
	v_add_f32_dpp v121, v131, v121 wave_shl:1 row_mask:0xf bank_mask:0xf bound_ctrl:1
	v_add_f32_dpp v122, v134, v122 wave_shl:1 row_mask:0xf bank_mask:0xf bound_ctrl:1
	v_add_f32_dpp v123, v135, v123 wave_shl:1 row_mask:0xf bank_mask:0xf bound_ctrl:1
	v_add_f32_dpp v124, v138, v124 wave_shl:1 row_mask:0xf bank_mask:0xf bound_ctrl:1
	s_add_i32 s4, s34, 9
	s_cmpk_lt_i32 s4, 0x201
	s_cselect_b64 s[12:13], s[0:1], 0
	v_add_f32_dpp v120, v148, v120 wave_shr:1 row_mask:0xf bank_mask:0xf bound_ctrl:1
	v_add_f32_dpp v121, v149, v121 wave_shr:1 row_mask:0xf bank_mask:0xf bound_ctrl:1
	v_add_f32_dpp v122, v150, v122 wave_shr:1 row_mask:0xf bank_mask:0xf bound_ctrl:1
	v_add_f32_dpp v123, v151, v123 wave_shr:1 row_mask:0xf bank_mask:0xf bound_ctrl:1
	v_add_f32_dpp v124, v156, v124 wave_shr:1 row_mask:0xf bank_mask:0xf bound_ctrl:1
	v_pk_fma_f32 v[120:121], v[12:13], v[194:195], v[120:121] op_sel_hi:[1,0,1] neg_lo:[0,0,1] neg_hi:[0,0,1]
	v_pk_fma_f32 v[122:123], v[14:15], v[194:195], v[122:123] op_sel_hi:[1,0,1] neg_lo:[0,0,1] neg_hi:[0,0,1]
	v_fma_f32 v124, v16, v194, -v124
	v_pk_add_f32 v[120:121], v[120:121], v[160:161] neg_lo:[0,1] neg_hi:[0,1]
	v_pk_add_f32 v[122:123], v[122:123], v[164:165] neg_lo:[0,1] neg_hi:[0,1]
	v_add_f32_e64 v124, v124, -v176
	v_pk_mul_f32 v[180:181], v[120:121], v[120:121]
	v_pk_fma_f32 v[180:181], v[122:123], v[122:123], v[180:181]
	v_add_f32_e32 v180, v180, v181
	v_fma_f32 v180, v124, v124, v180
	v_cndmask_b32_e64 v181, 0, v180, s[12:13]
	v_add_f32_e32 v0, v0, v181
